# v23 + agent-scope write-through (sc1) on every store of the G_in and KVQ/Q epilogues (phases that end in a grid barrier) so the leader's L2 writeback finds clean lines
# baseline (speedup 1.0000x reference)
.LBB0_174:
	v_mbcnt_lo_u32_b32 v250, -1, 0
	v_mbcnt_hi_u32_b32 v250, -1, v250
	v_lshrrev_b32_e32 v251, 2, v250
	v_and_b32_e32 v250, 3, v250
	v_lshl_add_u32 v250, v250, 4, v251
	v_lshlrev_b32_e32 v250, 2, v250
	s_ashr_i32 s15, s60, 3
	s_add_i32 s62, s15, s75
	s_lshl_b32 s15, s60, 8
	s_and_b32 s15, s15, 0x700
	s_cmp_eq_u32 s62, 0
	v_lshl_add_u32 v174, s28, 8, v1
	s_cselect_b64 s[26:27], -1, 0
	v_or_b32_e32 v82, s15, v209
	s_and_b64 s[26:27], s[50:51], s[26:27]
	v_or_b32_e32 v180, 16, v174
	v_or_b32_e32 v178, 32, v174
	v_or_b32_e32 v176, 48, v174
	s_mov_b64 s[64:65], -1
	s_and_b64 vcc, exec, s[26:27]
	v_lshlrev_b32_e32 v114, 1, v82
	v_ashrrev_i32_e32 v175, 31, v174
	v_ashrrev_i32_e32 v181, 31, v180
	v_ashrrev_i32_e32 v179, 31, v178
	v_ashrrev_i32_e32 v177, 31, v176
	s_cbranch_vccnz .LBB0_177
	v_lshl_add_u32 v158, s14, 10, v210
	ds_read2_b32 v[88:89], v158 offset1:16
	s_ashr_i32 s63, s62, 31
	s_lshl_b64 s[26:27], s[62:63], 25
	s_add_u32 s26, s84, s26
	s_addc_u32 s27, s85, s27
	v_lshl_add_u64 v[90:91], s[26:27], 0, v[114:115]
	v_lshlrev_b64 v[82:83], 12, v[174:175]
	s_waitcnt lgkmcnt(0)
	v_pk_mul_f32 v[84:85], v[144:145], v[88:89] op_sel_hi:[1,0]
	v_lshl_add_u64 v[82:83], v[90:91], 0, v[82:83]
	v_pk_mul_f32 v[86:87], v[146:147], v[88:89] op_sel_hi:[1,0]
	v_cvt_pk_bf16_f32 v84, v84, v85
	v_pk_mul_f32 v[92:93], v[142:143], v[88:89] op_sel_hi:[1,0]
	v_cvt_pk_bf16_f32 v85, v86, v87
	v_pk_mul_f32 v[94:95], v[140:141], v[88:89] op_sel_hi:[1,0]
	v_cvt_pk_bf16_f32 v87, v92, v93
	v_pk_mul_f32 v[92:93], v[134:135], v[88:89] op_sel_hi:[1,0]
	v_cvt_pk_bf16_f32 v86, v94, v95
	ds_bpermute_b32 v232, v250, v84
	ds_bpermute_b32 v233, v250, v85
	ds_bpermute_b32 v234, v250, v86
	ds_bpermute_b32 v235, v250, v87
	ds_bpermute_b32 v236, v250, v82
	v_pk_mul_f32 v[94:95], v[132:133], v[88:89] op_sel_hi:[1,0]
	s_mov_b32 s15, 0x80000
	v_pk_mul_f32 v[84:85], v[136:137], v[88:89] op_sel_hi:[1,0]
	v_pk_mul_f32 v[86:87], v[138:139], v[88:89] op_sel_hi:[1,0]
	v_cvt_pk_bf16_f32 v84, v84, v85
	v_mov_b32_e32 v88, v89
	v_cvt_pk_bf16_f32 v85, v86, v87
	v_cvt_pk_bf16_f32 v86, v94, v95
	v_cvt_pk_bf16_f32 v87, v92, v93
	ds_bpermute_b32 v238, v250, v84
	ds_bpermute_b32 v239, v250, v85
	ds_bpermute_b32 v240, v250, v86
	ds_bpermute_b32 v241, v250, v87
	ds_bpermute_b32 v242, v250, v82
	v_pk_mul_f32 v[94:95], v[126:127], v[88:89] op_sel_hi:[1,0]
	v_pk_mul_f32 v[96:97], v[124:125], v[88:89] op_sel_hi:[1,0]
	v_lshlrev_b64 v[84:85], 12, v[180:181]
	v_lshl_add_u64 v[92:93], v[90:91], 0, v[84:85]
	v_pk_mul_f32 v[86:87], v[130:131], v[88:89] op_sel_hi:[1,0]
	v_pk_mul_f32 v[84:85], v[128:129], v[88:89] op_sel_hi:[1,0]
	s_mov_b64 s[16:17], 0x80000
	v_cvt_pk_bf16_f32 v84, v84, v85
	v_cvt_pk_bf16_f32 v85, v86, v87
	v_cvt_pk_bf16_f32 v86, v96, v97
	v_cvt_pk_bf16_f32 v87, v94, v95
	s_waitcnt lgkmcnt(5)
	v_subrev_u32_e32 v236, s82, v236
	global_store_dwordx4 v236, v[232:235], s[82:83] sc1
	ds_bpermute_b32 v244, v250, v84
	ds_bpermute_b32 v245, v250, v85
	ds_bpermute_b32 v246, v250, v86
	ds_bpermute_b32 v247, v250, v87
	ds_bpermute_b32 v248, v250, v92
	v_pk_mul_f32 v[94:95], v[118:119], v[88:89] op_sel_hi:[1,0]
	s_nop 0
	v_pk_mul_f32 v[86:87], v[122:123], v[88:89] op_sel_hi:[1,0]
	v_pk_mul_f32 v[84:85], v[120:121], v[88:89] op_sel_hi:[1,0]
	v_pk_mul_f32 v[88:89], v[116:117], v[88:89] op_sel_hi:[1,0]
	v_cvt_pk_bf16_f32 v84, v84, v85
	v_cvt_pk_bf16_f32 v85, v86, v87
	v_cvt_pk_bf16_f32 v87, v94, v95
	s_nop 0
	v_cvt_pk_bf16_f32 v86, v88, v89
	ds_read2_b32 v[88:89], v158 offset0:32 offset1:48
	s_waitcnt lgkmcnt(6)
	v_subrev_u32_e32 v242, s82, v242
	global_store_dwordx4 v242, v[238:241], s[82:83] offset:64 sc1
	ds_bpermute_b32 v232, v250, v84
	ds_bpermute_b32 v233, v250, v85
	ds_bpermute_b32 v234, v250, v86
	ds_bpermute_b32 v235, v250, v87
	ds_bpermute_b32 v236, v250, v92
	s_waitcnt lgkmcnt(0)
	v_pk_mul_f32 v[94:95], v[108:109], v[88:89] op_sel_hi:[1,0]
	v_lshlrev_b64 v[84:85], 12, v[178:179]
	v_lshl_add_u64 v[92:93], v[90:91], 0, v[84:85]
	v_pk_mul_f32 v[84:85], v[110:111], v[88:89] op_sel_hi:[1,0]
	v_pk_mul_f32 v[86:87], v[112:113], v[88:89] op_sel_hi:[1,0]
	v_cvt_pk_bf16_f32 v84, v84, v85
	v_pk_mul_f32 v[96:97], v[106:107], v[88:89] op_sel_hi:[1,0]
	v_cvt_pk_bf16_f32 v85, v86, v87
	v_cvt_pk_bf16_f32 v87, v94, v95
	v_pk_mul_f32 v[94:95], v[100:101], v[88:89] op_sel_hi:[1,0]
	v_cvt_pk_bf16_f32 v86, v96, v97
	s_waitcnt lgkmcnt(6)
	v_subrev_u32_e32 v248, s82, v248
	global_store_dwordx4 v248, v[244:247], s[82:83] sc1
	ds_bpermute_b32 v238, v250, v84
	ds_bpermute_b32 v239, v250, v85
	ds_bpermute_b32 v240, v250, v86
	ds_bpermute_b32 v241, v250, v87
	ds_bpermute_b32 v242, v250, v92
	v_pk_mul_f32 v[96:97], v[98:99], v[88:89] op_sel_hi:[1,0]
	s_nop 0
	v_pk_mul_f32 v[84:85], v[102:103], v[88:89] op_sel_hi:[1,0]
	v_pk_mul_f32 v[86:87], v[104:105], v[88:89] op_sel_hi:[1,0]
	v_cvt_pk_bf16_f32 v84, v84, v85
	v_mov_b32_e32 v88, v89
	v_cvt_pk_bf16_f32 v85, v86, v87
	v_cvt_pk_bf16_f32 v86, v96, v97
	v_cvt_pk_bf16_f32 v87, v94, v95
	s_waitcnt lgkmcnt(5)
	v_subrev_u32_e32 v236, s82, v236
	global_store_dwordx4 v236, v[232:235], s[82:83] offset:64 sc1
	ds_bpermute_b32 v244, v250, v84
	ds_bpermute_b32 v245, v250, v85
	ds_bpermute_b32 v246, v250, v86
	ds_bpermute_b32 v247, v250, v87
	ds_bpermute_b32 v248, v250, v92
	v_pk_mul_f32 v[94:95], v[74:75], v[88:89] op_sel_hi:[1,0]
	v_pk_mul_f32 v[92:93], v[76:77], v[88:89] op_sel_hi:[1,0]
	v_lshlrev_b64 v[84:85], 12, v[176:177]
	v_lshl_add_u64 v[90:91], v[90:91], 0, v[84:85]
	v_pk_mul_f32 v[86:87], v[80:81], v[88:89] op_sel_hi:[1,0]
	v_pk_mul_f32 v[84:85], v[78:79], v[88:89] op_sel_hi:[1,0]
	s_nop 0
	v_cvt_pk_bf16_f32 v84, v84, v85
	v_cvt_pk_bf16_f32 v85, v86, v87
	v_cvt_pk_bf16_f32 v86, v94, v95
	ds_read2_b32 v[94:95], v158 offset0:128 offset1:144
	v_cvt_pk_bf16_f32 v87, v92, v93
	s_waitcnt lgkmcnt(6)
	v_subrev_u32_e32 v242, s82, v242
	global_store_dwordx4 v242, v[238:241], s[82:83] sc1
	ds_bpermute_b32 v232, v250, v84
	ds_bpermute_b32 v233, v250, v85
	ds_bpermute_b32 v234, v250, v86
	ds_bpermute_b32 v235, v250, v87
	ds_bpermute_b32 v236, v250, v90
	v_pk_mul_f32 v[92:93], v[68:69], v[88:89] op_sel_hi:[1,0]
	s_nop 0
	v_pk_mul_f32 v[86:87], v[72:73], v[88:89] op_sel_hi:[1,0]
	v_pk_mul_f32 v[84:85], v[70:71], v[88:89] op_sel_hi:[1,0]
	v_pk_mul_f32 v[88:89], v[66:67], v[88:89] op_sel_hi:[1,0]
	v_cvt_pk_bf16_f32 v84, v84, v85
	v_cvt_pk_bf16_f32 v85, v86, v87
	v_cvt_pk_bf16_f32 v87, v92, v93
	s_waitcnt lgkmcnt(0)
	v_pk_mul_f32 v[92:93], v[58:59], v[94:95] op_sel_hi:[1,0]
	v_cvt_pk_bf16_f32 v86, v88, v89
	s_waitcnt lgkmcnt(6)
	v_subrev_u32_e32 v248, s82, v248
	global_store_dwordx4 v248, v[244:247], s[82:83] offset:64 sc1
	ds_bpermute_b32 v238, v250, v84
	ds_bpermute_b32 v239, v250, v85
	ds_bpermute_b32 v240, v250, v86
	ds_bpermute_b32 v241, v250, v87
	ds_bpermute_b32 v242, v250, v90
	v_pk_mul_f32 v[90:91], v[60:61], v[94:95] op_sel_hi:[1,0]
	v_lshl_add_u64 v[88:89], v[82:83], 0, s[16:17]
	v_pk_mul_f32 v[86:87], v[64:65], v[94:95] op_sel_hi:[1,0]
	v_pk_mul_f32 v[84:85], v[62:63], v[94:95] op_sel_hi:[1,0]
	s_mov_b64 s[16:17], 0x90000
	v_cvt_pk_bf16_f32 v84, v84, v85
	v_cvt_pk_bf16_f32 v85, v86, v87
	v_cvt_pk_bf16_f32 v87, v90, v91
	v_add_co_u32_e32 v90, vcc, s15, v82
	v_cvt_pk_bf16_f32 v86, v92, v93
	v_pk_mul_f32 v[92:93], v[50:51], v[94:95] op_sel_hi:[1,0]
	s_nop 0
	v_addc_co_u32_e32 v91, vcc, 0, v83, vcc
	s_waitcnt lgkmcnt(5)
	v_subrev_u32_e32 v236, s82, v236
	global_store_dwordx4 v236, v[232:235], s[82:83] sc1
	ds_bpermute_b32 v244, v250, v84
	ds_bpermute_b32 v245, v250, v85
	ds_bpermute_b32 v246, v250, v86
	ds_bpermute_b32 v247, v250, v87
	ds_bpermute_b32 v248, v250, v90
	v_pk_mul_f32 v[90:91], v[52:53], v[94:95] op_sel_hi:[1,0]
	s_mov_b32 s15, 0x90000
	v_pk_mul_f32 v[86:87], v[56:57], v[94:95] op_sel_hi:[1,0]
	v_pk_mul_f32 v[84:85], v[54:55], v[94:95] op_sel_hi:[1,0]
	s_nop 0
	v_cvt_pk_bf16_f32 v84, v84, v85
	v_cvt_pk_bf16_f32 v85, v86, v87
	v_cvt_pk_bf16_f32 v86, v92, v93
	v_cvt_pk_bf16_f32 v87, v90, v91
	v_mov_b32_e32 v90, v95
	s_waitcnt lgkmcnt(5)
	v_subrev_u32_e32 v242, s82, v242
	global_store_dwordx4 v242, v[238:241], s[82:83] offset:64 sc1
	ds_bpermute_b32 v232, v250, v84
	ds_bpermute_b32 v233, v250, v85
	ds_bpermute_b32 v234, v250, v86
	ds_bpermute_b32 v235, v250, v87
	ds_bpermute_b32 v236, v250, v88
	v_pk_mul_f32 v[94:95], v[42:43], v[90:91] op_sel_hi:[1,0]
	v_pk_mul_f32 v[92:93], v[44:45], v[90:91] op_sel_hi:[1,0]
	v_pk_mul_f32 v[86:87], v[48:49], v[90:91] op_sel_hi:[1,0]
	v_pk_mul_f32 v[84:85], v[46:47], v[90:91] op_sel_hi:[1,0]
	v_lshl_add_u64 v[88:89], v[82:83], 0, s[16:17]
	v_cvt_pk_bf16_f32 v84, v84, v85
	v_cvt_pk_bf16_f32 v85, v86, v87
	v_cvt_pk_bf16_f32 v86, v94, v95
	ds_read2_b32 v[94:95], v158 offset0:160 offset1:176
	v_cvt_pk_bf16_f32 v87, v92, v93
	v_add_co_u32_e32 v92, vcc, s15, v82
	s_mov_b32 s15, 0xa0000
	s_nop 0
	v_addc_co_u32_e32 v93, vcc, 0, v83, vcc
	s_waitcnt lgkmcnt(6)
	v_subrev_u32_e32 v248, s82, v248
	global_store_dwordx4 v248, v[244:247], s[82:83] sc1
	ds_bpermute_b32 v238, v250, v84
	ds_bpermute_b32 v239, v250, v85
	ds_bpermute_b32 v240, v250, v86
	ds_bpermute_b32 v241, v250, v87
	ds_bpermute_b32 v242, v250, v92
	v_pk_mul_f32 v[92:93], v[36:37], v[90:91] op_sel_hi:[1,0]
	s_mov_b64 s[16:17], 0xa0000
	v_pk_mul_f32 v[86:87], v[40:41], v[90:91] op_sel_hi:[1,0]
	v_pk_mul_f32 v[84:85], v[38:39], v[90:91] op_sel_hi:[1,0]
	v_pk_mul_f32 v[90:91], v[34:35], v[90:91] op_sel_hi:[1,0]
	v_cvt_pk_bf16_f32 v84, v84, v85
	v_cvt_pk_bf16_f32 v85, v86, v87
	v_cvt_pk_bf16_f32 v87, v92, v93
	s_waitcnt lgkmcnt(0)
	v_pk_mul_f32 v[92:93], v[26:27], v[94:95] op_sel_hi:[1,0]
	v_cvt_pk_bf16_f32 v86, v90, v91
	s_waitcnt lgkmcnt(6)
	v_subrev_u32_e32 v236, s82, v236
	global_store_dwordx4 v236, v[232:235], s[82:83] offset:64 sc1
	ds_bpermute_b32 v244, v250, v84
	ds_bpermute_b32 v245, v250, v85
	ds_bpermute_b32 v246, v250, v86
	ds_bpermute_b32 v247, v250, v87
	ds_bpermute_b32 v248, v250, v88
	v_pk_mul_f32 v[90:91], v[28:29], v[94:95] op_sel_hi:[1,0]
	v_lshl_add_u64 v[88:89], v[82:83], 0, s[16:17]
	v_pk_mul_f32 v[86:87], v[32:33], v[94:95] op_sel_hi:[1,0]
	v_pk_mul_f32 v[84:85], v[30:31], v[94:95] op_sel_hi:[1,0]
	s_mov_b64 s[16:17], 0xb0000
	v_cvt_pk_bf16_f32 v84, v84, v85
	v_cvt_pk_bf16_f32 v85, v86, v87
	v_cvt_pk_bf16_f32 v87, v90, v91
	v_add_co_u32_e32 v90, vcc, s15, v82
	v_cvt_pk_bf16_f32 v86, v92, v93
	s_mov_b32 s15, 0xb0000
	s_nop 0
	v_addc_co_u32_e32 v91, vcc, 0, v83, vcc
	s_waitcnt lgkmcnt(5)
	v_subrev_u32_e32 v242, s82, v242
	global_store_dwordx4 v242, v[238:241], s[82:83] sc1
	ds_bpermute_b32 v232, v250, v84
	ds_bpermute_b32 v233, v250, v85
	ds_bpermute_b32 v234, v250, v86
	ds_bpermute_b32 v235, v250, v87
	ds_bpermute_b32 v236, v250, v90
	v_pk_mul_f32 v[90:91], v[20:21], v[94:95] op_sel_hi:[1,0]
	v_pk_mul_f32 v[92:93], v[18:19], v[94:95] op_sel_hi:[1,0]
	v_pk_mul_f32 v[86:87], v[24:25], v[94:95] op_sel_hi:[1,0]
	v_pk_mul_f32 v[84:85], v[22:23], v[94:95] op_sel_hi:[1,0]
	s_nop 0
	v_cvt_pk_bf16_f32 v84, v84, v85
	v_cvt_pk_bf16_f32 v85, v86, v87
	v_cvt_pk_bf16_f32 v87, v90, v91
	v_mov_b32_e32 v90, v95
	v_cvt_pk_bf16_f32 v86, v92, v93
	s_waitcnt lgkmcnt(5)
	v_subrev_u32_e32 v248, s82, v248
	global_store_dwordx4 v248, v[244:247], s[82:83] offset:64 sc1
	ds_bpermute_b32 v238, v250, v84
	ds_bpermute_b32 v239, v250, v85
	ds_bpermute_b32 v240, v250, v86
	ds_bpermute_b32 v241, v250, v87
	ds_bpermute_b32 v242, v250, v88
	v_lshl_add_u64 v[88:89], v[82:83], 0, s[16:17]
	v_add_co_u32_e32 v82, vcc, s15, v82
	v_pk_mul_f32 v[84:85], v[14:15], v[90:91] op_sel_hi:[1,0]
	v_pk_mul_f32 v[86:87], v[16:17], v[90:91] op_sel_hi:[1,0]
	v_cvt_pk_bf16_f32 v84, v84, v85
	v_addc_co_u32_e32 v83, vcc, 0, v83, vcc
	v_cvt_pk_bf16_f32 v85, v86, v87
	v_pk_mul_f32 v[92:93], v[12:13], v[90:91] op_sel_hi:[1,0]
	v_pk_mul_f32 v[94:95], v[10:11], v[90:91] op_sel_hi:[1,0]
	v_cvt_pk_bf16_f32 v87, v92, v93
	s_nop 0
	v_cvt_pk_bf16_f32 v86, v94, v95
	s_waitcnt lgkmcnt(5)
	v_subrev_u32_e32 v236, s82, v236
	global_store_dwordx4 v236, v[232:235], s[82:83] sc1
	ds_bpermute_b32 v244, v250, v84
	ds_bpermute_b32 v245, v250, v85
	ds_bpermute_b32 v246, v250, v86
	ds_bpermute_b32 v247, v250, v87
	ds_bpermute_b32 v248, v250, v82
	v_pk_mul_f32 v[82:83], v[6:7], v[90:91] op_sel_hi:[1,0]
	s_nop 0
	v_pk_mul_f32 v[84:85], v[8:9], v[90:91] op_sel_hi:[1,0]
	v_pk_mul_f32 v[86:87], v[4:5], v[90:91] op_sel_hi:[1,0]
	v_pk_mul_f32 v[90:91], v[2:3], v[90:91] op_sel_hi:[1,0]
	v_cvt_pk_bf16_f32 v82, v82, v83
	v_cvt_pk_bf16_f32 v83, v84, v85
	v_cvt_pk_bf16_f32 v85, v86, v87
	s_nop 0
	v_cvt_pk_bf16_f32 v84, v90, v91
	s_waitcnt lgkmcnt(5)
	v_subrev_u32_e32 v242, s82, v242
	global_store_dwordx4 v242, v[238:241], s[82:83] offset:64 sc1
	ds_bpermute_b32 v232, v250, v82
	ds_bpermute_b32 v233, v250, v83
	ds_bpermute_b32 v234, v250, v84
	ds_bpermute_b32 v235, v250, v85
	ds_bpermute_b32 v236, v250, v88
	s_waitcnt lgkmcnt(5)
	v_subrev_u32_e32 v248, s82, v248
	global_store_dwordx4 v248, v[244:247], s[82:83] sc1
	s_waitcnt lgkmcnt(0)
	v_subrev_u32_e32 v236, s82, v236
	global_store_dwordx4 v236, v[232:235], s[82:83] offset:64 sc1
	s_cbranch_execz .LBB0_178

.LBB0_178:
	s_lshl_b32 s14, s14, 10
	v_add_u32_e32 v213, s14, v211
	ds_read_b32 v82, v213
	s_waitcnt lgkmcnt(0)
	v_pk_mul_f32 v[84:85], v[146:147], v[82:83] op_sel_hi:[1,0]
	v_pk_mul_f32 v[86:87], v[144:145], v[82:83] op_sel_hi:[1,0]
	v_pk_mul_f32 v[84:85], v[84:85], v[84:85]
	v_pk_mul_f32 v[88:89], v[140:141], v[82:83] op_sel_hi:[1,0]
	v_pk_fma_f32 v[84:85], v[86:87], v[86:87], v[84:85]
	v_pk_mul_f32 v[86:87], v[142:143], v[82:83] op_sel_hi:[1,0]
	s_nop 0
	v_pk_mul_f32 v[86:87], v[86:87], v[86:87]
	s_nop 0
	v_pk_fma_f32 v[86:87], v[88:89], v[88:89], v[86:87]
	v_pk_mul_f32 v[88:89], v[136:137], v[82:83] op_sel_hi:[1,0]
	v_pk_add_f32 v[84:85], v[84:85], v[86:87]
	v_pk_mul_f32 v[86:87], v[138:139], v[82:83] op_sel_hi:[1,0]
	s_nop 0
	v_pk_mul_f32 v[86:87], v[86:87], v[86:87]
	s_nop 0
	v_pk_fma_f32 v[86:87], v[88:89], v[88:89], v[86:87]
	s_nop 0
	v_pk_add_f32 v[84:85], v[86:87], v[84:85]
	v_pk_mul_f32 v[86:87], v[134:135], v[82:83] op_sel_hi:[1,0]
	v_pk_mul_f32 v[82:83], v[132:133], v[82:83] op_sel_hi:[1,0]
	v_pk_mul_f32 v[86:87], v[86:87], v[86:87]
	s_nop 0
	v_pk_fma_f32 v[82:83], v[82:83], v[82:83], v[86:87]
	s_nop 0
	v_pk_add_f32 v[82:83], v[82:83], v[84:85]
	s_nop 0
	v_add_f32_e32 v82, v82, v83
	ds_swizzle_b32 v83, v82 offset:swizzle(SWAP,16)
	s_waitcnt lgkmcnt(0)
	v_add_f32_e32 v82, v82, v83
	v_mov_b32_e32 v83, v82
	s_nop 1
	v_permlane32_swap_b32_e32 v82, v83
	s_and_saveexec_b64 s[62:63], s[38:39]
	v_add_f32_e32 v82, v82, v83
	ds_write_b32 v183, v82
	s_or_b64 exec, exec, s[62:63]
	ds_read_b32 v82, v213 offset:64
	s_waitcnt lgkmcnt(0)
	v_pk_mul_f32 v[84:85], v[130:131], v[82:83] op_sel_hi:[1,0]
	v_pk_mul_f32 v[86:87], v[128:129], v[82:83] op_sel_hi:[1,0]
	v_pk_mul_f32 v[84:85], v[84:85], v[84:85]
	v_pk_mul_f32 v[88:89], v[124:125], v[82:83] op_sel_hi:[1,0]
	v_pk_fma_f32 v[84:85], v[86:87], v[86:87], v[84:85]
	v_pk_mul_f32 v[86:87], v[126:127], v[82:83] op_sel_hi:[1,0]
	s_nop 0
	v_pk_mul_f32 v[86:87], v[86:87], v[86:87]
	s_nop 0
	v_pk_fma_f32 v[86:87], v[88:89], v[88:89], v[86:87]
	v_pk_mul_f32 v[88:89], v[120:121], v[82:83] op_sel_hi:[1,0]
	v_pk_add_f32 v[84:85], v[84:85], v[86:87]
	v_pk_mul_f32 v[86:87], v[122:123], v[82:83] op_sel_hi:[1,0]
	s_nop 0
	v_pk_mul_f32 v[86:87], v[86:87], v[86:87]
	s_nop 0
	v_pk_fma_f32 v[86:87], v[88:89], v[88:89], v[86:87]
	s_nop 0
	v_pk_add_f32 v[84:85], v[86:87], v[84:85]
	v_pk_mul_f32 v[86:87], v[118:119], v[82:83] op_sel_hi:[1,0]
	v_pk_mul_f32 v[82:83], v[116:117], v[82:83] op_sel_hi:[1,0]
	v_pk_mul_f32 v[86:87], v[86:87], v[86:87]
	s_nop 0
	v_pk_fma_f32 v[82:83], v[82:83], v[82:83], v[86:87]
	s_nop 0
	v_pk_add_f32 v[82:83], v[82:83], v[84:85]
	s_nop 0
	v_add_f32_e32 v82, v82, v83
	ds_swizzle_b32 v83, v82 offset:swizzle(SWAP,16)
	s_waitcnt lgkmcnt(0)
	v_add_f32_e32 v82, v82, v83
	v_mov_b32_e32 v83, v82
	s_nop 1
	v_permlane32_swap_b32_e32 v82, v83
	s_and_saveexec_b64 s[62:63], s[38:39]
	v_add_f32_e32 v82, v82, v83
	ds_write_b32 v195, v82
	s_or_b64 exec, exec, s[62:63]
	ds_read_b32 v82, v213 offset:128
	s_waitcnt lgkmcnt(0)
	v_pk_mul_f32 v[84:85], v[112:113], v[82:83] op_sel_hi:[1,0]
	v_pk_mul_f32 v[86:87], v[110:111], v[82:83] op_sel_hi:[1,0]
	v_pk_mul_f32 v[84:85], v[84:85], v[84:85]
	v_pk_mul_f32 v[88:89], v[106:107], v[82:83] op_sel_hi:[1,0]
	v_pk_fma_f32 v[84:85], v[86:87], v[86:87], v[84:85]
	v_pk_mul_f32 v[86:87], v[108:109], v[82:83] op_sel_hi:[1,0]
	s_nop 0
	v_pk_mul_f32 v[86:87], v[86:87], v[86:87]
	s_nop 0
	v_pk_fma_f32 v[86:87], v[88:89], v[88:89], v[86:87]
	v_pk_mul_f32 v[88:89], v[102:103], v[82:83] op_sel_hi:[1,0]
	v_pk_add_f32 v[84:85], v[84:85], v[86:87]
	v_pk_mul_f32 v[86:87], v[104:105], v[82:83] op_sel_hi:[1,0]
	s_nop 0
	v_pk_mul_f32 v[86:87], v[86:87], v[86:87]
	s_nop 0
	v_pk_fma_f32 v[86:87], v[88:89], v[88:89], v[86:87]
	s_nop 0
	v_pk_add_f32 v[84:85], v[86:87], v[84:85]
	v_pk_mul_f32 v[86:87], v[100:101], v[82:83] op_sel_hi:[1,0]
	v_pk_mul_f32 v[82:83], v[98:99], v[82:83] op_sel_hi:[1,0]
	v_pk_mul_f32 v[86:87], v[86:87], v[86:87]
	s_nop 0
	v_pk_fma_f32 v[82:83], v[82:83], v[82:83], v[86:87]
	s_nop 0
	v_pk_add_f32 v[82:83], v[82:83], v[84:85]
	s_nop 0
	v_add_f32_e32 v82, v82, v83
	ds_swizzle_b32 v83, v82 offset:swizzle(SWAP,16)
	s_waitcnt lgkmcnt(0)
	v_add_f32_e32 v82, v82, v83
	v_mov_b32_e32 v83, v82
	s_nop 1
	v_permlane32_swap_b32_e32 v82, v83
	s_and_saveexec_b64 s[62:63], s[38:39]
	v_add_f32_e32 v82, v82, v83
	ds_write_b32 v197, v82
	s_or_b64 exec, exec, s[62:63]
	ds_read_b32 v82, v213 offset:192
	s_waitcnt lgkmcnt(0)
	v_pk_mul_f32 v[84:85], v[80:81], v[82:83] op_sel_hi:[1,0]
	v_pk_mul_f32 v[86:87], v[78:79], v[82:83] op_sel_hi:[1,0]
	v_pk_mul_f32 v[84:85], v[84:85], v[84:85]
	v_pk_mul_f32 v[88:89], v[74:75], v[82:83] op_sel_hi:[1,0]
	v_pk_fma_f32 v[84:85], v[86:87], v[86:87], v[84:85]
	v_pk_mul_f32 v[86:87], v[76:77], v[82:83] op_sel_hi:[1,0]
	s_nop 0
	v_pk_mul_f32 v[86:87], v[86:87], v[86:87]
	s_nop 0
	v_pk_fma_f32 v[86:87], v[88:89], v[88:89], v[86:87]
	v_pk_mul_f32 v[88:89], v[70:71], v[82:83] op_sel_hi:[1,0]
	v_pk_add_f32 v[84:85], v[84:85], v[86:87]
	v_pk_mul_f32 v[86:87], v[72:73], v[82:83] op_sel_hi:[1,0]
	s_nop 0
	v_pk_mul_f32 v[86:87], v[86:87], v[86:87]
	s_nop 0
	v_pk_fma_f32 v[86:87], v[88:89], v[88:89], v[86:87]
	s_nop 0
	v_pk_add_f32 v[84:85], v[86:87], v[84:85]
	v_pk_mul_f32 v[86:87], v[68:69], v[82:83] op_sel_hi:[1,0]
	v_pk_mul_f32 v[82:83], v[66:67], v[82:83] op_sel_hi:[1,0]
	v_pk_mul_f32 v[86:87], v[86:87], v[86:87]
	s_nop 0
	v_pk_fma_f32 v[82:83], v[82:83], v[82:83], v[86:87]
	s_nop 0
	v_pk_add_f32 v[82:83], v[82:83], v[84:85]
	s_nop 0
	v_add_f32_e32 v82, v82, v83
	ds_swizzle_b32 v83, v82 offset:swizzle(SWAP,16)
	s_waitcnt lgkmcnt(0)
	v_add_f32_e32 v82, v82, v83
	v_mov_b32_e32 v83, v82
	s_nop 1
	v_permlane32_swap_b32_e32 v82, v83
	s_and_saveexec_b64 s[62:63], s[38:39]
	v_add_f32_e32 v82, v82, v83
	ds_write_b32 v199, v82
	s_or_b64 exec, exec, s[62:63]
	ds_read_b32 v82, v213 offset:512
	s_waitcnt lgkmcnt(0)
	v_pk_mul_f32 v[84:85], v[64:65], v[82:83] op_sel_hi:[1,0]
	v_pk_mul_f32 v[86:87], v[62:63], v[82:83] op_sel_hi:[1,0]
	v_pk_mul_f32 v[84:85], v[84:85], v[84:85]
	v_pk_mul_f32 v[88:89], v[58:59], v[82:83] op_sel_hi:[1,0]
	v_pk_fma_f32 v[84:85], v[86:87], v[86:87], v[84:85]
	v_pk_mul_f32 v[86:87], v[60:61], v[82:83] op_sel_hi:[1,0]
	s_nop 0
	v_pk_mul_f32 v[86:87], v[86:87], v[86:87]
	s_nop 0
	v_pk_fma_f32 v[86:87], v[88:89], v[88:89], v[86:87]
	v_pk_mul_f32 v[88:89], v[54:55], v[82:83] op_sel_hi:[1,0]
	v_pk_add_f32 v[84:85], v[84:85], v[86:87]
	v_pk_mul_f32 v[86:87], v[56:57], v[82:83] op_sel_hi:[1,0]
	s_nop 0
	v_pk_mul_f32 v[86:87], v[86:87], v[86:87]
	s_nop 0
	v_pk_fma_f32 v[86:87], v[88:89], v[88:89], v[86:87]
	s_nop 0
	v_pk_add_f32 v[84:85], v[86:87], v[84:85]
	v_pk_mul_f32 v[86:87], v[52:53], v[82:83] op_sel_hi:[1,0]
	v_pk_mul_f32 v[82:83], v[50:51], v[82:83] op_sel_hi:[1,0]
	v_pk_mul_f32 v[86:87], v[86:87], v[86:87]
	s_nop 0
	v_pk_fma_f32 v[82:83], v[82:83], v[82:83], v[86:87]
	s_nop 0
	v_pk_add_f32 v[82:83], v[82:83], v[84:85]
	s_nop 0
	v_add_f32_e32 v82, v82, v83
	ds_swizzle_b32 v83, v82 offset:swizzle(SWAP,16)
	s_waitcnt lgkmcnt(0)
	v_add_f32_e32 v82, v82, v83
	v_mov_b32_e32 v83, v82
	s_nop 1
	v_permlane32_swap_b32_e32 v82, v83
	s_and_saveexec_b64 s[62:63], s[38:39]
	v_add_f32_e32 v82, v82, v83
	ds_write_b32 v201, v82
	s_or_b64 exec, exec, s[62:63]
	ds_read_b32 v82, v213 offset:576
	s_waitcnt lgkmcnt(0)
	v_pk_mul_f32 v[84:85], v[48:49], v[82:83] op_sel_hi:[1,0]
	v_pk_mul_f32 v[86:87], v[46:47], v[82:83] op_sel_hi:[1,0]
	v_pk_mul_f32 v[84:85], v[84:85], v[84:85]
	v_pk_mul_f32 v[88:89], v[42:43], v[82:83] op_sel_hi:[1,0]
	v_pk_fma_f32 v[84:85], v[86:87], v[86:87], v[84:85]
	v_pk_mul_f32 v[86:87], v[44:45], v[82:83] op_sel_hi:[1,0]
	s_nop 0
	v_pk_mul_f32 v[86:87], v[86:87], v[86:87]
	s_nop 0
	v_pk_fma_f32 v[86:87], v[88:89], v[88:89], v[86:87]
	v_pk_mul_f32 v[88:89], v[38:39], v[82:83] op_sel_hi:[1,0]
	v_pk_add_f32 v[84:85], v[84:85], v[86:87]
	v_pk_mul_f32 v[86:87], v[40:41], v[82:83] op_sel_hi:[1,0]
	s_nop 0
	v_pk_mul_f32 v[86:87], v[86:87], v[86:87]
	s_nop 0
	v_pk_fma_f32 v[86:87], v[88:89], v[88:89], v[86:87]
	s_nop 0
	v_pk_add_f32 v[84:85], v[86:87], v[84:85]
	v_pk_mul_f32 v[86:87], v[36:37], v[82:83] op_sel_hi:[1,0]
	v_pk_mul_f32 v[82:83], v[34:35], v[82:83] op_sel_hi:[1,0]
	v_pk_mul_f32 v[86:87], v[86:87], v[86:87]
	s_nop 0
	v_pk_fma_f32 v[82:83], v[82:83], v[82:83], v[86:87]
	s_nop 0
	v_pk_add_f32 v[82:83], v[82:83], v[84:85]
	s_nop 0
	v_add_f32_e32 v82, v82, v83
	ds_swizzle_b32 v83, v82 offset:swizzle(SWAP,16)
	s_waitcnt lgkmcnt(0)
	v_add_f32_e32 v82, v82, v83
	v_mov_b32_e32 v83, v82
	s_nop 1
	v_permlane32_swap_b32_e32 v82, v83
	s_and_saveexec_b64 s[62:63], s[38:39]
	v_add_f32_e32 v82, v82, v83
	ds_write_b32 v203, v82
	s_or_b64 exec, exec, s[62:63]
	ds_read_b32 v82, v213 offset:640
	s_waitcnt lgkmcnt(0)
	v_pk_mul_f32 v[84:85], v[32:33], v[82:83] op_sel_hi:[1,0]
	v_pk_mul_f32 v[86:87], v[30:31], v[82:83] op_sel_hi:[1,0]
	v_pk_mul_f32 v[84:85], v[84:85], v[84:85]
	v_pk_mul_f32 v[88:89], v[26:27], v[82:83] op_sel_hi:[1,0]
	v_pk_fma_f32 v[84:85], v[86:87], v[86:87], v[84:85]
	v_pk_mul_f32 v[86:87], v[28:29], v[82:83] op_sel_hi:[1,0]
	s_nop 0
	v_pk_mul_f32 v[86:87], v[86:87], v[86:87]
	s_nop 0
	v_pk_fma_f32 v[86:87], v[88:89], v[88:89], v[86:87]
	v_pk_mul_f32 v[88:89], v[22:23], v[82:83] op_sel_hi:[1,0]
	v_pk_add_f32 v[84:85], v[84:85], v[86:87]
	v_pk_mul_f32 v[86:87], v[24:25], v[82:83] op_sel_hi:[1,0]
	s_nop 0
	v_pk_mul_f32 v[86:87], v[86:87], v[86:87]
	s_nop 0
	v_pk_fma_f32 v[86:87], v[88:89], v[88:89], v[86:87]
	s_nop 0
	v_pk_add_f32 v[84:85], v[86:87], v[84:85]
	v_pk_mul_f32 v[86:87], v[20:21], v[82:83] op_sel_hi:[1,0]
	v_pk_mul_f32 v[82:83], v[18:19], v[82:83] op_sel_hi:[1,0]
	v_pk_mul_f32 v[86:87], v[86:87], v[86:87]
	s_nop 0
	v_pk_fma_f32 v[82:83], v[82:83], v[82:83], v[86:87]
	s_nop 0
	v_pk_add_f32 v[82:83], v[82:83], v[84:85]
	s_nop 0
	v_add_f32_e32 v82, v82, v83
	ds_swizzle_b32 v83, v82 offset:swizzle(SWAP,16)
	s_waitcnt lgkmcnt(0)
	v_add_f32_e32 v82, v82, v83
	v_mov_b32_e32 v83, v82
	s_nop 1
	v_permlane32_swap_b32_e32 v82, v83
	s_and_saveexec_b64 s[62:63], s[38:39]
	v_add_f32_e32 v82, v82, v83
	ds_write_b32 v205, v82
	s_or_b64 exec, exec, s[62:63]
	ds_read_b32 v82, v213 offset:704
	s_waitcnt lgkmcnt(0)
	v_pk_mul_f32 v[84:85], v[16:17], v[82:83] op_sel_hi:[1,0]
	v_pk_mul_f32 v[86:87], v[14:15], v[82:83] op_sel_hi:[1,0]
	v_pk_mul_f32 v[84:85], v[84:85], v[84:85]
	v_pk_mul_f32 v[88:89], v[10:11], v[82:83] op_sel_hi:[1,0]
	v_pk_fma_f32 v[84:85], v[86:87], v[86:87], v[84:85]
	v_pk_mul_f32 v[86:87], v[12:13], v[82:83] op_sel_hi:[1,0]
	s_nop 0
	v_pk_mul_f32 v[86:87], v[86:87], v[86:87]
	s_nop 0
	v_pk_fma_f32 v[86:87], v[88:89], v[88:89], v[86:87]
	v_pk_mul_f32 v[88:89], v[6:7], v[82:83] op_sel_hi:[1,0]
	v_pk_add_f32 v[84:85], v[84:85], v[86:87]
	v_pk_mul_f32 v[86:87], v[8:9], v[82:83] op_sel_hi:[1,0]
	s_nop 0
	v_pk_mul_f32 v[86:87], v[86:87], v[86:87]
	s_nop 0
	v_pk_fma_f32 v[86:87], v[88:89], v[88:89], v[86:87]
	s_nop 0
	v_pk_add_f32 v[84:85], v[86:87], v[84:85]
	v_pk_mul_f32 v[86:87], v[4:5], v[82:83] op_sel_hi:[1,0]
	v_pk_mul_f32 v[82:83], v[2:3], v[82:83] op_sel_hi:[1,0]
	v_pk_mul_f32 v[86:87], v[86:87], v[86:87]
	s_nop 0
	v_pk_fma_f32 v[82:83], v[82:83], v[82:83], v[86:87]
	s_nop 0
	v_pk_add_f32 v[82:83], v[82:83], v[84:85]
	s_nop 0
	v_add_f32_e32 v82, v82, v83
	ds_swizzle_b32 v83, v82 offset:swizzle(SWAP,16)
	s_waitcnt lgkmcnt(0)
	v_add_f32_e32 v82, v82, v83
	v_mov_b32_e32 v83, v82
	s_nop 1
	v_permlane32_swap_b32_e32 v82, v83
	s_and_saveexec_b64 s[62:63], s[38:39]
	v_add_f32_e32 v82, v82, v83
	ds_write_b32 v207, v82
	s_or_b64 exec, exec, s[62:63]
	s_waitcnt lgkmcnt(0)
	s_barrier
	global_load_dwordx4 v[94:97], v[168:169], off offset:16
	global_load_dwordx4 v[90:93], v[168:169], off
	global_load_dwordx4 v[82:85], v[168:169], off offset:144
	global_load_dwordx4 v[86:89], v[168:169], off offset:128
	ds_read_b32 v158, v183
	ds_read_b32 v159, v194
	s_lshl_b32 s14, s60, 1
	s_and_b32 s14, s14, 14
	s_lshl_b32 s15, s28, 1
	s_or_b32 s14, s88, s14
	s_waitcnt lgkmcnt(0)
	v_add_f32_e32 v158, v158, v159
	v_fmamk_f32 v158, v158, 0x3c000000, v185
	v_rsq_f32_e32 v160, v158
	ds_read2_b32 v[158:159], v213 offset1:16
	s_and_b32 s15, s15, 0x7fffff0
	s_or_b32 s14, s15, s14
	s_lshl_b32 s15, s28, 2
	s_and_b32 s15, s15, 28
	s_waitcnt lgkmcnt(0)
	v_mul_f32_e32 v158, v158, v160
	v_lshlrev_b64 v[160:161], 12, v[174:175]
	v_lshl_add_u64 v[160:161], s[46:47], 0, v[160:161]
	v_pk_mul_f32 v[144:145], v[144:145], v[158:159] op_sel_hi:[1,0]
	v_pk_mul_f32 v[146:147], v[146:147], v[158:159] op_sel_hi:[1,0]
	v_pk_mul_f32 v[218:219], v[140:141], v[158:159] op_sel_hi:[1,0]
	v_lshl_add_u64 v[160:161], v[160:161], 0, v[114:115]
	v_pk_mul_f32 v[140:141], v[142:143], v[158:159] op_sel_hi:[1,0]
	s_lshl_b32 s14, s14, 5
	s_add_i32 s15, s15, s8
	s_add_i32 s28, s15, s14
	s_ashr_i32 s29, s28, 31
	s_lshl_b64 s[14:15], s[28:29], 9
	s_waitcnt vmcnt(0)
	v_pk_mul_f32 v[142:143], v[94:95], v[218:219]
	v_pk_mul_f32 v[214:215], v[92:93], v[146:147]
	v_pk_mul_f32 v[216:217], v[90:91], v[144:145]
	v_pk_fma_f32 v[218:219], v[90:91], v[144:145], 0 op_sel_hi:[1,1,0]
	v_cvt_pk_bf16_f32 v144, v216, v217
	v_cvt_pk_bf16_f32 v145, v214, v215
	v_pk_mul_f32 v[140:141], v[96:97], v[140:141]
	v_pk_fma_f32 v[220:221], v[92:93], v[146:147], 0 op_sel_hi:[1,1,0]
	v_cvt_pk_bf16_f32 v146, v142, v143
	v_cvt_pk_bf16_f32 v147, v140, v141
	ds_bpermute_b32 v238, v250, v144
	ds_bpermute_b32 v239, v250, v145
	ds_bpermute_b32 v240, v250, v146
	ds_bpermute_b32 v241, v250, v147
	ds_bpermute_b32 v242, v250, v160
	s_nop 1
	v_pk_mul_f32 v[144:145], v[136:137], v[158:159] op_sel_hi:[1,0]
	v_pk_mul_f32 v[136:137], v[138:139], v[158:159] op_sel_hi:[1,0]
	v_pk_mul_f32 v[138:139], v[86:87], v[144:145]
	v_pk_mul_f32 v[144:145], v[132:133], v[158:159] op_sel_hi:[1,0]
	v_pk_mul_f32 v[132:133], v[134:135], v[158:159] op_sel_hi:[1,0]
	v_pk_mul_f32 v[136:137], v[88:89], v[136:137]
	v_pk_mul_f32 v[132:133], v[84:85], v[132:133]
	v_pk_mul_f32 v[134:135], v[82:83], v[144:145]
	v_cvt_pk_bf16_f32 v144, v138, v139
	v_cvt_pk_bf16_f32 v145, v136, v137
	v_cvt_pk_bf16_f32 v147, v132, v133
	s_nop 0
	v_cvt_pk_bf16_f32 v146, v134, v135
	ds_bpermute_b32 v244, v250, v144
	ds_bpermute_b32 v245, v250, v145
	ds_bpermute_b32 v246, v250, v146
	ds_bpermute_b32 v247, v250, v147
	ds_bpermute_b32 v248, v250, v160
	ds_read_b32 v144, v195
	ds_read_b32 v145, v196
	v_lshlrev_b64 v[146:147], 12, v[180:181]
	v_lshl_add_u64 v[146:147], s[46:47], 0, v[146:147]
	v_lshl_add_u64 v[146:147], v[146:147], 0, v[114:115]
	s_waitcnt lgkmcnt(0)
	v_add_f32_e32 v144, v144, v145
	v_fmamk_f32 v144, v144, 0x3c000000, v185
	v_rsq_f32_e32 v144, v144
	s_nop 0
	v_mul_f32_e32 v144, v159, v144
	v_pk_mul_f32 v[128:129], v[128:129], v[144:145] op_sel_hi:[1,0]
	v_pk_mul_f32 v[130:131], v[130:131], v[144:145] op_sel_hi:[1,0]
	v_pk_mul_f32 v[160:161], v[90:91], v[128:129]
	v_pk_mul_f32 v[158:159], v[92:93], v[130:131]
	v_pk_mul_f32 v[180:181], v[124:125], v[144:145] op_sel_hi:[1,0]
	v_pk_mul_f32 v[124:125], v[126:127], v[144:145] op_sel_hi:[1,0]
	v_pk_fma_f32 v[214:215], v[90:91], v[128:129], v[218:219]
	v_cvt_pk_bf16_f32 v128, v160, v161
	v_cvt_pk_bf16_f32 v129, v158, v159
	v_pk_mul_f32 v[124:125], v[96:97], v[124:125]
	v_pk_mul_f32 v[126:127], v[94:95], v[180:181]
	v_pk_fma_f32 v[180:181], v[92:93], v[130:131], v[220:221]
	v_cvt_pk_bf16_f32 v130, v126, v127
	v_cvt_pk_bf16_f32 v131, v124, v125
	s_waitcnt lgkmcnt(7)
	v_subrev_u32_e32 v242, s82, v242
	global_store_dwordx4 v242, v[238:241], s[82:83] sc1
	ds_bpermute_b32 v232, v250, v128
	ds_bpermute_b32 v233, v250, v129
	ds_bpermute_b32 v234, v250, v130
	ds_bpermute_b32 v235, v250, v131
	ds_bpermute_b32 v236, v250, v146
	s_nop 1
	v_pk_mul_f32 v[128:129], v[120:121], v[144:145] op_sel_hi:[1,0]
	v_pk_mul_f32 v[120:121], v[122:123], v[144:145] op_sel_hi:[1,0]
	v_pk_mul_f32 v[122:123], v[86:87], v[128:129]
	v_pk_mul_f32 v[128:129], v[116:117], v[144:145] op_sel_hi:[1,0]
	v_pk_mul_f32 v[116:117], v[118:119], v[144:145] op_sel_hi:[1,0]
	v_pk_mul_f32 v[120:121], v[88:89], v[120:121]
	v_pk_mul_f32 v[116:117], v[84:85], v[116:117]
	v_pk_mul_f32 v[118:119], v[82:83], v[128:129]
	v_cvt_pk_bf16_f32 v128, v122, v123
	v_cvt_pk_bf16_f32 v129, v120, v121
	v_cvt_pk_bf16_f32 v131, v116, v117
	s_nop 0
	v_cvt_pk_bf16_f32 v130, v118, v119
	s_waitcnt lgkmcnt(7)
	v_subrev_u32_e32 v248, s82, v248
	global_store_dwordx4 v248, v[244:247], s[82:83] offset:64 sc1
	ds_bpermute_b32 v238, v250, v128
	ds_bpermute_b32 v239, v250, v129
	ds_bpermute_b32 v240, v250, v130
	ds_bpermute_b32 v241, v250, v131
	ds_bpermute_b32 v242, v250, v146
	ds_read_b32 v128, v197
	ds_read_b32 v129, v198
	s_waitcnt lgkmcnt(0)
	v_add_f32_e32 v128, v128, v129
	v_fmamk_f32 v128, v128, 0x3c000000, v185
	v_rsq_f32_e32 v130, v128
	ds_read2_b32 v[128:129], v213 offset0:32 offset1:48
	s_waitcnt lgkmcnt(0)
	v_mul_f32_e32 v128, v128, v130
	v_lshlrev_b64 v[130:131], 12, v[178:179]
	v_pk_mul_f32 v[110:111], v[110:111], v[128:129] op_sel_hi:[1,0]
	v_lshl_add_u64 v[130:131], s[46:47], 0, v[130:131]
	v_pk_mul_f32 v[112:113], v[112:113], v[128:129] op_sel_hi:[1,0]
	v_pk_mul_f32 v[144:145], v[90:91], v[110:111]
	v_lshl_add_u64 v[130:131], v[130:131], 0, v[114:115]
	v_pk_mul_f32 v[146:147], v[92:93], v[112:113]
	v_pk_mul_f32 v[158:159], v[106:107], v[128:129] op_sel_hi:[1,0]
	v_pk_mul_f32 v[106:107], v[108:109], v[128:129] op_sel_hi:[1,0]
	v_cvt_pk_bf16_f32 v144, v144, v145
	v_cvt_pk_bf16_f32 v145, v146, v147
	v_pk_mul_f32 v[108:109], v[94:95], v[158:159]
	v_pk_mul_f32 v[106:107], v[96:97], v[106:107]
	v_cvt_pk_bf16_f32 v146, v108, v109
	v_pk_fma_f32 v[110:111], v[90:91], v[110:111], v[214:215]
	v_cvt_pk_bf16_f32 v147, v106, v107
	s_waitcnt lgkmcnt(8)
	v_subrev_u32_e32 v236, s82, v236
	global_store_dwordx4 v236, v[232:235], s[82:83] sc1
	ds_bpermute_b32 v244, v250, v144
	ds_bpermute_b32 v245, v250, v145
	ds_bpermute_b32 v246, v250, v146
	ds_bpermute_b32 v247, v250, v147
	ds_bpermute_b32 v248, v250, v130
	v_pk_fma_f32 v[112:113], v[92:93], v[112:113], v[180:181]
	s_nop 0
	v_pk_mul_f32 v[144:145], v[102:103], v[128:129] op_sel_hi:[1,0]
	v_pk_mul_f32 v[102:103], v[104:105], v[128:129] op_sel_hi:[1,0]
	v_pk_mul_f32 v[104:105], v[86:87], v[144:145]
	v_pk_mul_f32 v[144:145], v[98:99], v[128:129] op_sel_hi:[1,0]
	v_pk_mul_f32 v[98:99], v[100:101], v[128:129] op_sel_hi:[1,0]
	v_pk_mul_f32 v[102:103], v[88:89], v[102:103]
	v_pk_mul_f32 v[98:99], v[84:85], v[98:99]
	v_pk_mul_f32 v[100:101], v[82:83], v[144:145]
	v_cvt_pk_bf16_f32 v144, v104, v105
	v_cvt_pk_bf16_f32 v145, v102, v103
	v_cvt_pk_bf16_f32 v147, v98, v99
	s_nop 0
	v_cvt_pk_bf16_f32 v146, v100, v101
	s_waitcnt lgkmcnt(8)
	v_subrev_u32_e32 v242, s82, v242
	global_store_dwordx4 v242, v[238:241], s[82:83] offset:64 sc1
	ds_bpermute_b32 v232, v250, v144
	ds_bpermute_b32 v233, v250, v145
	ds_bpermute_b32 v234, v250, v146
	ds_bpermute_b32 v235, v250, v147
	ds_bpermute_b32 v236, v250, v130
	ds_read_b32 v128, v199
	ds_read_b32 v130, v200
	s_waitcnt lgkmcnt(0)
	v_add_f32_e32 v128, v128, v130
	v_fmamk_f32 v128, v128, 0x3c000000, v185
	v_rsq_f32_e32 v128, v128
	v_lshlrev_b64 v[130:131], 12, v[176:177]
	v_lshl_add_u64 v[130:131], s[46:47], 0, v[130:131]
	v_lshl_add_u64 v[130:131], v[130:131], 0, v[114:115]
	v_mul_f32_e32 v128, v129, v128
	v_pk_mul_f32 v[144:145], v[78:79], v[128:129] op_sel_hi:[1,0]
	v_pk_mul_f32 v[80:81], v[80:81], v[128:129] op_sel_hi:[1,0]
	v_pk_mul_f32 v[74:75], v[74:75], v[128:129] op_sel_hi:[1,0]
	v_pk_mul_f32 v[76:77], v[76:77], v[128:129] op_sel_hi:[1,0]
	v_pk_mul_f32 v[146:147], v[92:93], v[80:81]
	v_pk_mul_f32 v[158:159], v[90:91], v[144:145]
	v_pk_mul_f32 v[76:77], v[96:97], v[76:77]
	v_pk_mul_f32 v[78:79], v[94:95], v[74:75]
	v_pk_fma_f32 v[160:161], v[92:93], v[80:81], v[112:113]
	v_pk_fma_f32 v[80:81], v[90:91], v[144:145], v[110:111]
	v_cvt_pk_bf16_f32 v110, v158, v159
	v_cvt_pk_bf16_f32 v111, v146, v147
	v_cvt_pk_bf16_f32 v112, v78, v79
	v_cvt_pk_bf16_f32 v113, v76, v77
	v_pk_mul_f32 v[70:71], v[70:71], v[128:129] op_sel_hi:[1,0]
	v_pk_mul_f32 v[72:73], v[72:73], v[128:129] op_sel_hi:[1,0]
	v_pk_mul_f32 v[66:67], v[66:67], v[128:129] op_sel_hi:[1,0]
	v_pk_mul_f32 v[68:69], v[68:69], v[128:129] op_sel_hi:[1,0]
	s_waitcnt lgkmcnt(7)
	v_subrev_u32_e32 v248, s82, v248
	global_store_dwordx4 v248, v[244:247], s[82:83] sc1
	ds_bpermute_b32 v238, v250, v110
	ds_bpermute_b32 v239, v250, v111
	ds_bpermute_b32 v240, v250, v112
	ds_bpermute_b32 v241, v250, v113
	ds_bpermute_b32 v242, v250, v130
	v_pk_mul_f32 v[72:73], v[88:89], v[72:73]
	v_pk_mul_f32 v[74:75], v[86:87], v[70:71]
	v_pk_mul_f32 v[68:69], v[84:85], v[68:69]
	v_pk_mul_f32 v[70:71], v[82:83], v[66:67]
	v_cvt_pk_bf16_f32 v110, v74, v75
	v_cvt_pk_bf16_f32 v111, v72, v73
	v_cvt_pk_bf16_f32 v113, v68, v69
	v_lshl_add_u64 v[66:67], v[166:167], 0, s[14:15]
	v_cvt_pk_bf16_f32 v112, v70, v71
	s_waitcnt lgkmcnt(7)
	v_subrev_u32_e32 v236, s82, v236
	global_store_dwordx4 v236, v[232:235], s[82:83] offset:64 sc1
	ds_bpermute_b32 v244, v250, v110
	ds_bpermute_b32 v245, v250, v111
	ds_bpermute_b32 v246, v250, v112
	ds_bpermute_b32 v247, v250, v113
	ds_bpermute_b32 v248, v250, v130
	ds_swizzle_b32 v110, v80 offset:swizzle(SWAP,1)
	ds_swizzle_b32 v111, v81 offset:swizzle(SWAP,1)
	ds_swizzle_b32 v112, v160 offset:swizzle(SWAP,1)
	ds_swizzle_b32 v113, v161 offset:swizzle(SWAP,1)
	s_waitcnt lgkmcnt(2)
	v_pk_add_f32 v[80:81], v[80:81], v[110:111]
	ds_swizzle_b32 v110, v80 offset:swizzle(SWAP,2)
	s_waitcnt lgkmcnt(1)
	v_pk_add_f32 v[112:113], v[160:161], v[112:113]
	ds_swizzle_b32 v111, v81 offset:swizzle(SWAP,2)
	ds_swizzle_b32 v128, v112 offset:swizzle(SWAP,2)
	ds_swizzle_b32 v129, v113 offset:swizzle(SWAP,2)
	s_waitcnt lgkmcnt(2)
	v_pk_add_f32 v[80:81], v[80:81], v[110:111]
	ds_swizzle_b32 v110, v80 offset:swizzle(SWAP,4)
	s_waitcnt lgkmcnt(1)
	v_pk_add_f32 v[112:113], v[112:113], v[128:129]
	ds_swizzle_b32 v111, v81 offset:swizzle(SWAP,4)
	ds_swizzle_b32 v128, v112 offset:swizzle(SWAP,4)
	ds_swizzle_b32 v129, v113 offset:swizzle(SWAP,4)
	s_waitcnt lgkmcnt(2)
	v_pk_add_f32 v[80:81], v[80:81], v[110:111]
	ds_swizzle_b32 v110, v80 offset:swizzle(SWAP,8)
	s_waitcnt lgkmcnt(1)
	v_pk_add_f32 v[112:113], v[112:113], v[128:129]
	ds_swizzle_b32 v111, v81 offset:swizzle(SWAP,8)
	ds_swizzle_b32 v128, v112 offset:swizzle(SWAP,8)
	ds_swizzle_b32 v129, v113 offset:swizzle(SWAP,8)
	s_waitcnt lgkmcnt(15)
	v_subrev_u32_e32 v242, s82, v242
	global_store_dwordx4 v242, v[238:241], s[82:83] sc1
	s_waitcnt lgkmcnt(15)
	v_subrev_u32_e32 v248, s82, v248
	global_store_dwordx4 v248, v[244:247], s[82:83] offset:64 sc1
	s_and_saveexec_b64 s[60:61], s[40:41]
	s_cbranch_execz .LBB0_196
	s_waitcnt lgkmcnt(0)
	v_pk_add_f32 v[112:113], v[112:113], v[128:129]
	v_pk_add_f32 v[110:111], v[80:81], v[110:111]
	global_store_dwordx4 v[66:67], v[110:113], off sc1
.LBB0_196:
	s_or_b64 exec, exec, s[60:61]
	v_pk_add_f32 v[80:81], v[140:141], 0 op_sel_hi:[1,0]
	s_waitcnt lgkmcnt(2)
	v_pk_add_f32 v[110:111], v[142:143], 0 op_sel_hi:[1,0]
	v_pk_add_f32 v[80:81], v[80:81], v[124:125]
	v_pk_add_f32 v[110:111], v[110:111], v[126:127]
	v_pk_add_f32 v[80:81], v[80:81], v[106:107]
	v_pk_add_f32 v[106:107], v[110:111], v[108:109]
	v_pk_add_f32 v[76:77], v[80:81], v[76:77]
	v_pk_add_f32 v[78:79], v[106:107], v[78:79]
	ds_swizzle_b32 v106, v78 offset:swizzle(SWAP,1)
	ds_swizzle_b32 v107, v79 offset:swizzle(SWAP,1)
	ds_swizzle_b32 v80, v76 offset:swizzle(SWAP,1)
	ds_swizzle_b32 v81, v77 offset:swizzle(SWAP,1)
	s_waitcnt lgkmcnt(2)
	v_pk_add_f32 v[78:79], v[78:79], v[106:107]
	ds_swizzle_b32 v106, v78 offset:swizzle(SWAP,2)
	s_waitcnt lgkmcnt(1)
	v_pk_add_f32 v[76:77], v[76:77], v[80:81]
	ds_swizzle_b32 v107, v79 offset:swizzle(SWAP,2)
	ds_swizzle_b32 v80, v76 offset:swizzle(SWAP,2)
	ds_swizzle_b32 v81, v77 offset:swizzle(SWAP,2)
	s_waitcnt lgkmcnt(2)
	v_pk_add_f32 v[78:79], v[78:79], v[106:107]
	ds_swizzle_b32 v106, v78 offset:swizzle(SWAP,4)
	s_waitcnt lgkmcnt(1)
	v_pk_add_f32 v[80:81], v[76:77], v[80:81]
	ds_swizzle_b32 v107, v79 offset:swizzle(SWAP,4)
	ds_swizzle_b32 v108, v80 offset:swizzle(SWAP,4)
	ds_swizzle_b32 v109, v81 offset:swizzle(SWAP,4)
	s_waitcnt lgkmcnt(2)
	v_pk_add_f32 v[76:77], v[78:79], v[106:107]
	ds_swizzle_b32 v78, v76 offset:swizzle(SWAP,8)
	s_waitcnt lgkmcnt(1)
	v_pk_add_f32 v[80:81], v[80:81], v[108:109]
	ds_swizzle_b32 v79, v77 offset:swizzle(SWAP,8)
	ds_swizzle_b32 v106, v80 offset:swizzle(SWAP,8)
	ds_swizzle_b32 v107, v81 offset:swizzle(SWAP,8)
	s_and_saveexec_b64 s[60:61], s[40:41]
	s_cbranch_execz .LBB0_198
	s_waitcnt lgkmcnt(0)
	v_pk_add_f32 v[80:81], v[80:81], v[106:107]
	v_pk_add_f32 v[78:79], v[76:77], v[78:79]
	global_store_dwordx4 v[66:67], v[78:81], off offset:16 sc1
.LBB0_198:
	s_or_b64 exec, exec, s[60:61]
	v_pk_add_f32 v[76:77], v[136:137], 0 op_sel_hi:[1,0]
	s_waitcnt lgkmcnt(2)
	v_pk_add_f32 v[78:79], v[138:139], 0 op_sel_hi:[1,0]
	v_pk_add_f32 v[76:77], v[76:77], v[120:121]
	v_pk_add_f32 v[78:79], v[78:79], v[122:123]
	v_pk_add_f32 v[76:77], v[76:77], v[102:103]
	v_pk_add_f32 v[78:79], v[78:79], v[104:105]
	v_pk_add_f32 v[72:73], v[76:77], v[72:73]
	v_pk_add_f32 v[74:75], v[78:79], v[74:75]
	ds_swizzle_b32 v78, v74 offset:swizzle(SWAP,1)
	ds_swizzle_b32 v79, v75 offset:swizzle(SWAP,1)
	ds_swizzle_b32 v76, v72 offset:swizzle(SWAP,1)
	ds_swizzle_b32 v77, v73 offset:swizzle(SWAP,1)
	s_waitcnt lgkmcnt(2)
	v_pk_add_f32 v[74:75], v[74:75], v[78:79]
	ds_swizzle_b32 v78, v74 offset:swizzle(SWAP,2)
	s_waitcnt lgkmcnt(1)
	v_pk_add_f32 v[72:73], v[72:73], v[76:77]
	ds_swizzle_b32 v79, v75 offset:swizzle(SWAP,2)
	ds_swizzle_b32 v76, v72 offset:swizzle(SWAP,2)
	ds_swizzle_b32 v77, v73 offset:swizzle(SWAP,2)
	s_waitcnt lgkmcnt(2)
	v_pk_add_f32 v[74:75], v[74:75], v[78:79]
	ds_swizzle_b32 v78, v74 offset:swizzle(SWAP,4)
	s_waitcnt lgkmcnt(1)
	v_pk_add_f32 v[76:77], v[72:73], v[76:77]
	ds_swizzle_b32 v79, v75 offset:swizzle(SWAP,4)
	ds_swizzle_b32 v80, v76 offset:swizzle(SWAP,4)
	ds_swizzle_b32 v81, v77 offset:swizzle(SWAP,4)
	s_waitcnt lgkmcnt(2)
	v_pk_add_f32 v[72:73], v[74:75], v[78:79]
	ds_swizzle_b32 v74, v72 offset:swizzle(SWAP,8)
	s_waitcnt lgkmcnt(1)
	v_pk_add_f32 v[76:77], v[76:77], v[80:81]
	ds_swizzle_b32 v75, v73 offset:swizzle(SWAP,8)
	ds_swizzle_b32 v78, v76 offset:swizzle(SWAP,8)
	ds_swizzle_b32 v79, v77 offset:swizzle(SWAP,8)
	s_and_saveexec_b64 s[60:61], s[40:41]
	s_cbranch_execz .LBB0_200
	s_waitcnt lgkmcnt(0)
	v_pk_add_f32 v[76:77], v[76:77], v[78:79]
	v_pk_add_f32 v[74:75], v[72:73], v[74:75]
	global_store_dwordx4 v[66:67], v[74:77], off offset:128 sc1
.LBB0_200:
	s_or_b64 exec, exec, s[60:61]
	v_pk_add_f32 v[72:73], v[132:133], 0 op_sel_hi:[1,0]
	s_waitcnt lgkmcnt(2)
	v_pk_add_f32 v[74:75], v[134:135], 0 op_sel_hi:[1,0]
	v_pk_add_f32 v[72:73], v[72:73], v[116:117]
	v_pk_add_f32 v[74:75], v[74:75], v[118:119]
	v_pk_add_f32 v[72:73], v[72:73], v[98:99]
	v_pk_add_f32 v[74:75], v[74:75], v[100:101]
	v_pk_add_f32 v[68:69], v[72:73], v[68:69]
	v_pk_add_f32 v[70:71], v[74:75], v[70:71]
	ds_swizzle_b32 v74, v70 offset:swizzle(SWAP,1)
	ds_swizzle_b32 v75, v71 offset:swizzle(SWAP,1)
	ds_swizzle_b32 v72, v68 offset:swizzle(SWAP,1)
	ds_swizzle_b32 v73, v69 offset:swizzle(SWAP,1)
	s_waitcnt lgkmcnt(2)
	v_pk_add_f32 v[70:71], v[70:71], v[74:75]
	ds_swizzle_b32 v74, v70 offset:swizzle(SWAP,2)
	s_waitcnt lgkmcnt(1)
	v_pk_add_f32 v[68:69], v[68:69], v[72:73]
	ds_swizzle_b32 v75, v71 offset:swizzle(SWAP,2)
	ds_swizzle_b32 v72, v68 offset:swizzle(SWAP,2)
	ds_swizzle_b32 v73, v69 offset:swizzle(SWAP,2)
	s_waitcnt lgkmcnt(2)
	v_pk_add_f32 v[70:71], v[70:71], v[74:75]
	ds_swizzle_b32 v74, v70 offset:swizzle(SWAP,4)
	s_waitcnt lgkmcnt(1)
	v_pk_add_f32 v[72:73], v[68:69], v[72:73]
	ds_swizzle_b32 v75, v71 offset:swizzle(SWAP,4)
	ds_swizzle_b32 v76, v72 offset:swizzle(SWAP,4)
	ds_swizzle_b32 v77, v73 offset:swizzle(SWAP,4)
	s_waitcnt lgkmcnt(2)
	v_pk_add_f32 v[68:69], v[70:71], v[74:75]
	ds_swizzle_b32 v70, v68 offset:swizzle(SWAP,8)
	s_waitcnt lgkmcnt(1)
	v_pk_add_f32 v[72:73], v[72:73], v[76:77]
	ds_swizzle_b32 v71, v69 offset:swizzle(SWAP,8)
	ds_swizzle_b32 v74, v72 offset:swizzle(SWAP,8)
	ds_swizzle_b32 v75, v73 offset:swizzle(SWAP,8)
	s_and_saveexec_b64 s[60:61], s[40:41]
	s_cbranch_execz .LBB0_202
	s_waitcnt lgkmcnt(0)
	v_pk_add_f32 v[72:73], v[72:73], v[74:75]
	v_pk_add_f32 v[70:71], v[68:69], v[70:71]
	global_store_dwordx4 v[66:67], v[70:73], off offset:144 sc1
.LBB0_202:
	s_or_b64 exec, exec, s[60:61]
	ds_read_b32 v66, v201
	ds_read_b32 v67, v202
	ds_read2_b32 v[68:69], v213 offset0:128 offset1:144
	s_mov_b64 s[14:15], 0x80000
	s_waitcnt lgkmcnt(1)
	v_add_f32_e32 v66, v66, v67
	v_fmamk_f32 v66, v66, 0x3c000000, v185
	v_rsq_f32_e32 v66, v66
	s_waitcnt lgkmcnt(0)
	v_mul_f32_e32 v68, v68, v66
	v_lshlrev_b64 v[66:67], 12, v[174:175]
	v_lshl_add_u64 v[66:67], s[46:47], 0, v[66:67]
	v_lshl_add_u64 v[66:67], v[66:67], 0, v[114:115]
	v_pk_mul_f32 v[64:65], v[64:65], v[68:69] op_sel_hi:[1,0]
	v_lshl_add_u64 v[70:71], v[66:67], 0, s[14:15]
	v_pk_mul_f32 v[62:63], v[62:63], v[68:69] op_sel_hi:[1,0]
	v_pk_mul_f32 v[72:73], v[92:93], v[64:65]
	v_pk_mul_f32 v[76:77], v[58:59], v[68:69] op_sel_hi:[1,0]
	s_mov_b32 s14, 0x80000
	v_pk_mul_f32 v[74:75], v[90:91], v[62:63]
	v_pk_mul_f32 v[58:59], v[60:61], v[68:69] op_sel_hi:[1,0]
	v_pk_mul_f32 v[60:61], v[94:95], v[76:77]
	v_pk_fma_f32 v[76:77], v[90:91], v[62:63], 0 op_sel_hi:[1,1,0]
	v_cvt_pk_bf16_f32 v63, v72, v73
	v_add_co_u32_e32 v72, vcc, s14, v66
	v_cvt_pk_bf16_f32 v62, v74, v75
	v_pk_mul_f32 v[58:59], v[96:97], v[58:59]
	s_nop 0
	v_addc_co_u32_e32 v73, vcc, 0, v67, vcc
	v_pk_fma_f32 v[78:79], v[92:93], v[64:65], 0 op_sel_hi:[1,1,0]
	v_cvt_pk_bf16_f32 v64, v60, v61
	v_cvt_pk_bf16_f32 v65, v58, v59
	ds_bpermute_b32 v232, v250, v62
	ds_bpermute_b32 v233, v250, v63
	ds_bpermute_b32 v234, v250, v64
	ds_bpermute_b32 v235, v250, v65
	ds_bpermute_b32 v236, v250, v72
	s_mov_b64 s[14:15], 0x90000
	s_nop 0
	v_pk_mul_f32 v[62:63], v[54:55], v[68:69] op_sel_hi:[1,0]
	v_pk_mul_f32 v[54:55], v[56:57], v[68:69] op_sel_hi:[1,0]
	v_pk_mul_f32 v[56:57], v[86:87], v[62:63]
	v_pk_mul_f32 v[62:63], v[50:51], v[68:69] op_sel_hi:[1,0]
	v_pk_mul_f32 v[50:51], v[52:53], v[68:69] op_sel_hi:[1,0]
	v_pk_mul_f32 v[54:55], v[88:89], v[54:55]
	v_pk_mul_f32 v[50:51], v[84:85], v[50:51]
	v_pk_mul_f32 v[52:53], v[82:83], v[62:63]
	v_cvt_pk_bf16_f32 v62, v56, v57
	v_cvt_pk_bf16_f32 v63, v54, v55
	v_cvt_pk_bf16_f32 v65, v50, v51
	s_nop 0
	v_cvt_pk_bf16_f32 v64, v52, v53
	ds_bpermute_b32 v238, v250, v62
	ds_bpermute_b32 v239, v250, v63
	ds_bpermute_b32 v240, v250, v64
	ds_bpermute_b32 v241, v250, v65
	ds_bpermute_b32 v242, v250, v70
	ds_read_b32 v62, v203
	ds_read_b32 v63, v204
	v_lshl_add_u64 v[64:65], v[66:67], 0, s[14:15]
	s_mov_b32 s14, 0x90000
	s_waitcnt lgkmcnt(0)
	v_add_f32_e32 v62, v62, v63
	v_fmamk_f32 v62, v62, 0x3c000000, v185
	v_rsq_f32_e32 v62, v62
	s_nop 0
	v_mul_f32_e32 v62, v69, v62
	v_pk_mul_f32 v[48:49], v[48:49], v[62:63] op_sel_hi:[1,0]
	v_pk_mul_f32 v[46:47], v[46:47], v[62:63] op_sel_hi:[1,0]
	v_pk_mul_f32 v[68:69], v[92:93], v[48:49]
	v_pk_mul_f32 v[70:71], v[90:91], v[46:47]
	v_pk_fma_f32 v[74:75], v[90:91], v[46:47], v[76:77]
	v_cvt_pk_bf16_f32 v47, v68, v69
	v_add_co_u32_e32 v68, vcc, s14, v66
	v_pk_mul_f32 v[72:73], v[42:43], v[62:63] op_sel_hi:[1,0]
	v_pk_mul_f32 v[42:43], v[44:45], v[62:63] op_sel_hi:[1,0]
	v_cvt_pk_bf16_f32 v46, v70, v71
	v_addc_co_u32_e32 v69, vcc, 0, v67, vcc
	v_pk_mul_f32 v[42:43], v[96:97], v[42:43]
	v_pk_mul_f32 v[44:45], v[94:95], v[72:73]
	v_pk_fma_f32 v[72:73], v[92:93], v[48:49], v[78:79]
	v_cvt_pk_bf16_f32 v48, v44, v45
	v_cvt_pk_bf16_f32 v49, v42, v43
	s_waitcnt lgkmcnt(7)
	v_subrev_u32_e32 v236, s82, v236
	global_store_dwordx4 v236, v[232:235], s[82:83] sc1
	ds_bpermute_b32 v244, v250, v46
	ds_bpermute_b32 v245, v250, v47
	ds_bpermute_b32 v246, v250, v48
	ds_bpermute_b32 v247, v250, v49
	ds_bpermute_b32 v248, v250, v68
	s_mov_b64 s[14:15], 0xa0000
	s_nop 0
	v_pk_mul_f32 v[46:47], v[38:39], v[62:63] op_sel_hi:[1,0]
	v_pk_mul_f32 v[38:39], v[40:41], v[62:63] op_sel_hi:[1,0]
	v_pk_mul_f32 v[40:41], v[86:87], v[46:47]
	v_pk_mul_f32 v[46:47], v[34:35], v[62:63] op_sel_hi:[1,0]
	v_pk_mul_f32 v[34:35], v[36:37], v[62:63] op_sel_hi:[1,0]
	v_pk_mul_f32 v[38:39], v[88:89], v[38:39]
	v_pk_mul_f32 v[34:35], v[84:85], v[34:35]
	v_pk_mul_f32 v[36:37], v[82:83], v[46:47]
	v_cvt_pk_bf16_f32 v46, v40, v41
	v_cvt_pk_bf16_f32 v47, v38, v39
	v_cvt_pk_bf16_f32 v49, v34, v35
	s_nop 0
	v_cvt_pk_bf16_f32 v48, v36, v37
	s_waitcnt lgkmcnt(7)
	v_subrev_u32_e32 v242, s82, v242
	global_store_dwordx4 v242, v[238:241], s[82:83] offset:64 sc1
	ds_bpermute_b32 v232, v250, v46
	ds_bpermute_b32 v233, v250, v47
	ds_bpermute_b32 v234, v250, v48
	ds_bpermute_b32 v235, v250, v49
	ds_bpermute_b32 v236, v250, v64
	ds_read_b32 v46, v205
	ds_read_b32 v47, v206
	s_waitcnt lgkmcnt(0)
	v_add_f32_e32 v46, v46, v47
	v_fmamk_f32 v46, v46, 0x3c000000, v185
	v_rsq_f32_e32 v48, v46
	ds_read2_b32 v[46:47], v213 offset0:160 offset1:176
	s_waitcnt lgkmcnt(0)
	v_mul_f32_e32 v46, v46, v48
	v_lshl_add_u64 v[48:49], v[66:67], 0, s[14:15]
	v_pk_mul_f32 v[30:31], v[30:31], v[46:47] op_sel_hi:[1,0]
	v_pk_mul_f32 v[68:69], v[26:27], v[46:47] op_sel_hi:[1,0]
	s_mov_b32 s14, 0xa0000
	v_pk_mul_f32 v[32:33], v[32:33], v[46:47] op_sel_hi:[1,0]
	v_pk_mul_f32 v[62:63], v[90:91], v[30:31]
	v_pk_mul_f32 v[26:27], v[28:29], v[46:47] op_sel_hi:[1,0]
	v_pk_mul_f32 v[28:29], v[94:95], v[68:69]
	v_add_co_u32_e32 v68, vcc, s14, v66
	v_pk_mul_f32 v[64:65], v[92:93], v[32:33]
	v_cvt_pk_bf16_f32 v62, v62, v63
	s_nop 0
	v_addc_co_u32_e32 v69, vcc, 0, v67, vcc
	v_cvt_pk_bf16_f32 v63, v64, v65
	v_pk_mul_f32 v[26:27], v[96:97], v[26:27]
	v_cvt_pk_bf16_f32 v64, v28, v29
	s_mov_b64 s[14:15], 0xb0000
	v_cvt_pk_bf16_f32 v65, v26, v27
	s_waitcnt lgkmcnt(8)
	v_subrev_u32_e32 v248, s82, v248
	global_store_dwordx4 v248, v[244:247], s[82:83] sc1
	ds_bpermute_b32 v238, v250, v62
	ds_bpermute_b32 v239, v250, v63
	ds_bpermute_b32 v240, v250, v64
	ds_bpermute_b32 v241, v250, v65
	ds_bpermute_b32 v242, v250, v68
	v_pk_fma_f32 v[30:31], v[90:91], v[30:31], v[74:75]
	v_pk_fma_f32 v[32:33], v[92:93], v[32:33], v[72:73]
	v_pk_mul_f32 v[62:63], v[22:23], v[46:47] op_sel_hi:[1,0]
	v_pk_mul_f32 v[22:23], v[24:25], v[46:47] op_sel_hi:[1,0]
	v_pk_mul_f32 v[24:25], v[86:87], v[62:63]
	v_pk_mul_f32 v[62:63], v[18:19], v[46:47] op_sel_hi:[1,0]
	v_pk_mul_f32 v[18:19], v[20:21], v[46:47] op_sel_hi:[1,0]
	v_pk_mul_f32 v[22:23], v[88:89], v[22:23]
	v_pk_mul_f32 v[18:19], v[84:85], v[18:19]
	v_pk_mul_f32 v[20:21], v[82:83], v[62:63]
	v_cvt_pk_bf16_f32 v62, v24, v25
	v_cvt_pk_bf16_f32 v63, v22, v23
	v_cvt_pk_bf16_f32 v65, v18, v19
	s_nop 0
	v_cvt_pk_bf16_f32 v64, v20, v21
	s_waitcnt lgkmcnt(8)
	v_subrev_u32_e32 v236, s82, v236
	global_store_dwordx4 v236, v[232:235], s[82:83] offset:64 sc1
	ds_bpermute_b32 v244, v250, v62
	ds_bpermute_b32 v245, v250, v63
	ds_bpermute_b32 v246, v250, v64
	ds_bpermute_b32 v247, v250, v65
	ds_bpermute_b32 v248, v250, v48
	ds_read_b32 v46, v207
	ds_read_b32 v48, v208
	s_waitcnt lgkmcnt(0)
	v_add_f32_e32 v46, v46, v48
	v_fmamk_f32 v46, v46, 0x3c000000, v185
	v_rsq_f32_e32 v46, v46
	v_lshl_add_u64 v[48:49], v[66:67], 0, s[14:15]
	s_mov_b32 s14, 0xb0000
	v_mul_f32_e32 v46, v47, v46
	v_pk_mul_f32 v[10:11], v[10:11], v[46:47] op_sel_hi:[1,0]
	v_pk_mul_f32 v[62:63], v[14:15], v[46:47] op_sel_hi:[1,0]
	v_pk_mul_f32 v[16:17], v[16:17], v[46:47] op_sel_hi:[1,0]
	v_pk_mul_f32 v[12:13], v[12:13], v[46:47] op_sel_hi:[1,0]
	v_pk_mul_f32 v[14:15], v[94:95], v[10:11]
	v_add_co_u32_e32 v10, vcc, s14, v66
	v_pk_mul_f32 v[64:65], v[92:93], v[16:17]
	v_pk_mul_f32 v[68:69], v[90:91], v[62:63]
	v_pk_mul_f32 v[12:13], v[96:97], v[12:13]
	v_pk_fma_f32 v[70:71], v[92:93], v[16:17], v[32:33]
	v_pk_fma_f32 v[16:17], v[90:91], v[62:63], v[30:31]
	v_cvt_pk_bf16_f32 v30, v68, v69
	v_cvt_pk_bf16_f32 v31, v64, v65
	v_cvt_pk_bf16_f32 v32, v14, v15
	v_cvt_pk_bf16_f32 v33, v12, v13
	v_addc_co_u32_e32 v11, vcc, 0, v67, vcc
	v_pk_mul_f32 v[6:7], v[6:7], v[46:47] op_sel_hi:[1,0]
	v_pk_mul_f32 v[8:9], v[8:9], v[46:47] op_sel_hi:[1,0]
	v_pk_mul_f32 v[2:3], v[2:3], v[46:47] op_sel_hi:[1,0]
	v_pk_mul_f32 v[4:5], v[4:5], v[46:47] op_sel_hi:[1,0]
	s_waitcnt lgkmcnt(7)
	v_subrev_u32_e32 v242, s82, v242
	global_store_dwordx4 v242, v[238:241], s[82:83] sc1
	ds_bpermute_b32 v232, v250, v30
	ds_bpermute_b32 v233, v250, v31
	ds_bpermute_b32 v234, v250, v32
	ds_bpermute_b32 v235, v250, v33
	ds_bpermute_b32 v236, v250, v10
	v_pk_mul_f32 v[8:9], v[88:89], v[8:9]
	v_pk_mul_f32 v[10:11], v[86:87], v[6:7]
	v_pk_mul_f32 v[4:5], v[84:85], v[4:5]
	v_pk_mul_f32 v[6:7], v[82:83], v[2:3]
	v_cvt_pk_bf16_f32 v30, v10, v11
	v_cvt_pk_bf16_f32 v31, v8, v9
	v_cvt_pk_bf16_f32 v33, v4, v5
	s_add_i32 s14, s28, 2
	v_cvt_pk_bf16_f32 v32, v6, v7
	s_waitcnt lgkmcnt(7)
	v_subrev_u32_e32 v248, s82, v248
	global_store_dwordx4 v248, v[244:247], s[82:83] offset:64 sc1
	ds_bpermute_b32 v238, v250, v30
	ds_bpermute_b32 v239, v250, v31
	ds_bpermute_b32 v240, v250, v32
	ds_bpermute_b32 v241, v250, v33
	ds_bpermute_b32 v242, v250, v48
	ds_swizzle_b32 v30, v16 offset:swizzle(SWAP,1)
	ds_swizzle_b32 v31, v17 offset:swizzle(SWAP,1)
	ds_swizzle_b32 v32, v70 offset:swizzle(SWAP,1)
	ds_swizzle_b32 v33, v71 offset:swizzle(SWAP,1)
	s_ashr_i32 s15, s14, 31
	s_lshl_b64 s[14:15], s[14:15], 9
	s_waitcnt lgkmcnt(2)
	v_pk_add_f32 v[16:17], v[16:17], v[30:31]
	ds_swizzle_b32 v30, v16 offset:swizzle(SWAP,2)
	s_waitcnt lgkmcnt(1)
	v_pk_add_f32 v[32:33], v[70:71], v[32:33]
	ds_swizzle_b32 v31, v17 offset:swizzle(SWAP,2)
	ds_swizzle_b32 v46, v32 offset:swizzle(SWAP,2)
	ds_swizzle_b32 v47, v33 offset:swizzle(SWAP,2)
	v_lshl_add_u64 v[2:3], v[166:167], 0, s[14:15]
	s_waitcnt lgkmcnt(2)
	v_pk_add_f32 v[16:17], v[16:17], v[30:31]
	ds_swizzle_b32 v30, v16 offset:swizzle(SWAP,4)
	s_waitcnt lgkmcnt(1)
	v_pk_add_f32 v[32:33], v[32:33], v[46:47]
	ds_swizzle_b32 v31, v17 offset:swizzle(SWAP,4)
	ds_swizzle_b32 v46, v32 offset:swizzle(SWAP,4)
	ds_swizzle_b32 v47, v33 offset:swizzle(SWAP,4)
	s_waitcnt lgkmcnt(2)
	v_pk_add_f32 v[16:17], v[16:17], v[30:31]
	ds_swizzle_b32 v30, v16 offset:swizzle(SWAP,8)
	s_waitcnt lgkmcnt(1)
	v_pk_add_f32 v[32:33], v[32:33], v[46:47]
	ds_swizzle_b32 v31, v17 offset:swizzle(SWAP,8)
	ds_swizzle_b32 v46, v32 offset:swizzle(SWAP,8)
	ds_swizzle_b32 v47, v33 offset:swizzle(SWAP,8)
	s_waitcnt lgkmcnt(15)
	v_subrev_u32_e32 v236, s82, v236
	global_store_dwordx4 v236, v[232:235], s[82:83] sc1
	s_waitcnt lgkmcnt(15)
	v_subrev_u32_e32 v242, s82, v242
	global_store_dwordx4 v242, v[238:241], s[82:83] offset:64 sc1
	s_and_saveexec_b64 s[28:29], s[40:41]
	s_cbranch_execz .LBB0_204
	s_waitcnt lgkmcnt(0)
	v_pk_add_f32 v[32:33], v[32:33], v[46:47]
	v_pk_add_f32 v[30:31], v[16:17], v[30:31]
	global_store_dwordx4 v[2:3], v[30:33], off sc1
.LBB0_204:
	s_or_b64 exec, exec, s[28:29]
	v_pk_add_f32 v[16:17], v[58:59], 0 op_sel_hi:[1,0]
	s_waitcnt lgkmcnt(2)
	v_pk_add_f32 v[30:31], v[60:61], 0 op_sel_hi:[1,0]
	v_pk_add_f32 v[16:17], v[16:17], v[42:43]
	v_pk_add_f32 v[30:31], v[30:31], v[44:45]
	v_pk_add_f32 v[16:17], v[16:17], v[26:27]
	v_pk_add_f32 v[26:27], v[30:31], v[28:29]
	v_pk_add_f32 v[12:13], v[16:17], v[12:13]
	v_pk_add_f32 v[14:15], v[26:27], v[14:15]
	ds_swizzle_b32 v26, v14 offset:swizzle(SWAP,1)
	ds_swizzle_b32 v27, v15 offset:swizzle(SWAP,1)
	ds_swizzle_b32 v16, v12 offset:swizzle(SWAP,1)
	ds_swizzle_b32 v17, v13 offset:swizzle(SWAP,1)
	s_waitcnt lgkmcnt(2)
	v_pk_add_f32 v[14:15], v[14:15], v[26:27]
	ds_swizzle_b32 v26, v14 offset:swizzle(SWAP,2)
	s_waitcnt lgkmcnt(1)
	v_pk_add_f32 v[12:13], v[12:13], v[16:17]
	ds_swizzle_b32 v27, v15 offset:swizzle(SWAP,2)
	ds_swizzle_b32 v16, v12 offset:swizzle(SWAP,2)
	ds_swizzle_b32 v17, v13 offset:swizzle(SWAP,2)
	s_waitcnt lgkmcnt(2)
	v_pk_add_f32 v[14:15], v[14:15], v[26:27]
	ds_swizzle_b32 v26, v14 offset:swizzle(SWAP,4)
	s_waitcnt lgkmcnt(1)
	v_pk_add_f32 v[16:17], v[12:13], v[16:17]
	ds_swizzle_b32 v27, v15 offset:swizzle(SWAP,4)
	ds_swizzle_b32 v28, v16 offset:swizzle(SWAP,4)
	ds_swizzle_b32 v29, v17 offset:swizzle(SWAP,4)
	s_waitcnt lgkmcnt(2)
	v_pk_add_f32 v[12:13], v[14:15], v[26:27]
	ds_swizzle_b32 v14, v12 offset:swizzle(SWAP,8)
	s_waitcnt lgkmcnt(1)
	v_pk_add_f32 v[16:17], v[16:17], v[28:29]
	ds_swizzle_b32 v15, v13 offset:swizzle(SWAP,8)
	ds_swizzle_b32 v26, v16 offset:swizzle(SWAP,8)
	ds_swizzle_b32 v27, v17 offset:swizzle(SWAP,8)
	s_and_saveexec_b64 s[28:29], s[40:41]
	s_cbranch_execz .LBB0_206
	s_waitcnt lgkmcnt(0)
	v_pk_add_f32 v[16:17], v[16:17], v[26:27]
	v_pk_add_f32 v[14:15], v[12:13], v[14:15]
	global_store_dwordx4 v[2:3], v[14:17], off offset:16 sc1
.LBB0_206:
	s_or_b64 exec, exec, s[28:29]
	v_pk_add_f32 v[12:13], v[54:55], 0 op_sel_hi:[1,0]
	s_waitcnt lgkmcnt(2)
	v_pk_add_f32 v[14:15], v[56:57], 0 op_sel_hi:[1,0]
	v_pk_add_f32 v[12:13], v[12:13], v[38:39]
	v_pk_add_f32 v[14:15], v[14:15], v[40:41]
	v_pk_add_f32 v[12:13], v[12:13], v[22:23]
	v_pk_add_f32 v[14:15], v[14:15], v[24:25]
	v_pk_add_f32 v[8:9], v[12:13], v[8:9]
	v_pk_add_f32 v[10:11], v[14:15], v[10:11]
	ds_swizzle_b32 v14, v10 offset:swizzle(SWAP,1)
	ds_swizzle_b32 v15, v11 offset:swizzle(SWAP,1)
	ds_swizzle_b32 v12, v8 offset:swizzle(SWAP,1)
	ds_swizzle_b32 v13, v9 offset:swizzle(SWAP,1)
	s_waitcnt lgkmcnt(2)
	v_pk_add_f32 v[10:11], v[10:11], v[14:15]
	ds_swizzle_b32 v14, v10 offset:swizzle(SWAP,2)
	s_waitcnt lgkmcnt(1)
	v_pk_add_f32 v[8:9], v[8:9], v[12:13]
	ds_swizzle_b32 v15, v11 offset:swizzle(SWAP,2)
	ds_swizzle_b32 v12, v8 offset:swizzle(SWAP,2)
	ds_swizzle_b32 v13, v9 offset:swizzle(SWAP,2)
	s_waitcnt lgkmcnt(2)
	v_pk_add_f32 v[10:11], v[10:11], v[14:15]
	ds_swizzle_b32 v14, v10 offset:swizzle(SWAP,4)
	s_waitcnt lgkmcnt(1)
	v_pk_add_f32 v[12:13], v[8:9], v[12:13]
	ds_swizzle_b32 v15, v11 offset:swizzle(SWAP,4)
	ds_swizzle_b32 v16, v12 offset:swizzle(SWAP,4)
	ds_swizzle_b32 v17, v13 offset:swizzle(SWAP,4)
	s_waitcnt lgkmcnt(2)
	v_pk_add_f32 v[8:9], v[10:11], v[14:15]
	ds_swizzle_b32 v10, v8 offset:swizzle(SWAP,8)
	s_waitcnt lgkmcnt(1)
	v_pk_add_f32 v[12:13], v[12:13], v[16:17]
	ds_swizzle_b32 v11, v9 offset:swizzle(SWAP,8)
	ds_swizzle_b32 v14, v12 offset:swizzle(SWAP,8)
	ds_swizzle_b32 v15, v13 offset:swizzle(SWAP,8)
	s_and_saveexec_b64 s[28:29], s[40:41]
	s_cbranch_execz .LBB0_208
	s_waitcnt lgkmcnt(0)
	v_pk_add_f32 v[12:13], v[12:13], v[14:15]
	v_pk_add_f32 v[10:11], v[8:9], v[10:11]
	global_store_dwordx4 v[2:3], v[10:13], off offset:128 sc1
.LBB0_208:
	s_or_b64 exec, exec, s[28:29]
	v_pk_add_f32 v[8:9], v[50:51], 0 op_sel_hi:[1,0]
	s_waitcnt lgkmcnt(2)
	v_pk_add_f32 v[10:11], v[52:53], 0 op_sel_hi:[1,0]
	v_pk_add_f32 v[8:9], v[8:9], v[34:35]
	v_pk_add_f32 v[10:11], v[10:11], v[36:37]
	v_pk_add_f32 v[8:9], v[8:9], v[18:19]
	v_pk_add_f32 v[10:11], v[10:11], v[20:21]
	v_pk_add_f32 v[4:5], v[8:9], v[4:5]
	v_pk_add_f32 v[6:7], v[10:11], v[6:7]
	ds_swizzle_b32 v10, v6 offset:swizzle(SWAP,1)
	ds_swizzle_b32 v11, v7 offset:swizzle(SWAP,1)
	ds_swizzle_b32 v8, v4 offset:swizzle(SWAP,1)
	ds_swizzle_b32 v9, v5 offset:swizzle(SWAP,1)
	s_waitcnt lgkmcnt(2)
	v_pk_add_f32 v[6:7], v[6:7], v[10:11]
	ds_swizzle_b32 v10, v6 offset:swizzle(SWAP,2)
	s_waitcnt lgkmcnt(1)
	v_pk_add_f32 v[4:5], v[4:5], v[8:9]
	ds_swizzle_b32 v11, v7 offset:swizzle(SWAP,2)
	ds_swizzle_b32 v8, v4 offset:swizzle(SWAP,2)
	ds_swizzle_b32 v9, v5 offset:swizzle(SWAP,2)
	s_waitcnt lgkmcnt(2)
	v_pk_add_f32 v[6:7], v[6:7], v[10:11]
	ds_swizzle_b32 v10, v6 offset:swizzle(SWAP,4)
	s_waitcnt lgkmcnt(1)
	v_pk_add_f32 v[8:9], v[4:5], v[8:9]
	ds_swizzle_b32 v11, v7 offset:swizzle(SWAP,4)
	ds_swizzle_b32 v12, v8 offset:swizzle(SWAP,4)
	ds_swizzle_b32 v13, v9 offset:swizzle(SWAP,4)
	s_waitcnt lgkmcnt(2)
	v_pk_add_f32 v[4:5], v[6:7], v[10:11]
	ds_swizzle_b32 v6, v4 offset:swizzle(SWAP,8)
	s_waitcnt lgkmcnt(1)
	v_pk_add_f32 v[8:9], v[8:9], v[12:13]
	ds_swizzle_b32 v7, v5 offset:swizzle(SWAP,8)
	ds_swizzle_b32 v10, v8 offset:swizzle(SWAP,8)
	ds_swizzle_b32 v11, v9 offset:swizzle(SWAP,8)
	s_and_saveexec_b64 s[28:29], s[40:41]
	s_cbranch_execz .LBB0_210
	s_waitcnt lgkmcnt(0)
	v_pk_add_f32 v[8:9], v[8:9], v[10:11]
	v_pk_add_f32 v[6:7], v[4:5], v[6:7]
	global_store_dwordx4 v[2:3], v[6:9], off offset:144 sc1

.LBB0_352:
	s_ashr_i32 s59, s58, 31
	s_lshl_b64 s[14:15], s[58:59], 25
	s_add_u32 s14, s37, s14
	s_addc_u32 s15, s64, s15
	v_lshlrev_b32_e32 v114, 1, v177
	v_ashrrev_i32_e32 v153, 31, v152
	v_lshl_add_u64 v[132:133], s[14:15], 0, v[114:115]
	v_lshlrev_b64 v[136:137], 12, v[152:153]
	v_mov_b32_e32 v155, v154
	v_lshl_add_u64 v[136:137], v[132:133], 0, v[136:137]
	v_cvt_pk_bf16_f32 v166, v166, v167
	v_cvt_pk_bf16_f32 v167, v134, v135
	v_cvt_pk_bf16_f32 v168, v168, v169
	v_cvt_pk_bf16_f32 v169, v138, v139
	v_mov_b32_e32 v158, v154
	v_mov_b32_e32 v159, v154
	v_cndmask_b32_e64 v114, 0, 1, s[56:57]
	ds_bpermute_b32 v232, v250, v166
	ds_bpermute_b32 v233, v250, v167
	ds_bpermute_b32 v234, v250, v168
	ds_bpermute_b32 v235, v250, v169
	ds_bpermute_b32 v236, v250, v136
	v_pk_mul_f32 v[138:139], v[122:123], v[158:159]
	v_pk_mul_f32 v[134:135], v[120:121], v[154:155]
	v_pk_mul_f32 v[166:167], v[118:119], v[158:159]
	v_cmp_ne_u32_e64 s[40:41], 1, v114
	s_andn2_b64 vcc, exec, s[56:57]
	v_pk_mul_f32 v[168:169], v[116:117], v[154:155]
	s_waitcnt lgkmcnt(0)
	v_subrev_u32_e32 v236, s82, v236
	global_store_dwordx4 v236, v[232:235], s[82:83] sc1
	s_cbranch_vccnz .LBB0_354
	v_max_f32_e32 v114, v134, v134
	v_max_f32_e32 v134, 0xc2a00000, v114
	v_max_f32_e32 v114, v168, v168
	v_max_f32_e32 v158, 0xc2a00000, v114
	v_mul_f32_e32 v114, 0xbfb8aa3b, v134
	v_exp_f32_e32 v114, v114
	v_mul_f32_e32 v155, 0xbfb8aa3b, v158
	v_exp_f32_e32 v155, v155
	v_max_f32_e32 v135, v135, v135
	v_add_f32_e32 v114, 1.0, v114
	v_rcp_f32_e32 v160, v114
	v_add_f32_e32 v114, 1.0, v155
	v_max_f32_e32 v135, 0xc2a00000, v135
	v_max_f32_e32 v155, v169, v169
	v_max_f32_e32 v159, 0xc2a00000, v155
	v_mul_f32_e32 v155, 0xbfb8aa3b, v135
	v_exp_f32_e32 v155, v155
	v_mul_f32_e32 v161, 0xbfb8aa3b, v159
	v_exp_f32_e32 v169, v161
	v_max_f32_e32 v138, v138, v138
	v_rcp_f32_e32 v168, v114
	v_add_f32_e32 v114, 1.0, v155
	v_max_f32_e32 v138, 0xc2a00000, v138
	v_max_f32_e32 v155, v166, v166
	v_max_f32_e32 v166, 0xc2a00000, v155
	v_mul_f32_e32 v155, 0xbfb8aa3b, v138
	v_exp_f32_e32 v155, v155
	v_rcp_f32_e32 v161, v114
	v_add_f32_e32 v114, 1.0, v169
	v_mul_f32_e32 v169, 0xbfb8aa3b, v166
	v_exp_f32_e32 v171, v169
	v_max_f32_e32 v139, v139, v139
	v_rcp_f32_e32 v169, v114
	v_add_f32_e32 v114, 1.0, v155
	v_max_f32_e32 v139, 0xc2a00000, v139
	v_max_f32_e32 v155, v167, v167
	v_max_f32_e32 v167, 0xc2a00000, v155
	v_mul_f32_e32 v155, 0xbfb8aa3b, v139
	v_rcp_f32_e32 v170, v114
	v_add_f32_e32 v114, 1.0, v171
	v_exp_f32_e32 v155, v155
	v_mul_f32_e32 v171, 0xbfb8aa3b, v167
	v_exp_f32_e32 v179, v171
	v_rcp_f32_e32 v178, v114
	v_add_f32_e32 v114, 1.0, v155
	v_rcp_f32_e32 v171, v114
	v_add_f32_e32 v114, 1.0, v179
	v_rcp_f32_e32 v179, v114
	v_pk_mul_f32 v[134:135], v[134:135], v[160:161]
	v_pk_mul_f32 v[138:139], v[138:139], v[170:171]
	v_pk_mul_f32 v[168:169], v[158:159], v[168:169]
	v_pk_mul_f32 v[166:167], v[166:167], v[178:179]
.LBB0_354:
	v_cvt_pk_bf16_f32 v178, v134, v135
	ds_read_b32 v134, v176 offset:64
	v_cvt_pk_bf16_f32 v179, v138, v139
	v_cvt_pk_bf16_f32 v180, v168, v169
	v_cvt_pk_bf16_f32 v181, v166, v167
	s_and_b64 vcc, exec, s[40:41]
	s_waitcnt lgkmcnt(0)
	v_pk_mul_f32 v[138:139], v[112:113], v[134:135] op_sel_hi:[1,0]
	v_pk_mul_f32 v[168:169], v[110:111], v[134:135] op_sel_hi:[1,0]
	v_pk_mul_f32 v[166:167], v[108:109], v[134:135] op_sel_hi:[1,0]
	v_pk_mul_f32 v[170:171], v[106:107], v[134:135] op_sel_hi:[1,0]
	ds_bpermute_b32 v238, v250, v178
	ds_bpermute_b32 v239, v250, v179
	ds_bpermute_b32 v240, v250, v180
	ds_bpermute_b32 v241, v250, v181
	ds_bpermute_b32 v242, v250, v136
	s_waitcnt lgkmcnt(0)
	v_subrev_u32_e32 v242, s82, v242
	global_store_dwordx4 v242, v[238:241], s[82:83] offset:64 sc1
	s_cbranch_vccnz .LBB0_356
	v_max_f32_e32 v114, v168, v168
	v_max_f32_e32 v136, 0xc2a00000, v114
	v_max_f32_e32 v114, v170, v170
	v_max_f32_e32 v158, 0xc2a00000, v114
	v_mul_f32_e32 v114, 0xbfb8aa3b, v136
	v_exp_f32_e32 v114, v114
	v_mul_f32_e32 v135, 0xbfb8aa3b, v158
	v_exp_f32_e32 v135, v135
	v_add_f32_e32 v114, 1.0, v114
	v_rcp_f32_e32 v160, v114
	v_add_f32_e32 v114, 1.0, v135
	v_max_f32_e32 v135, v169, v169
	v_max_f32_e32 v137, 0xc2a00000, v135
	v_max_f32_e32 v135, v171, v171
	v_max_f32_e32 v159, 0xc2a00000, v135
	v_mul_f32_e32 v135, 0xbfb8aa3b, v137
	v_exp_f32_e32 v135, v135
	v_mul_f32_e32 v155, 0xbfb8aa3b, v159
	v_rcp_f32_e32 v170, v114
	v_exp_f32_e32 v155, v155
	v_add_f32_e32 v114, 1.0, v135
	v_max_f32_e32 v135, v138, v138
	v_max_f32_e32 v138, 0xc2a00000, v135
	v_max_f32_e32 v135, v166, v166
	v_max_f32_e32 v166, 0xc2a00000, v135
	v_mul_f32_e32 v135, 0xbfb8aa3b, v138
	v_exp_f32_e32 v135, v135
	v_rcp_f32_e32 v161, v114
	v_add_f32_e32 v114, 1.0, v155
	v_mul_f32_e32 v155, 0xbfb8aa3b, v166
	v_exp_f32_e32 v155, v155
	v_rcp_f32_e32 v171, v114
	v_add_f32_e32 v114, 1.0, v135
	v_max_f32_e32 v135, v139, v139
	v_max_f32_e32 v139, 0xc2a00000, v135
	v_max_f32_e32 v135, v167, v167
	v_max_f32_e32 v167, 0xc2a00000, v135
	v_mul_f32_e32 v135, 0xbfb8aa3b, v139
	v_rcp_f32_e32 v178, v114
	v_add_f32_e32 v114, 1.0, v155
	v_exp_f32_e32 v135, v135
	v_mul_f32_e32 v155, 0xbfb8aa3b, v167
	v_exp_f32_e32 v155, v155
	v_rcp_f32_e32 v180, v114
	v_add_f32_e32 v114, 1.0, v135
	v_rcp_f32_e32 v179, v114
	v_add_f32_e32 v114, 1.0, v155
	v_rcp_f32_e32 v181, v114
	v_pk_mul_f32 v[168:169], v[136:137], v[160:161]
	v_pk_mul_f32 v[138:139], v[138:139], v[178:179]
	v_pk_mul_f32 v[170:171], v[158:159], v[170:171]
	v_pk_mul_f32 v[166:167], v[166:167], v[180:181]
.LBB0_356:
	v_or_b32_e32 v136, 16, v152
	v_ashrrev_i32_e32 v137, 31, v136
	v_lshlrev_b64 v[136:137], 12, v[136:137]
	v_mov_b32_e32 v135, v134
	v_lshl_add_u64 v[136:137], v[132:133], 0, v[136:137]
	v_cvt_pk_bf16_f32 v168, v168, v169
	v_cvt_pk_bf16_f32 v169, v138, v139
	v_cvt_pk_bf16_f32 v170, v170, v171
	v_cvt_pk_bf16_f32 v171, v166, v167
	v_mov_b32_e32 v158, v134
	v_mov_b32_e32 v159, v134
	ds_bpermute_b32 v244, v250, v168
	ds_bpermute_b32 v245, v250, v169
	ds_bpermute_b32 v246, v250, v170
	ds_bpermute_b32 v247, v250, v171
	ds_bpermute_b32 v248, v250, v136
	v_pk_mul_f32 v[138:139], v[104:105], v[158:159]
	v_pk_mul_f32 v[166:167], v[100:101], v[158:159]
	v_pk_mul_f32 v[168:169], v[102:103], v[134:135]
	s_and_b64 vcc, exec, s[40:41]
	v_pk_mul_f32 v[170:171], v[98:99], v[134:135]
	s_waitcnt lgkmcnt(0)
	v_subrev_u32_e32 v248, s82, v248
	global_store_dwordx4 v248, v[244:247], s[82:83] sc1
	s_cbranch_vccnz .LBB0_358
	v_max_f32_e32 v114, v168, v168
	v_max_f32_e32 v134, 0xc2a00000, v114
	v_max_f32_e32 v114, v170, v170
	v_max_f32_e32 v158, 0xc2a00000, v114
	v_mul_f32_e32 v114, 0xbfb8aa3b, v134
	v_exp_f32_e32 v114, v114
	v_mul_f32_e32 v135, 0xbfb8aa3b, v158
	v_exp_f32_e32 v135, v135
	v_max_f32_e32 v155, v171, v171
	v_add_f32_e32 v114, 1.0, v114
	v_rcp_f32_e32 v160, v114
	v_add_f32_e32 v114, 1.0, v135
	v_max_f32_e32 v135, v169, v169
	v_max_f32_e32 v135, 0xc2a00000, v135
	v_max_f32_e32 v159, 0xc2a00000, v155
	v_mul_f32_e32 v155, 0xbfb8aa3b, v135
	v_exp_f32_e32 v155, v155
	v_mul_f32_e32 v161, 0xbfb8aa3b, v159
	v_exp_f32_e32 v168, v161
	v_max_f32_e32 v138, v138, v138
	v_rcp_f32_e32 v170, v114
	v_add_f32_e32 v114, 1.0, v155
	v_max_f32_e32 v138, 0xc2a00000, v138
	v_max_f32_e32 v155, v166, v166
	v_max_f32_e32 v166, 0xc2a00000, v155
	v_mul_f32_e32 v155, 0xbfb8aa3b, v138
	v_exp_f32_e32 v155, v155
	v_rcp_f32_e32 v161, v114
	v_add_f32_e32 v114, 1.0, v168
	v_mul_f32_e32 v168, 0xbfb8aa3b, v166
	v_exp_f32_e32 v168, v168
	v_max_f32_e32 v139, v139, v139
	v_rcp_f32_e32 v171, v114
	v_add_f32_e32 v114, 1.0, v155
	v_max_f32_e32 v139, 0xc2a00000, v139
	v_max_f32_e32 v155, v167, v167
	v_max_f32_e32 v167, 0xc2a00000, v155
	v_mul_f32_e32 v155, 0xbfb8aa3b, v139
	v_rcp_f32_e32 v178, v114
	v_add_f32_e32 v114, 1.0, v168
	v_exp_f32_e32 v155, v155
	v_mul_f32_e32 v168, 0xbfb8aa3b, v167
	v_exp_f32_e32 v168, v168
	v_rcp_f32_e32 v180, v114
	v_add_f32_e32 v114, 1.0, v155
	v_rcp_f32_e32 v179, v114
	v_add_f32_e32 v114, 1.0, v168
	v_rcp_f32_e32 v181, v114
	v_pk_mul_f32 v[168:169], v[134:135], v[160:161]
	v_pk_mul_f32 v[138:139], v[138:139], v[178:179]
	v_pk_mul_f32 v[170:171], v[158:159], v[170:171]
	v_pk_mul_f32 v[166:167], v[166:167], v[180:181]
.LBB0_358:
	ds_read_b32 v134, v176 offset:128
	v_cvt_pk_bf16_f32 v168, v168, v169
	v_cvt_pk_bf16_f32 v169, v138, v139
	v_cvt_pk_bf16_f32 v170, v170, v171
	v_cvt_pk_bf16_f32 v171, v166, v167
	ds_bpermute_b32 v232, v250, v168
	ds_bpermute_b32 v233, v250, v169
	ds_bpermute_b32 v234, v250, v170
	ds_bpermute_b32 v235, v250, v171
	ds_bpermute_b32 v236, v250, v136
	s_waitcnt lgkmcnt(0)
	v_pk_mul_f32 v[138:139], v[96:97], v[134:135] op_sel_hi:[1,0]
	v_pk_mul_f32 v[166:167], v[92:93], v[134:135] op_sel_hi:[1,0]
	v_pk_mul_f32 v[168:169], v[94:95], v[134:135] op_sel_hi:[1,0]
	s_and_b64 vcc, exec, s[40:41]
	v_pk_mul_f32 v[170:171], v[90:91], v[134:135] op_sel_hi:[1,0]
	s_waitcnt lgkmcnt(0)
	v_subrev_u32_e32 v236, s82, v236
	global_store_dwordx4 v236, v[232:235], s[82:83] offset:64 sc1
	s_cbranch_vccnz .LBB0_360
	v_max_f32_e32 v114, v168, v168
	v_max_f32_e32 v136, 0xc2a00000, v114
	v_max_f32_e32 v114, v170, v170
	v_max_f32_e32 v158, 0xc2a00000, v114
	v_mul_f32_e32 v114, 0xbfb8aa3b, v136
	v_exp_f32_e32 v114, v114
	v_mul_f32_e32 v135, 0xbfb8aa3b, v158
	v_exp_f32_e32 v135, v135
	v_add_f32_e32 v114, 1.0, v114
	v_rcp_f32_e32 v160, v114
	v_add_f32_e32 v114, 1.0, v135
	v_max_f32_e32 v135, v169, v169
	v_max_f32_e32 v137, 0xc2a00000, v135
	v_max_f32_e32 v135, v171, v171
	v_max_f32_e32 v159, 0xc2a00000, v135
	v_mul_f32_e32 v135, 0xbfb8aa3b, v137
	v_exp_f32_e32 v135, v135
	v_mul_f32_e32 v155, 0xbfb8aa3b, v159
	v_rcp_f32_e32 v170, v114
	v_exp_f32_e32 v155, v155
	v_add_f32_e32 v114, 1.0, v135
	v_max_f32_e32 v135, v138, v138
	v_max_f32_e32 v138, 0xc2a00000, v135
	v_max_f32_e32 v135, v166, v166
	v_max_f32_e32 v166, 0xc2a00000, v135
	v_mul_f32_e32 v135, 0xbfb8aa3b, v138
	v_exp_f32_e32 v135, v135
	v_rcp_f32_e32 v161, v114
	v_add_f32_e32 v114, 1.0, v155
	v_mul_f32_e32 v155, 0xbfb8aa3b, v166
	v_exp_f32_e32 v155, v155
	v_rcp_f32_e32 v171, v114
	v_add_f32_e32 v114, 1.0, v135
	v_max_f32_e32 v135, v139, v139
	v_max_f32_e32 v139, 0xc2a00000, v135
	v_max_f32_e32 v135, v167, v167
	v_max_f32_e32 v167, 0xc2a00000, v135
	v_mul_f32_e32 v135, 0xbfb8aa3b, v139
	v_rcp_f32_e32 v178, v114
	v_add_f32_e32 v114, 1.0, v155
	v_exp_f32_e32 v135, v135
	v_mul_f32_e32 v155, 0xbfb8aa3b, v167
	v_exp_f32_e32 v155, v155
	v_rcp_f32_e32 v180, v114
	v_add_f32_e32 v114, 1.0, v135
	v_rcp_f32_e32 v179, v114
	v_add_f32_e32 v114, 1.0, v155
	v_rcp_f32_e32 v181, v114
	v_pk_mul_f32 v[168:169], v[136:137], v[160:161]
	v_pk_mul_f32 v[138:139], v[138:139], v[178:179]
	v_pk_mul_f32 v[170:171], v[158:159], v[170:171]
	v_pk_mul_f32 v[166:167], v[166:167], v[180:181]
.LBB0_360:
	v_or_b32_e32 v136, 32, v152
	v_ashrrev_i32_e32 v137, 31, v136
	v_lshlrev_b64 v[136:137], 12, v[136:137]
	v_mov_b32_e32 v135, v134
	v_lshl_add_u64 v[136:137], v[132:133], 0, v[136:137]
	v_cvt_pk_bf16_f32 v168, v168, v169
	v_cvt_pk_bf16_f32 v169, v138, v139
	v_cvt_pk_bf16_f32 v170, v170, v171
	v_cvt_pk_bf16_f32 v171, v166, v167
	v_mov_b32_e32 v158, v134
	v_mov_b32_e32 v159, v134
	ds_bpermute_b32 v238, v250, v168
	ds_bpermute_b32 v239, v250, v169
	ds_bpermute_b32 v240, v250, v170
	ds_bpermute_b32 v241, v250, v171
	ds_bpermute_b32 v242, v250, v136
	v_pk_mul_f32 v[138:139], v[88:89], v[158:159]
	v_pk_mul_f32 v[166:167], v[84:85], v[158:159]
	v_pk_mul_f32 v[168:169], v[86:87], v[134:135]
	s_and_b64 vcc, exec, s[40:41]
	v_pk_mul_f32 v[170:171], v[82:83], v[134:135]
	s_waitcnt lgkmcnt(0)
	v_subrev_u32_e32 v242, s82, v242
	global_store_dwordx4 v242, v[238:241], s[82:83] sc1
	s_cbranch_vccnz .LBB0_362
	v_max_f32_e32 v114, v168, v168
	v_max_f32_e32 v134, 0xc2a00000, v114
	v_max_f32_e32 v114, v170, v170
	v_max_f32_e32 v158, 0xc2a00000, v114
	v_mul_f32_e32 v114, 0xbfb8aa3b, v134
	v_exp_f32_e32 v114, v114
	v_mul_f32_e32 v135, 0xbfb8aa3b, v158
	v_exp_f32_e32 v135, v135
	v_max_f32_e32 v155, v171, v171
	v_add_f32_e32 v114, 1.0, v114
	v_rcp_f32_e32 v160, v114
	v_add_f32_e32 v114, 1.0, v135
	v_max_f32_e32 v135, v169, v169
	v_max_f32_e32 v135, 0xc2a00000, v135
	v_max_f32_e32 v159, 0xc2a00000, v155
	v_mul_f32_e32 v155, 0xbfb8aa3b, v135
	v_exp_f32_e32 v155, v155
	v_mul_f32_e32 v161, 0xbfb8aa3b, v159
	v_exp_f32_e32 v168, v161
	v_max_f32_e32 v138, v138, v138
	v_rcp_f32_e32 v170, v114
	v_add_f32_e32 v114, 1.0, v155
	v_max_f32_e32 v138, 0xc2a00000, v138
	v_max_f32_e32 v155, v166, v166
	v_max_f32_e32 v166, 0xc2a00000, v155
	v_mul_f32_e32 v155, 0xbfb8aa3b, v138
	v_exp_f32_e32 v155, v155
	v_rcp_f32_e32 v161, v114
	v_add_f32_e32 v114, 1.0, v168
	v_mul_f32_e32 v168, 0xbfb8aa3b, v166
	v_exp_f32_e32 v168, v168
	v_max_f32_e32 v139, v139, v139
	v_rcp_f32_e32 v171, v114
	v_add_f32_e32 v114, 1.0, v155
	v_max_f32_e32 v139, 0xc2a00000, v139
	v_max_f32_e32 v155, v167, v167
	v_max_f32_e32 v167, 0xc2a00000, v155
	v_mul_f32_e32 v155, 0xbfb8aa3b, v139
	v_rcp_f32_e32 v178, v114
	v_add_f32_e32 v114, 1.0, v168
	v_exp_f32_e32 v155, v155
	v_mul_f32_e32 v168, 0xbfb8aa3b, v167
	v_exp_f32_e32 v168, v168
	v_rcp_f32_e32 v180, v114
	v_add_f32_e32 v114, 1.0, v155
	v_rcp_f32_e32 v179, v114
	v_add_f32_e32 v114, 1.0, v168
	v_rcp_f32_e32 v181, v114
	v_pk_mul_f32 v[168:169], v[134:135], v[160:161]
	v_pk_mul_f32 v[138:139], v[138:139], v[178:179]
	v_pk_mul_f32 v[170:171], v[158:159], v[170:171]
	v_pk_mul_f32 v[166:167], v[166:167], v[180:181]
.LBB0_362:
	ds_read_b32 v134, v176 offset:192
	v_cvt_pk_bf16_f32 v168, v168, v169
	v_cvt_pk_bf16_f32 v169, v138, v139
	v_cvt_pk_bf16_f32 v170, v170, v171
	v_cvt_pk_bf16_f32 v171, v166, v167
	ds_bpermute_b32 v244, v250, v168
	ds_bpermute_b32 v245, v250, v169
	ds_bpermute_b32 v246, v250, v170
	ds_bpermute_b32 v247, v250, v171
	ds_bpermute_b32 v248, v250, v136
	s_waitcnt lgkmcnt(0)
	v_pk_mul_f32 v[138:139], v[80:81], v[134:135] op_sel_hi:[1,0]
	v_pk_mul_f32 v[166:167], v[76:77], v[134:135] op_sel_hi:[1,0]
	v_pk_mul_f32 v[168:169], v[78:79], v[134:135] op_sel_hi:[1,0]
	s_and_b64 vcc, exec, s[40:41]
	v_pk_mul_f32 v[170:171], v[74:75], v[134:135] op_sel_hi:[1,0]
	s_waitcnt lgkmcnt(0)
	v_subrev_u32_e32 v248, s82, v248
	global_store_dwordx4 v248, v[244:247], s[82:83] offset:64 sc1
	s_cbranch_vccnz .LBB0_364
	v_max_f32_e32 v114, v168, v168
	v_max_f32_e32 v136, 0xc2a00000, v114
	v_max_f32_e32 v114, v170, v170
	v_max_f32_e32 v158, 0xc2a00000, v114
	v_mul_f32_e32 v114, 0xbfb8aa3b, v136
	v_exp_f32_e32 v114, v114
	v_mul_f32_e32 v135, 0xbfb8aa3b, v158
	v_exp_f32_e32 v135, v135
	v_add_f32_e32 v114, 1.0, v114
	v_rcp_f32_e32 v160, v114
	v_add_f32_e32 v114, 1.0, v135
	v_max_f32_e32 v135, v169, v169
	v_max_f32_e32 v137, 0xc2a00000, v135
	v_max_f32_e32 v135, v171, v171
	v_max_f32_e32 v159, 0xc2a00000, v135
	v_mul_f32_e32 v135, 0xbfb8aa3b, v137
	v_exp_f32_e32 v135, v135
	v_mul_f32_e32 v155, 0xbfb8aa3b, v159
	v_rcp_f32_e32 v170, v114
	v_exp_f32_e32 v155, v155
	v_add_f32_e32 v114, 1.0, v135
	v_max_f32_e32 v135, v138, v138
	v_max_f32_e32 v138, 0xc2a00000, v135
	v_max_f32_e32 v135, v166, v166
	v_max_f32_e32 v166, 0xc2a00000, v135
	v_mul_f32_e32 v135, 0xbfb8aa3b, v138
	v_exp_f32_e32 v135, v135
	v_rcp_f32_e32 v161, v114
	v_add_f32_e32 v114, 1.0, v155
	v_mul_f32_e32 v155, 0xbfb8aa3b, v166
	v_exp_f32_e32 v155, v155
	v_rcp_f32_e32 v171, v114
	v_add_f32_e32 v114, 1.0, v135
	v_max_f32_e32 v135, v139, v139
	v_max_f32_e32 v139, 0xc2a00000, v135
	v_max_f32_e32 v135, v167, v167
	v_max_f32_e32 v167, 0xc2a00000, v135
	v_mul_f32_e32 v135, 0xbfb8aa3b, v139
	v_rcp_f32_e32 v178, v114
	v_add_f32_e32 v114, 1.0, v155
	v_exp_f32_e32 v135, v135
	v_mul_f32_e32 v155, 0xbfb8aa3b, v167
	v_exp_f32_e32 v155, v155
	v_rcp_f32_e32 v180, v114
	v_add_f32_e32 v114, 1.0, v135
	v_rcp_f32_e32 v179, v114
	v_add_f32_e32 v114, 1.0, v155
	v_rcp_f32_e32 v181, v114
	v_pk_mul_f32 v[168:169], v[136:137], v[160:161]
	v_pk_mul_f32 v[138:139], v[138:139], v[178:179]
	v_pk_mul_f32 v[170:171], v[158:159], v[170:171]
	v_pk_mul_f32 v[166:167], v[166:167], v[180:181]
.LBB0_364:
	v_or_b32_e32 v136, 48, v152
	v_ashrrev_i32_e32 v137, 31, v136
	v_lshlrev_b64 v[136:137], 12, v[136:137]
	v_mov_b32_e32 v135, v134
	v_lshl_add_u64 v[136:137], v[132:133], 0, v[136:137]
	v_cvt_pk_bf16_f32 v168, v168, v169
	v_cvt_pk_bf16_f32 v169, v138, v139
	v_cvt_pk_bf16_f32 v170, v170, v171
	v_cvt_pk_bf16_f32 v171, v166, v167
	v_mov_b32_e32 v158, v134
	v_mov_b32_e32 v159, v134
	ds_bpermute_b32 v232, v250, v168
	ds_bpermute_b32 v233, v250, v169
	ds_bpermute_b32 v234, v250, v170
	ds_bpermute_b32 v235, v250, v171
	ds_bpermute_b32 v236, v250, v136
	v_pk_mul_f32 v[138:139], v[72:73], v[158:159]
	v_pk_mul_f32 v[166:167], v[68:69], v[158:159]
	v_pk_mul_f32 v[168:169], v[70:71], v[134:135]
	s_and_b64 vcc, exec, s[40:41]
	v_pk_mul_f32 v[170:171], v[66:67], v[134:135]
	s_waitcnt lgkmcnt(0)
	v_subrev_u32_e32 v236, s82, v236
	global_store_dwordx4 v236, v[232:235], s[82:83] sc1
	s_cbranch_vccnz .LBB0_366
	v_max_f32_e32 v114, v168, v168
	v_max_f32_e32 v134, 0xc2a00000, v114
	v_max_f32_e32 v114, v170, v170
	v_max_f32_e32 v158, 0xc2a00000, v114
	v_mul_f32_e32 v114, 0xbfb8aa3b, v134
	v_exp_f32_e32 v114, v114
	v_mul_f32_e32 v135, 0xbfb8aa3b, v158
	v_exp_f32_e32 v135, v135
	v_max_f32_e32 v155, v171, v171
	v_add_f32_e32 v114, 1.0, v114
	v_rcp_f32_e32 v160, v114
	v_add_f32_e32 v114, 1.0, v135
	v_max_f32_e32 v135, v169, v169
	v_max_f32_e32 v135, 0xc2a00000, v135
	v_max_f32_e32 v159, 0xc2a00000, v155
	v_mul_f32_e32 v155, 0xbfb8aa3b, v135
	v_exp_f32_e32 v155, v155
	v_mul_f32_e32 v161, 0xbfb8aa3b, v159
	v_exp_f32_e32 v168, v161
	v_max_f32_e32 v138, v138, v138
	v_rcp_f32_e32 v170, v114
	v_add_f32_e32 v114, 1.0, v155
	v_max_f32_e32 v138, 0xc2a00000, v138
	v_max_f32_e32 v155, v166, v166
	v_max_f32_e32 v166, 0xc2a00000, v155
	v_mul_f32_e32 v155, 0xbfb8aa3b, v138
	v_exp_f32_e32 v155, v155
	v_rcp_f32_e32 v161, v114
	v_add_f32_e32 v114, 1.0, v168
	v_mul_f32_e32 v168, 0xbfb8aa3b, v166
	v_exp_f32_e32 v168, v168
	v_max_f32_e32 v139, v139, v139
	v_rcp_f32_e32 v171, v114
	v_add_f32_e32 v114, 1.0, v155
	v_max_f32_e32 v139, 0xc2a00000, v139
	v_max_f32_e32 v155, v167, v167
	v_max_f32_e32 v167, 0xc2a00000, v155
	v_mul_f32_e32 v155, 0xbfb8aa3b, v139
	v_rcp_f32_e32 v178, v114
	v_add_f32_e32 v114, 1.0, v168
	v_exp_f32_e32 v155, v155
	v_mul_f32_e32 v168, 0xbfb8aa3b, v167
	v_exp_f32_e32 v168, v168
	v_rcp_f32_e32 v180, v114
	v_add_f32_e32 v114, 1.0, v155
	v_rcp_f32_e32 v179, v114
	v_add_f32_e32 v114, 1.0, v168
	v_rcp_f32_e32 v181, v114
	v_pk_mul_f32 v[168:169], v[134:135], v[160:161]
	v_pk_mul_f32 v[138:139], v[138:139], v[178:179]
	v_pk_mul_f32 v[170:171], v[158:159], v[170:171]
	v_pk_mul_f32 v[166:167], v[166:167], v[180:181]
.LBB0_366:
	ds_read_b32 v134, v176 offset:512
	v_cvt_pk_bf16_f32 v168, v168, v169
	v_cvt_pk_bf16_f32 v169, v138, v139
	v_cvt_pk_bf16_f32 v170, v170, v171
	v_cvt_pk_bf16_f32 v171, v166, v167
	ds_bpermute_b32 v238, v250, v168
	ds_bpermute_b32 v239, v250, v169
	ds_bpermute_b32 v240, v250, v170
	ds_bpermute_b32 v241, v250, v171
	ds_bpermute_b32 v242, v250, v136
	s_waitcnt lgkmcnt(0)
	v_pk_mul_f32 v[138:139], v[64:65], v[134:135] op_sel_hi:[1,0]
	v_pk_mul_f32 v[166:167], v[60:61], v[134:135] op_sel_hi:[1,0]
	v_pk_mul_f32 v[168:169], v[62:63], v[134:135] op_sel_hi:[1,0]
	s_and_b64 vcc, exec, s[40:41]
	v_pk_mul_f32 v[170:171], v[58:59], v[134:135] op_sel_hi:[1,0]
	s_waitcnt lgkmcnt(0)
	v_subrev_u32_e32 v242, s82, v242
	global_store_dwordx4 v242, v[238:241], s[82:83] offset:64 sc1
	s_cbranch_vccnz .LBB0_368
	v_max_f32_e32 v114, v168, v168
	v_max_f32_e32 v136, 0xc2a00000, v114
	v_max_f32_e32 v114, v170, v170
	v_max_f32_e32 v158, 0xc2a00000, v114
	v_mul_f32_e32 v114, 0xbfb8aa3b, v136
	v_exp_f32_e32 v114, v114
	v_mul_f32_e32 v135, 0xbfb8aa3b, v158
	v_exp_f32_e32 v135, v135
	v_add_f32_e32 v114, 1.0, v114
	v_rcp_f32_e32 v160, v114
	v_add_f32_e32 v114, 1.0, v135
	v_max_f32_e32 v135, v169, v169
	v_max_f32_e32 v137, 0xc2a00000, v135
	v_max_f32_e32 v135, v171, v171
	v_max_f32_e32 v159, 0xc2a00000, v135
	v_mul_f32_e32 v135, 0xbfb8aa3b, v137
	v_exp_f32_e32 v135, v135
	v_mul_f32_e32 v155, 0xbfb8aa3b, v159
	v_rcp_f32_e32 v170, v114
	v_exp_f32_e32 v155, v155
	v_add_f32_e32 v114, 1.0, v135
	v_max_f32_e32 v135, v138, v138
	v_max_f32_e32 v138, 0xc2a00000, v135
	v_max_f32_e32 v135, v166, v166
	v_max_f32_e32 v166, 0xc2a00000, v135
	v_mul_f32_e32 v135, 0xbfb8aa3b, v138
	v_exp_f32_e32 v135, v135
	v_rcp_f32_e32 v161, v114
	v_add_f32_e32 v114, 1.0, v155
	v_mul_f32_e32 v155, 0xbfb8aa3b, v166
	v_exp_f32_e32 v155, v155
	v_rcp_f32_e32 v171, v114
	v_add_f32_e32 v114, 1.0, v135
	v_max_f32_e32 v135, v139, v139
	v_max_f32_e32 v139, 0xc2a00000, v135
	v_max_f32_e32 v135, v167, v167
	v_max_f32_e32 v167, 0xc2a00000, v135
	v_mul_f32_e32 v135, 0xbfb8aa3b, v139
	v_rcp_f32_e32 v178, v114
	v_add_f32_e32 v114, 1.0, v155
	v_exp_f32_e32 v135, v135
	v_mul_f32_e32 v155, 0xbfb8aa3b, v167
	v_exp_f32_e32 v155, v155
	v_rcp_f32_e32 v180, v114
	v_add_f32_e32 v114, 1.0, v135
	v_rcp_f32_e32 v179, v114
	v_add_f32_e32 v114, 1.0, v155
	v_rcp_f32_e32 v181, v114
	v_pk_mul_f32 v[168:169], v[136:137], v[160:161]
	v_pk_mul_f32 v[138:139], v[138:139], v[178:179]
	v_pk_mul_f32 v[170:171], v[158:159], v[170:171]
	v_pk_mul_f32 v[166:167], v[166:167], v[180:181]
.LBB0_368:
	v_lshlrev_b64 v[136:137], 12, v[152:153]
	v_lshl_add_u64 v[136:137], v[132:133], 0, v[136:137]
	s_mov_b32 s14, 0x80000
	v_cvt_pk_bf16_f32 v168, v168, v169
	v_cvt_pk_bf16_f32 v169, v138, v139
	v_add_co_u32_e32 v138, vcc, s14, v136
	v_mov_b32_e32 v135, v134
	v_cvt_pk_bf16_f32 v170, v170, v171
	v_cvt_pk_bf16_f32 v171, v166, v167
	s_nop 0
	v_addc_co_u32_e32 v139, vcc, 0, v137, vcc
	v_mov_b32_e32 v158, v134
	v_mov_b32_e32 v159, v134
	ds_bpermute_b32 v244, v250, v168
	ds_bpermute_b32 v245, v250, v169
	ds_bpermute_b32 v246, v250, v170
	ds_bpermute_b32 v247, v250, v171
	ds_bpermute_b32 v248, v250, v138
	v_pk_mul_f32 v[138:139], v[56:57], v[158:159]
	v_pk_mul_f32 v[166:167], v[52:53], v[158:159]
	v_pk_mul_f32 v[168:169], v[54:55], v[134:135]
	s_and_b64 vcc, exec, s[40:41]
	v_pk_mul_f32 v[170:171], v[50:51], v[134:135]
	s_waitcnt lgkmcnt(0)
	v_subrev_u32_e32 v248, s82, v248
	global_store_dwordx4 v248, v[244:247], s[82:83] sc1
	s_cbranch_vccnz .LBB0_370
	v_max_f32_e32 v114, v168, v168
	v_max_f32_e32 v134, 0xc2a00000, v114
	v_max_f32_e32 v114, v170, v170
	v_max_f32_e32 v158, 0xc2a00000, v114
	v_mul_f32_e32 v114, 0xbfb8aa3b, v134
	v_exp_f32_e32 v114, v114
	v_mul_f32_e32 v135, 0xbfb8aa3b, v158
	v_exp_f32_e32 v135, v135
	v_max_f32_e32 v155, v171, v171
	v_add_f32_e32 v114, 1.0, v114
	v_rcp_f32_e32 v160, v114
	v_add_f32_e32 v114, 1.0, v135
	v_max_f32_e32 v135, v169, v169
	v_max_f32_e32 v135, 0xc2a00000, v135
	v_max_f32_e32 v159, 0xc2a00000, v155
	v_mul_f32_e32 v155, 0xbfb8aa3b, v135
	v_exp_f32_e32 v155, v155
	v_mul_f32_e32 v161, 0xbfb8aa3b, v159
	v_exp_f32_e32 v168, v161
	v_max_f32_e32 v138, v138, v138
	v_rcp_f32_e32 v170, v114
	v_add_f32_e32 v114, 1.0, v155
	v_max_f32_e32 v138, 0xc2a00000, v138
	v_max_f32_e32 v155, v166, v166
	v_max_f32_e32 v166, 0xc2a00000, v155
	v_mul_f32_e32 v155, 0xbfb8aa3b, v138
	v_exp_f32_e32 v155, v155
	v_rcp_f32_e32 v161, v114
	v_add_f32_e32 v114, 1.0, v168
	v_mul_f32_e32 v168, 0xbfb8aa3b, v166
	v_exp_f32_e32 v168, v168
	v_max_f32_e32 v139, v139, v139
	v_rcp_f32_e32 v171, v114
	v_add_f32_e32 v114, 1.0, v155
	v_max_f32_e32 v139, 0xc2a00000, v139
	v_max_f32_e32 v155, v167, v167
	v_max_f32_e32 v167, 0xc2a00000, v155
	v_mul_f32_e32 v155, 0xbfb8aa3b, v139
	v_rcp_f32_e32 v178, v114
	v_add_f32_e32 v114, 1.0, v168
	v_exp_f32_e32 v155, v155
	v_mul_f32_e32 v168, 0xbfb8aa3b, v167
	v_exp_f32_e32 v168, v168
	v_rcp_f32_e32 v180, v114
	v_add_f32_e32 v114, 1.0, v155
	v_rcp_f32_e32 v179, v114
	v_add_f32_e32 v114, 1.0, v168
	v_rcp_f32_e32 v181, v114
	v_pk_mul_f32 v[168:169], v[134:135], v[160:161]
	v_pk_mul_f32 v[138:139], v[138:139], v[178:179]
	v_pk_mul_f32 v[170:171], v[158:159], v[170:171]
	v_pk_mul_f32 v[166:167], v[166:167], v[180:181]
.LBB0_370:
	ds_read_b32 v134, v176 offset:576
	s_mov_b64 s[14:15], 0x80000
	v_lshl_add_u64 v[158:159], v[136:137], 0, s[14:15]
	v_cvt_pk_bf16_f32 v137, v138, v139
	v_cvt_pk_bf16_f32 v138, v170, v171
	v_cvt_pk_bf16_f32 v139, v166, v167
	v_cvt_pk_bf16_f32 v136, v168, v169
	ds_bpermute_b32 v232, v250, v136
	ds_bpermute_b32 v233, v250, v137
	ds_bpermute_b32 v234, v250, v138
	ds_bpermute_b32 v235, v250, v139
	ds_bpermute_b32 v236, v250, v158
	s_waitcnt lgkmcnt(0)
	v_pk_mul_f32 v[168:169], v[46:47], v[134:135] op_sel_hi:[1,0]
	v_pk_mul_f32 v[166:167], v[44:45], v[134:135] op_sel_hi:[1,0]
	v_pk_mul_f32 v[138:139], v[48:49], v[134:135] op_sel_hi:[1,0]
	s_and_b64 vcc, exec, s[40:41]
	v_pk_mul_f32 v[170:171], v[42:43], v[134:135] op_sel_hi:[1,0]
	s_waitcnt lgkmcnt(0)
	v_subrev_u32_e32 v236, s82, v236
	global_store_dwordx4 v236, v[232:235], s[82:83] offset:64 sc1
	s_cbranch_vccnz .LBB0_372
	v_max_f32_e32 v114, v168, v168
	v_max_f32_e32 v136, 0xc2a00000, v114
	v_max_f32_e32 v114, v170, v170
	v_max_f32_e32 v158, 0xc2a00000, v114
	v_mul_f32_e32 v114, 0xbfb8aa3b, v136
	v_exp_f32_e32 v114, v114
	v_mul_f32_e32 v135, 0xbfb8aa3b, v158
	v_exp_f32_e32 v135, v135
	v_add_f32_e32 v114, 1.0, v114
	v_rcp_f32_e32 v160, v114
	v_add_f32_e32 v114, 1.0, v135
	v_max_f32_e32 v135, v169, v169
	v_max_f32_e32 v137, 0xc2a00000, v135
	v_max_f32_e32 v135, v171, v171
	v_max_f32_e32 v159, 0xc2a00000, v135
	v_mul_f32_e32 v135, 0xbfb8aa3b, v137
	v_exp_f32_e32 v135, v135
	v_mul_f32_e32 v155, 0xbfb8aa3b, v159
	v_rcp_f32_e32 v170, v114
	v_exp_f32_e32 v155, v155
	v_add_f32_e32 v114, 1.0, v135
	v_max_f32_e32 v135, v138, v138
	v_max_f32_e32 v138, 0xc2a00000, v135
	v_max_f32_e32 v135, v166, v166
	v_max_f32_e32 v166, 0xc2a00000, v135
	v_mul_f32_e32 v135, 0xbfb8aa3b, v138
	v_exp_f32_e32 v135, v135
	v_rcp_f32_e32 v161, v114
	v_add_f32_e32 v114, 1.0, v155
	v_mul_f32_e32 v155, 0xbfb8aa3b, v166
	v_exp_f32_e32 v155, v155
	v_rcp_f32_e32 v171, v114
	v_add_f32_e32 v114, 1.0, v135
	v_max_f32_e32 v135, v139, v139
	v_max_f32_e32 v139, 0xc2a00000, v135
	v_max_f32_e32 v135, v167, v167
	v_max_f32_e32 v167, 0xc2a00000, v135
	v_mul_f32_e32 v135, 0xbfb8aa3b, v139
	v_rcp_f32_e32 v178, v114
	v_add_f32_e32 v114, 1.0, v155
	v_exp_f32_e32 v135, v135
	v_mul_f32_e32 v155, 0xbfb8aa3b, v167
	v_exp_f32_e32 v155, v155
	v_rcp_f32_e32 v180, v114
	v_add_f32_e32 v114, 1.0, v135
	v_rcp_f32_e32 v179, v114
	v_add_f32_e32 v114, 1.0, v155
	v_rcp_f32_e32 v181, v114
	v_pk_mul_f32 v[168:169], v[136:137], v[160:161]
	v_pk_mul_f32 v[138:139], v[138:139], v[178:179]
	v_pk_mul_f32 v[170:171], v[158:159], v[170:171]
	v_pk_mul_f32 v[166:167], v[166:167], v[180:181]
.LBB0_372:
	v_lshlrev_b64 v[136:137], 12, v[152:153]
	v_lshl_add_u64 v[136:137], v[132:133], 0, v[136:137]
	s_mov_b32 s14, 0x90000
	v_cvt_pk_bf16_f32 v168, v168, v169
	v_cvt_pk_bf16_f32 v169, v138, v139
	v_add_co_u32_e32 v138, vcc, s14, v136
	v_mov_b32_e32 v135, v134
	v_cvt_pk_bf16_f32 v170, v170, v171
	v_cvt_pk_bf16_f32 v171, v166, v167
	s_nop 0
	v_addc_co_u32_e32 v139, vcc, 0, v137, vcc
	v_mov_b32_e32 v158, v134
	v_mov_b32_e32 v159, v134
	ds_bpermute_b32 v238, v250, v168
	ds_bpermute_b32 v239, v250, v169
	ds_bpermute_b32 v240, v250, v170
	ds_bpermute_b32 v241, v250, v171
	ds_bpermute_b32 v242, v250, v138
	v_pk_mul_f32 v[138:139], v[40:41], v[158:159]
	v_pk_mul_f32 v[166:167], v[36:37], v[158:159]
	v_pk_mul_f32 v[168:169], v[38:39], v[134:135]
	s_and_b64 vcc, exec, s[40:41]
	v_pk_mul_f32 v[170:171], v[34:35], v[134:135]
	s_waitcnt lgkmcnt(0)
	v_subrev_u32_e32 v242, s82, v242
	global_store_dwordx4 v242, v[238:241], s[82:83] sc1
	s_cbranch_vccnz .LBB0_374
	v_max_f32_e32 v114, v168, v168
	v_max_f32_e32 v134, 0xc2a00000, v114
	v_max_f32_e32 v114, v170, v170
	v_max_f32_e32 v158, 0xc2a00000, v114
	v_mul_f32_e32 v114, 0xbfb8aa3b, v134
	v_exp_f32_e32 v114, v114
	v_mul_f32_e32 v135, 0xbfb8aa3b, v158
	v_exp_f32_e32 v135, v135
	v_max_f32_e32 v155, v171, v171
	v_add_f32_e32 v114, 1.0, v114
	v_rcp_f32_e32 v160, v114
	v_add_f32_e32 v114, 1.0, v135
	v_max_f32_e32 v135, v169, v169
	v_max_f32_e32 v135, 0xc2a00000, v135
	v_max_f32_e32 v159, 0xc2a00000, v155
	v_mul_f32_e32 v155, 0xbfb8aa3b, v135
	v_exp_f32_e32 v155, v155
	v_mul_f32_e32 v161, 0xbfb8aa3b, v159
	v_exp_f32_e32 v168, v161
	v_max_f32_e32 v138, v138, v138
	v_rcp_f32_e32 v170, v114
	v_add_f32_e32 v114, 1.0, v155
	v_max_f32_e32 v138, 0xc2a00000, v138
	v_max_f32_e32 v155, v166, v166
	v_max_f32_e32 v166, 0xc2a00000, v155
	v_mul_f32_e32 v155, 0xbfb8aa3b, v138
	v_exp_f32_e32 v155, v155
	v_rcp_f32_e32 v161, v114
	v_add_f32_e32 v114, 1.0, v168
	v_mul_f32_e32 v168, 0xbfb8aa3b, v166
	v_exp_f32_e32 v168, v168
	v_max_f32_e32 v139, v139, v139
	v_rcp_f32_e32 v171, v114
	v_add_f32_e32 v114, 1.0, v155
	v_max_f32_e32 v139, 0xc2a00000, v139
	v_max_f32_e32 v155, v167, v167
	v_max_f32_e32 v167, 0xc2a00000, v155
	v_mul_f32_e32 v155, 0xbfb8aa3b, v139
	v_rcp_f32_e32 v178, v114
	v_add_f32_e32 v114, 1.0, v168
	v_exp_f32_e32 v155, v155
	v_mul_f32_e32 v168, 0xbfb8aa3b, v167
	v_exp_f32_e32 v168, v168
	v_rcp_f32_e32 v180, v114
	v_add_f32_e32 v114, 1.0, v155
	v_rcp_f32_e32 v179, v114
	v_add_f32_e32 v114, 1.0, v168
	v_rcp_f32_e32 v181, v114
	v_pk_mul_f32 v[168:169], v[134:135], v[160:161]
	v_pk_mul_f32 v[138:139], v[138:139], v[178:179]
	v_pk_mul_f32 v[170:171], v[158:159], v[170:171]
	v_pk_mul_f32 v[166:167], v[166:167], v[180:181]
.LBB0_374:
	ds_read_b32 v134, v176 offset:640
	s_mov_b64 s[14:15], 0x90000
	v_lshl_add_u64 v[158:159], v[136:137], 0, s[14:15]
	v_cvt_pk_bf16_f32 v137, v138, v139
	v_cvt_pk_bf16_f32 v138, v170, v171
	v_cvt_pk_bf16_f32 v139, v166, v167
	v_cvt_pk_bf16_f32 v136, v168, v169
	ds_bpermute_b32 v244, v250, v136
	ds_bpermute_b32 v245, v250, v137
	ds_bpermute_b32 v246, v250, v138
	ds_bpermute_b32 v247, v250, v139
	ds_bpermute_b32 v248, v250, v158
	s_waitcnt lgkmcnt(0)
	v_pk_mul_f32 v[168:169], v[30:31], v[134:135] op_sel_hi:[1,0]
	v_pk_mul_f32 v[166:167], v[28:29], v[134:135] op_sel_hi:[1,0]
	v_pk_mul_f32 v[138:139], v[32:33], v[134:135] op_sel_hi:[1,0]
	s_and_b64 vcc, exec, s[40:41]
	v_pk_mul_f32 v[170:171], v[26:27], v[134:135] op_sel_hi:[1,0]
	s_waitcnt lgkmcnt(0)
	v_subrev_u32_e32 v248, s82, v248
	global_store_dwordx4 v248, v[244:247], s[82:83] offset:64 sc1
	s_cbranch_vccnz .LBB0_376
	v_max_f32_e32 v114, v168, v168
	v_max_f32_e32 v136, 0xc2a00000, v114
	v_max_f32_e32 v114, v170, v170
	v_max_f32_e32 v158, 0xc2a00000, v114
	v_mul_f32_e32 v114, 0xbfb8aa3b, v136
	v_exp_f32_e32 v114, v114
	v_mul_f32_e32 v135, 0xbfb8aa3b, v158
	v_exp_f32_e32 v135, v135
	v_add_f32_e32 v114, 1.0, v114
	v_rcp_f32_e32 v160, v114
	v_add_f32_e32 v114, 1.0, v135
	v_max_f32_e32 v135, v169, v169
	v_max_f32_e32 v137, 0xc2a00000, v135
	v_max_f32_e32 v135, v171, v171
	v_max_f32_e32 v159, 0xc2a00000, v135
	v_mul_f32_e32 v135, 0xbfb8aa3b, v137
	v_exp_f32_e32 v135, v135
	v_mul_f32_e32 v155, 0xbfb8aa3b, v159
	v_rcp_f32_e32 v170, v114
	v_exp_f32_e32 v155, v155
	v_add_f32_e32 v114, 1.0, v135
	v_max_f32_e32 v135, v138, v138
	v_max_f32_e32 v138, 0xc2a00000, v135
	v_max_f32_e32 v135, v166, v166
	v_max_f32_e32 v166, 0xc2a00000, v135
	v_mul_f32_e32 v135, 0xbfb8aa3b, v138
	v_exp_f32_e32 v135, v135
	v_rcp_f32_e32 v161, v114
	v_add_f32_e32 v114, 1.0, v155
	v_mul_f32_e32 v155, 0xbfb8aa3b, v166
	v_exp_f32_e32 v155, v155
	v_rcp_f32_e32 v171, v114
	v_add_f32_e32 v114, 1.0, v135
	v_max_f32_e32 v135, v139, v139
	v_max_f32_e32 v139, 0xc2a00000, v135
	v_max_f32_e32 v135, v167, v167
	v_max_f32_e32 v167, 0xc2a00000, v135
	v_mul_f32_e32 v135, 0xbfb8aa3b, v139
	v_rcp_f32_e32 v178, v114
	v_add_f32_e32 v114, 1.0, v155
	v_exp_f32_e32 v135, v135
	v_mul_f32_e32 v155, 0xbfb8aa3b, v167
	v_exp_f32_e32 v155, v155
	v_rcp_f32_e32 v180, v114
	v_add_f32_e32 v114, 1.0, v135
	v_rcp_f32_e32 v179, v114
	v_add_f32_e32 v114, 1.0, v155
	v_rcp_f32_e32 v181, v114
	v_pk_mul_f32 v[168:169], v[136:137], v[160:161]
	v_pk_mul_f32 v[138:139], v[138:139], v[178:179]
	v_pk_mul_f32 v[170:171], v[158:159], v[170:171]
	v_pk_mul_f32 v[166:167], v[166:167], v[180:181]
.LBB0_376:
	v_lshlrev_b64 v[136:137], 12, v[152:153]
	v_lshl_add_u64 v[136:137], v[132:133], 0, v[136:137]
	s_mov_b32 s14, 0xa0000
	v_cvt_pk_bf16_f32 v168, v168, v169
	v_cvt_pk_bf16_f32 v169, v138, v139
	v_add_co_u32_e32 v138, vcc, s14, v136
	v_mov_b32_e32 v135, v134
	v_cvt_pk_bf16_f32 v170, v170, v171
	v_cvt_pk_bf16_f32 v171, v166, v167
	s_nop 0
	v_addc_co_u32_e32 v139, vcc, 0, v137, vcc
	v_mov_b32_e32 v158, v134
	v_mov_b32_e32 v159, v134
	ds_bpermute_b32 v232, v250, v168
	ds_bpermute_b32 v233, v250, v169
	ds_bpermute_b32 v234, v250, v170
	ds_bpermute_b32 v235, v250, v171
	ds_bpermute_b32 v236, v250, v138
	v_pk_mul_f32 v[138:139], v[24:25], v[158:159]
	v_pk_mul_f32 v[166:167], v[20:21], v[158:159]
	v_pk_mul_f32 v[168:169], v[22:23], v[134:135]
	s_and_b64 vcc, exec, s[40:41]
	v_pk_mul_f32 v[170:171], v[18:19], v[134:135]
	s_waitcnt lgkmcnt(0)
	v_subrev_u32_e32 v236, s82, v236
	global_store_dwordx4 v236, v[232:235], s[82:83] sc1
	s_cbranch_vccnz .LBB0_378
	v_max_f32_e32 v114, v168, v168
	v_max_f32_e32 v134, 0xc2a00000, v114
	v_max_f32_e32 v114, v170, v170
	v_max_f32_e32 v158, 0xc2a00000, v114
	v_mul_f32_e32 v114, 0xbfb8aa3b, v134
	v_exp_f32_e32 v114, v114
	v_mul_f32_e32 v135, 0xbfb8aa3b, v158
	v_exp_f32_e32 v135, v135
	v_max_f32_e32 v155, v171, v171
	v_add_f32_e32 v114, 1.0, v114
	v_rcp_f32_e32 v160, v114
	v_add_f32_e32 v114, 1.0, v135
	v_max_f32_e32 v135, v169, v169
	v_max_f32_e32 v135, 0xc2a00000, v135
	v_max_f32_e32 v159, 0xc2a00000, v155
	v_mul_f32_e32 v155, 0xbfb8aa3b, v135
	v_exp_f32_e32 v155, v155
	v_mul_f32_e32 v161, 0xbfb8aa3b, v159
	v_exp_f32_e32 v168, v161
	v_max_f32_e32 v138, v138, v138
	v_rcp_f32_e32 v170, v114
	v_add_f32_e32 v114, 1.0, v155
	v_max_f32_e32 v138, 0xc2a00000, v138
	v_max_f32_e32 v155, v166, v166
	v_max_f32_e32 v166, 0xc2a00000, v155
	v_mul_f32_e32 v155, 0xbfb8aa3b, v138
	v_exp_f32_e32 v155, v155
	v_rcp_f32_e32 v161, v114
	v_add_f32_e32 v114, 1.0, v168
	v_mul_f32_e32 v168, 0xbfb8aa3b, v166
	v_exp_f32_e32 v168, v168
	v_max_f32_e32 v139, v139, v139
	v_rcp_f32_e32 v171, v114
	v_add_f32_e32 v114, 1.0, v155
	v_max_f32_e32 v139, 0xc2a00000, v139
	v_max_f32_e32 v155, v167, v167
	v_max_f32_e32 v167, 0xc2a00000, v155
	v_mul_f32_e32 v155, 0xbfb8aa3b, v139
	v_rcp_f32_e32 v178, v114
	v_add_f32_e32 v114, 1.0, v168
	v_exp_f32_e32 v155, v155
	v_mul_f32_e32 v168, 0xbfb8aa3b, v167
	v_exp_f32_e32 v168, v168
	v_rcp_f32_e32 v180, v114
	v_add_f32_e32 v114, 1.0, v155
	v_rcp_f32_e32 v179, v114
	v_add_f32_e32 v114, 1.0, v168
	v_rcp_f32_e32 v181, v114
	v_pk_mul_f32 v[168:169], v[134:135], v[160:161]
	v_pk_mul_f32 v[138:139], v[138:139], v[178:179]
	v_pk_mul_f32 v[170:171], v[158:159], v[170:171]
	v_pk_mul_f32 v[166:167], v[166:167], v[180:181]
.LBB0_378:
	ds_read_b32 v134, v176 offset:704
	s_mov_b64 s[14:15], 0xa0000
	v_lshl_add_u64 v[158:159], v[136:137], 0, s[14:15]
	v_cvt_pk_bf16_f32 v136, v168, v169
	v_cvt_pk_bf16_f32 v137, v138, v139
	v_cvt_pk_bf16_f32 v138, v170, v171
	v_cvt_pk_bf16_f32 v139, v166, v167
	ds_bpermute_b32 v238, v250, v136
	ds_bpermute_b32 v239, v250, v137
	ds_bpermute_b32 v240, v250, v138
	ds_bpermute_b32 v241, v250, v139
	ds_bpermute_b32 v242, v250, v158
	s_waitcnt lgkmcnt(0)
	v_pk_mul_f32 v[166:167], v[14:15], v[134:135] op_sel_hi:[1,0]
	s_and_b64 vcc, exec, s[40:41]
	v_pk_mul_f32 v[136:137], v[16:17], v[134:135] op_sel_hi:[1,0]
	v_pk_mul_f32 v[138:139], v[12:13], v[134:135] op_sel_hi:[1,0]
	v_pk_mul_f32 v[168:169], v[10:11], v[134:135] op_sel_hi:[1,0]
	s_waitcnt lgkmcnt(0)
	v_subrev_u32_e32 v242, s82, v242
	global_store_dwordx4 v242, v[238:241], s[82:83] offset:64 sc1
	s_cbranch_vccnz .LBB0_380
	v_max_f32_e32 v114, v166, v166
	v_max_f32_e32 v158, 0xc2a00000, v114
	v_max_f32_e32 v114, v168, v168
	v_max_f32_e32 v160, 0xc2a00000, v114
	v_mul_f32_e32 v114, 0xbfb8aa3b, v158
	v_exp_f32_e32 v114, v114
	v_mul_f32_e32 v135, 0xbfb8aa3b, v160
	v_exp_f32_e32 v135, v135
	v_add_f32_e32 v114, 1.0, v114
	v_rcp_f32_e32 v166, v114
	v_add_f32_e32 v114, 1.0, v135
	v_max_f32_e32 v135, v167, v167
	v_max_f32_e32 v159, 0xc2a00000, v135
	v_max_f32_e32 v135, v169, v169
	v_max_f32_e32 v161, 0xc2a00000, v135
	v_mul_f32_e32 v135, 0xbfb8aa3b, v159
	v_exp_f32_e32 v135, v135
	v_mul_f32_e32 v155, 0xbfb8aa3b, v161
	v_rcp_f32_e32 v168, v114
	v_exp_f32_e32 v155, v155
	v_add_f32_e32 v114, 1.0, v135
	v_max_f32_e32 v135, v136, v136
	v_max_f32_e32 v136, 0xc2a00000, v135
	v_max_f32_e32 v135, v138, v138
	v_max_f32_e32 v138, 0xc2a00000, v135
	v_mul_f32_e32 v135, 0xbfb8aa3b, v136
	v_exp_f32_e32 v135, v135
	v_rcp_f32_e32 v167, v114
	v_add_f32_e32 v114, 1.0, v155
	v_mul_f32_e32 v155, 0xbfb8aa3b, v138
	v_exp_f32_e32 v155, v155
	v_rcp_f32_e32 v169, v114
	v_add_f32_e32 v114, 1.0, v135
	v_max_f32_e32 v135, v137, v137
	v_max_f32_e32 v137, 0xc2a00000, v135
	v_max_f32_e32 v135, v139, v139
	v_max_f32_e32 v139, 0xc2a00000, v135
	v_mul_f32_e32 v135, 0xbfb8aa3b, v137
	v_rcp_f32_e32 v170, v114
	v_add_f32_e32 v114, 1.0, v155
	v_exp_f32_e32 v135, v135
	v_mul_f32_e32 v155, 0xbfb8aa3b, v139
	v_exp_f32_e32 v155, v155
	v_rcp_f32_e32 v178, v114
	v_add_f32_e32 v114, 1.0, v135
	v_rcp_f32_e32 v171, v114
	v_add_f32_e32 v114, 1.0, v155
	v_rcp_f32_e32 v179, v114
	v_pk_mul_f32 v[166:167], v[158:159], v[166:167]
	v_pk_mul_f32 v[136:137], v[136:137], v[170:171]
	v_pk_mul_f32 v[168:169], v[160:161], v[168:169]
	v_pk_mul_f32 v[138:139], v[138:139], v[178:179]
.LBB0_380:
	v_lshlrev_b64 v[158:159], 12, v[152:153]
	v_lshl_add_u64 v[132:133], v[132:133], 0, v[158:159]
	s_mov_b32 s14, 0xb0000
	v_cvt_pk_bf16_f32 v166, v166, v167
	v_cvt_pk_bf16_f32 v167, v136, v137
	v_add_co_u32_e32 v136, vcc, s14, v132
	v_mov_b32_e32 v135, v134
	s_nop 0
	v_addc_co_u32_e32 v137, vcc, 0, v133, vcc
	v_cvt_pk_bf16_f32 v168, v168, v169
	v_cvt_pk_bf16_f32 v169, v138, v139
	ds_bpermute_b32 v244, v250, v166
	ds_bpermute_b32 v245, v250, v167
	ds_bpermute_b32 v246, v250, v168
	ds_bpermute_b32 v247, v250, v169
	ds_bpermute_b32 v248, v250, v136
	v_mov_b32_e32 v136, v134
	v_mov_b32_e32 v137, v134
	v_pk_mul_f32 v[138:139], v[8:9], v[136:137]
	v_pk_mul_f32 v[168:169], v[6:7], v[134:135]
	v_pk_mul_f32 v[166:167], v[4:5], v[136:137]
	s_and_b64 vcc, exec, s[40:41]
	v_pk_mul_f32 v[134:135], v[2:3], v[134:135]
	s_waitcnt lgkmcnt(0)
	v_subrev_u32_e32 v248, s82, v248
	global_store_dwordx4 v248, v[244:247], s[82:83] sc1
	s_cbranch_vccnz .LBB0_382
	v_max_f32_e32 v114, v168, v168
	v_max_f32_e32 v136, 0xc2a00000, v114
	v_max_f32_e32 v114, v134, v134
	v_max_f32_e32 v134, 0xc2a00000, v114
	v_mul_f32_e32 v114, 0xbfb8aa3b, v136
	v_exp_f32_e32 v114, v114
	v_mul_f32_e32 v137, 0xbfb8aa3b, v134
	v_exp_f32_e32 v137, v137
	v_max_f32_e32 v135, v135, v135
	v_add_f32_e32 v114, 1.0, v114
	v_rcp_f32_e32 v158, v114
	v_add_f32_e32 v114, 1.0, v137
	v_max_f32_e32 v137, v169, v169
	v_max_f32_e32 v137, 0xc2a00000, v137
	v_mul_f32_e32 v153, 0xbfb8aa3b, v137
	v_exp_f32_e32 v153, v153
	v_max_f32_e32 v135, 0xc2a00000, v135
	v_mul_f32_e32 v155, 0xbfb8aa3b, v135
	v_exp_f32_e32 v155, v155
	v_max_f32_e32 v138, v138, v138
	v_rcp_f32_e32 v160, v114
	v_add_f32_e32 v114, 1.0, v153
	v_max_f32_e32 v138, 0xc2a00000, v138
	v_max_f32_e32 v153, v166, v166
	v_max_f32_e32 v166, 0xc2a00000, v153
	v_mul_f32_e32 v153, 0xbfb8aa3b, v138
	v_exp_f32_e32 v153, v153
	v_rcp_f32_e32 v159, v114
	v_add_f32_e32 v114, 1.0, v155
	v_mul_f32_e32 v155, 0xbfb8aa3b, v166
	v_exp_f32_e32 v155, v155
	v_max_f32_e32 v139, v139, v139
	v_rcp_f32_e32 v161, v114
	v_add_f32_e32 v114, 1.0, v153
	v_max_f32_e32 v139, 0xc2a00000, v139
	v_max_f32_e32 v153, v167, v167
	v_max_f32_e32 v167, 0xc2a00000, v153
	v_mul_f32_e32 v153, 0xbfb8aa3b, v139
	v_rcp_f32_e32 v170, v114
	v_add_f32_e32 v114, 1.0, v155
	v_exp_f32_e32 v153, v153
	v_mul_f32_e32 v155, 0xbfb8aa3b, v167
	v_exp_f32_e32 v155, v155
	v_rcp_f32_e32 v178, v114
	v_add_f32_e32 v114, 1.0, v153
	v_rcp_f32_e32 v171, v114
	v_add_f32_e32 v114, 1.0, v155
	v_rcp_f32_e32 v179, v114
	v_pk_mul_f32 v[168:169], v[136:137], v[158:159]
	v_pk_mul_f32 v[138:139], v[138:139], v[170:171]
	v_pk_mul_f32 v[134:135], v[134:135], v[160:161]
	v_pk_mul_f32 v[166:167], v[166:167], v[178:179]

.LBB0_383:
	s_andn2_b64 vcc, exec, s[38:39]
	s_mov_b64 s[28:29], -1
	ds_bpermute_b32 v232, v250, v132
	ds_bpermute_b32 v233, v250, v133
	ds_bpermute_b32 v234, v250, v134
	ds_bpermute_b32 v235, v250, v135
	ds_bpermute_b32 v236, v250, v136
	s_waitcnt lgkmcnt(0)
	v_subrev_u32_e32 v236, s82, v236
	global_store_dwordx4 v236, v[232:235], s[82:83] offset:64 sc1
	s_cbranch_vccnz .LBB0_338
	s_branch .LBB0_386
.LBB0_384:
	s_and_b64 vcc, exec, s[40:41]
	s_cbranch_vccz .LBB0_383
	v_lshlrev_b32_e32 v155, 2, v177
	global_load_dwordx4 v[136:139], v155, s[44:45]
	global_load_dwordx4 v[132:135], v155, s[44:45] offset:16
	s_waitcnt lgkmcnt(0)
	v_mul_f32_e32 v160, v128, v154
	v_mul_f32_e32 v161, v129, v154
	v_mul_f32_e32 v166, v130, v154
	v_mul_f32_e32 v167, v131, v154
	v_mul_f32_e32 v168, v124, v154
	v_mul_f32_e32 v169, v125, v154
	v_mul_f32_e32 v170, v126, v154
	v_mul_f32_e32 v171, v127, v154
	global_load_dwordx4 v[124:127], v155, s[44:45] offset:144
	global_load_dwordx4 v[128:131], v155, s[44:45] offset:128
	v_ashrrev_i32_e32 v153, 31, v152
	v_lshlrev_b64 v[158:159], 12, v[152:153]
	v_max_f32_e32 v153, 0xc2a00000, v160
	v_max_f32_e32 v155, 0xc2a00000, v161
	v_max_f32_e32 v160, 0xc2a00000, v166
	v_max_f32_e32 v161, 0xc2a00000, v167
	v_max_f32_e32 v166, 0xc2a00000, v168
	v_max_f32_e32 v167, 0xc2a00000, v169
	v_max_f32_e32 v168, 0xc2a00000, v170
	v_max_f32_e32 v169, 0xc2a00000, v171
	v_mul_f32_e32 v153, 0xbfb8aa3b, v153
	v_mul_f32_e32 v155, 0xbfb8aa3b, v155
	v_mul_f32_e32 v168, 0xbfb8aa3b, v168
	v_mul_f32_e32 v169, 0xbfb8aa3b, v169
	v_exp_f32_e32 v153, v153
	v_exp_f32_e32 v155, v155
	v_mul_f32_e32 v160, 0xbfb8aa3b, v160
	v_mul_f32_e32 v161, 0xbfb8aa3b, v161
	v_exp_f32_e32 v168, v168
	v_exp_f32_e32 v169, v169
	v_exp_f32_e32 v160, v160
	v_exp_f32_e32 v161, v161
	v_mul_f32_e32 v120, v120, v154
	v_max_f32_e32 v120, 0xc2a00000, v120
	v_add_f32_e32 v153, 1.0, v153
	v_add_f32_e32 v155, 1.0, v155
	v_mul_f32_e32 v121, v121, v154
	v_lshlrev_b32_e32 v114, 1, v177
	v_mul_f32_e32 v166, 0xbfb8aa3b, v166
	v_mul_f32_e32 v167, 0xbfb8aa3b, v167
	v_lshl_add_u64 v[158:159], s[42:43], 0, v[158:159]
	v_add_f32_e32 v168, 1.0, v168
	v_add_f32_e32 v169, 1.0, v169
	v_rcp_f32_e32 v153, v153
	v_rcp_f32_e32 v181, v155
	v_mul_f32_e32 v120, 0xbfb8aa3b, v120
	v_max_f32_e32 v121, 0xc2a00000, v121
	v_exp_f32_e32 v170, v166
	v_exp_f32_e32 v171, v167
	v_lshl_add_u64 v[166:167], v[158:159], 0, v[114:115]
	v_add_f32_e32 v158, 1.0, v160
	v_add_f32_e32 v159, 1.0, v161
	v_rcp_f32_e32 v168, v168
	v_rcp_f32_e32 v182, v169
	v_exp_f32_e32 v120, v120
	v_mul_f32_e32 v121, 0xbfb8aa3b, v121
	v_rcp_f32_e32 v158, v158
	v_rcp_f32_e32 v159, v159
	v_exp_f32_e32 v121, v121
	v_add_f32_e32 v120, 1.0, v120
	v_rcp_f32_e32 v120, v120
	v_mul_f32_e32 v116, v116, v154
	v_add_f32_e32 v121, 1.0, v121
	v_rcp_f32_e32 v121, v121
	v_add_f32_e32 v160, 1.0, v170
	v_add_f32_e32 v161, 1.0, v171
	v_max_f32_e32 v116, 0xc2a00000, v116
	v_mul_f32_e32 v117, v117, v154
	v_rcp_f32_e32 v160, v160
	v_rcp_f32_e32 v161, v161
	v_mul_f32_e32 v116, 0xbfb8aa3b, v116
	v_max_f32_e32 v117, 0xc2a00000, v117
	v_exp_f32_e32 v116, v116
	v_mul_f32_e32 v117, 0xbfb8aa3b, v117
	v_exp_f32_e32 v117, v117
	s_mov_b64 s[14:15], 0x80000
	v_add_f32_e32 v116, 1.0, v116
	v_rcp_f32_e32 v116, v116
	v_add_f32_e32 v117, 1.0, v117
	s_waitcnt vmcnt(0)
	v_sub_f32_e32 v180, 1.0, v136
	v_sub_f32_e32 v179, 1.0, v137
	v_sub_f32_e32 v169, 1.0, v134
	v_sub_f32_e32 v155, 1.0, v135
	v_fma_f32 v153, v180, v153, v136
	v_fma_f32 v181, v179, v181, v137
	v_sub_f32_e32 v178, 1.0, v138
	v_sub_f32_e32 v177, 1.0, v139
	v_fma_f32 v168, v169, v168, v134
	v_fma_f32 v182, v155, v182, v135
	v_log_f32_e32 v153, v153
	v_log_f32_e32 v181, v181
	v_fma_f32 v158, v178, v158, v138
	v_fma_f32 v159, v177, v159, v139
	v_log_f32_e32 v168, v168
	v_log_f32_e32 v182, v182
	v_log_f32_e32 v158, v158
	v_log_f32_e32 v159, v159
	v_cvt_pk_f16_f32 v194, v153, v181
	v_sub_f32_e32 v153, 1.0, v128
	v_cvt_pk_f16_f32 v197, v168, v182
	v_fma_f32 v120, v153, v120, v128
	v_sub_f32_e32 v168, 1.0, v129
	v_cvt_pk_f16_f32 v195, v158, v159
	v_log_f32_e32 v158, v120
	v_fma_f32 v120, v168, v121, v129
	v_log_f32_e32 v159, v120
	v_mul_f32_e32 v120, v122, v154
	v_max_f32_e32 v120, 0xc2a00000, v120
	v_mul_f32_e32 v121, v123, v154
	v_mul_f32_e32 v120, 0xbfb8aa3b, v120
	v_max_f32_e32 v121, 0xc2a00000, v121
	v_exp_f32_e32 v120, v120
	v_mul_f32_e32 v121, 0xbfb8aa3b, v121
	v_exp_f32_e32 v122, v121
	v_sub_f32_e32 v171, 1.0, v132
	v_sub_f32_e32 v170, 1.0, v133
	v_add_f32_e32 v120, 1.0, v120
	v_fma_f32 v160, v171, v160, v132
	v_fma_f32 v161, v170, v161, v133
	v_rcp_f32_e32 v120, v120
	v_add_f32_e32 v122, 1.0, v122
	v_log_f32_e32 v160, v160
	v_log_f32_e32 v161, v161
	v_rcp_f32_e32 v123, v122
	v_sub_f32_e32 v121, 1.0, v130
	v_rcp_f32_e32 v117, v117
	v_fma_f32 v120, v121, v120, v130
	v_sub_f32_e32 v122, 1.0, v131
	v_cvt_pk_f16_f32 v196, v160, v161
	v_log_f32_e32 v160, v120
	v_fma_f32 v120, v122, v123, v131
	v_sub_f32_e32 v123, 1.0, v124
	v_log_f32_e32 v161, v120
	v_fma_f32 v116, v123, v116, v124
	v_sub_f32_e32 v120, 1.0, v125
	v_log_f32_e32 v181, v116
	v_fma_f32 v116, v120, v117, v125
	v_log_f32_e32 v182, v116
	v_mul_f32_e32 v116, v118, v154
	v_max_f32_e32 v116, 0xc2a00000, v116
	v_mul_f32_e32 v117, v119, v154
	v_mul_f32_e32 v116, 0xbfb8aa3b, v116
	v_max_f32_e32 v117, 0xc2a00000, v117
	v_exp_f32_e32 v116, v116
	v_mul_f32_e32 v117, 0xbfb8aa3b, v117
	v_exp_f32_e32 v117, v117
	v_sub_f32_e32 v118, 1.0, v126
	v_add_f32_e32 v116, 1.0, v116
	v_rcp_f32_e32 v116, v116
	v_add_f32_e32 v117, 1.0, v117
	v_rcp_f32_e32 v117, v117
	v_sub_f32_e32 v119, 1.0, v127
	v_fma_f32 v116, v118, v116, v126
	v_log_f32_e32 v154, v116
	v_fma_f32 v116, v119, v117, v127
	v_log_f32_e32 v183, v116
	ds_read2_b32 v[116:117], v176 offset0:16 offset1:32
	ds_bpermute_b32 v238, v250, v194
	ds_bpermute_b32 v239, v250, v195
	ds_bpermute_b32 v240, v250, v196
	ds_bpermute_b32 v241, v250, v197
	ds_bpermute_b32 v242, v250, v166
	s_waitcnt lgkmcnt(0)
	v_mul_f32_e32 v106, v106, v116
	v_max_f32_e32 v106, 0xc2a00000, v106
	v_mul_f32_e32 v106, 0xbfb8aa3b, v106
	v_exp_f32_e32 v106, v106
	v_mul_f32_e32 v110, v110, v116
	v_max_f32_e32 v110, 0xc2a00000, v110
	v_mul_f32_e32 v111, v111, v116
	v_mul_f32_e32 v110, 0xbfb8aa3b, v110
	v_max_f32_e32 v111, 0xc2a00000, v111
	v_mul_f32_e32 v107, v107, v116
	v_exp_f32_e32 v110, v110
	v_mul_f32_e32 v111, 0xbfb8aa3b, v111
	v_add_f32_e32 v106, 1.0, v106
	v_max_f32_e32 v107, 0xc2a00000, v107
	v_exp_f32_e32 v111, v111
	v_rcp_f32_e32 v106, v106
	v_mul_f32_e32 v107, 0xbfb8aa3b, v107
	v_exp_f32_e32 v107, v107
	v_cvt_pk_f16_f32 v194, v158, v159
	v_or_b32_e32 v158, 16, v152
	v_add_f32_e32 v110, 1.0, v110
	v_mul_f32_e32 v112, v112, v116
	v_mul_f32_e32 v113, v113, v116
	v_cvt_pk_f16_f32 v197, v154, v183
	v_ashrrev_i32_e32 v159, 31, v158
	v_rcp_f32_e32 v154, v110
	v_add_f32_e32 v110, 1.0, v111
	v_max_f32_e32 v112, 0xc2a00000, v112
	v_max_f32_e32 v113, 0xc2a00000, v113
	v_fma_f32 v106, v171, v106, v132
	v_cvt_pk_f16_f32 v195, v160, v161
	v_rcp_f32_e32 v160, v110
	v_lshlrev_b64 v[110:111], 12, v[158:159]
	v_mul_f32_e32 v112, 0xbfb8aa3b, v112
	v_mul_f32_e32 v113, 0xbfb8aa3b, v113
	v_log_f32_e32 v159, v106
	v_add_f32_e32 v106, 1.0, v107
	v_mul_f32_e32 v107, v108, v116
	v_exp_f32_e32 v112, v112
	v_exp_f32_e32 v113, v113
	v_max_f32_e32 v107, 0xc2a00000, v107
	v_mul_f32_e32 v108, v109, v116
	v_mul_f32_e32 v107, 0xbfb8aa3b, v107
	v_max_f32_e32 v108, 0xc2a00000, v108
	v_exp_f32_e32 v107, v107
	v_mul_f32_e32 v108, 0xbfb8aa3b, v108
	v_exp_f32_e32 v108, v108
	v_add_f32_e32 v112, 1.0, v112
	v_add_f32_e32 v113, 1.0, v113
	v_rcp_f32_e32 v112, v112
	v_rcp_f32_e32 v113, v113
	v_mul_f32_e32 v98, v98, v116
	v_rcp_f32_e32 v106, v106
	v_add_f32_e32 v107, 1.0, v107
	v_max_f32_e32 v98, 0xc2a00000, v98
	v_rcp_f32_e32 v107, v107
	v_add_f32_e32 v108, 1.0, v108
	v_mul_f32_e32 v98, 0xbfb8aa3b, v98
	v_rcp_f32_e32 v108, v108
	v_exp_f32_e32 v98, v98
	v_fma_f32 v112, v178, v112, v138
	v_fma_f32 v113, v177, v113, v139
	v_log_f32_e32 v112, v112
	v_log_f32_e32 v113, v113
	v_fma_f32 v106, v170, v106, v133
	v_log_f32_e32 v109, v106
	v_fma_f32 v106, v169, v107, v134
	v_mul_f32_e32 v102, v102, v116
	v_mul_f32_e32 v99, v99, v116
	v_fma_f32 v154, v180, v154, v136
	v_fma_f32 v158, v179, v160, v137
	v_log_f32_e32 v160, v106
	v_fma_f32 v106, v155, v108, v135
	v_max_f32_e32 v102, 0xc2a00000, v102
	v_add_f32_e32 v98, 1.0, v98
	v_max_f32_e32 v99, 0xc2a00000, v99
	v_log_f32_e32 v154, v154
	v_log_f32_e32 v158, v158
	v_log_f32_e32 v161, v106
	v_mul_f32_e32 v102, 0xbfb8aa3b, v102
	v_rcp_f32_e32 v98, v98
	v_mul_f32_e32 v99, 0xbfb8aa3b, v99
	v_cvt_pk_f16_f32 v107, v112, v113
	v_exp_f32_e32 v112, v102
	v_mul_f32_e32 v102, v103, v116
	v_exp_f32_e32 v99, v99
	v_max_f32_e32 v102, 0xc2a00000, v102
	v_lshl_add_u64 v[110:111], s[42:43], 0, v[110:111]
	v_mul_f32_e32 v102, 0xbfb8aa3b, v102
	v_cvt_pk_f16_f32 v106, v154, v158
	v_cvt_pk_f16_f32 v108, v159, v109
	v_cvt_pk_f16_f32 v109, v160, v161
	v_exp_f32_e32 v113, v102
	v_lshl_add_u64 v[102:103], v[110:111], 0, v[114:115]
	v_fma_f32 v98, v123, v98, v124
	ds_bpermute_b32 v244, v250, v106
	ds_bpermute_b32 v245, v250, v107
	ds_bpermute_b32 v246, v250, v108
	ds_bpermute_b32 v247, v250, v109
	ds_bpermute_b32 v248, v250, v102
	v_mul_f32_e32 v104, v104, v116
	v_mul_f32_e32 v105, v105, v116
	v_log_f32_e32 v108, v98
	v_add_f32_e32 v98, 1.0, v99
	v_mul_f32_e32 v99, v100, v116
	v_max_f32_e32 v99, 0xc2a00000, v99
	v_mul_f32_e32 v100, v101, v116
	v_max_f32_e32 v104, 0xc2a00000, v104
	v_max_f32_e32 v105, 0xc2a00000, v105
	v_mul_f32_e32 v99, 0xbfb8aa3b, v99
	v_max_f32_e32 v100, 0xc2a00000, v100
	v_mul_f32_e32 v104, 0xbfb8aa3b, v104
	v_mul_f32_e32 v105, 0xbfb8aa3b, v105
	v_exp_f32_e32 v99, v99
	v_mul_f32_e32 v100, 0xbfb8aa3b, v100
	v_exp_f32_e32 v104, v104
	v_exp_f32_e32 v105, v105
	v_exp_f32_e32 v100, v100
	v_rcp_f32_e32 v98, v98
	v_add_f32_e32 v99, 1.0, v99
	v_add_f32_e32 v110, 1.0, v112
	v_add_f32_e32 v111, 1.0, v113
	v_add_f32_e32 v104, 1.0, v104
	v_add_f32_e32 v105, 1.0, v105
	v_rcp_f32_e32 v99, v99
	v_add_f32_e32 v100, 1.0, v100
	v_rcp_f32_e32 v110, v110
	v_rcp_f32_e32 v111, v111
	v_rcp_f32_e32 v104, v104
	v_rcp_f32_e32 v105, v105
	v_rcp_f32_e32 v100, v100
	v_mul_f32_e32 v90, v90, v117
	v_fma_f32 v98, v120, v98, v125
	v_mul_f32_e32 v94, v94, v117
	v_max_f32_e32 v90, 0xc2a00000, v90
	v_log_f32_e32 v101, v98
	v_fma_f32 v98, v118, v99, v126
	v_max_f32_e32 v94, 0xc2a00000, v94
	v_mul_f32_e32 v90, 0xbfb8aa3b, v90
	v_fma_f32 v106, v153, v110, v128
	v_fma_f32 v107, v168, v111, v129
	v_fma_f32 v104, v121, v104, v130
	v_fma_f32 v105, v122, v105, v131
	v_log_f32_e32 v109, v98
	v_fma_f32 v98, v119, v100, v127
	v_mul_f32_e32 v94, 0xbfb8aa3b, v94
	v_exp_f32_e32 v90, v90
	v_log_f32_e32 v106, v106
	v_log_f32_e32 v107, v107
	v_log_f32_e32 v104, v104
	v_log_f32_e32 v105, v105
	v_log_f32_e32 v110, v98
	v_exp_f32_e32 v94, v94
	v_mul_f32_e32 v95, v95, v117
	v_max_f32_e32 v95, 0xc2a00000, v95
	v_mul_f32_e32 v91, v91, v117
	v_mul_f32_e32 v95, 0xbfb8aa3b, v95
	v_add_f32_e32 v90, 1.0, v90
	v_max_f32_e32 v91, 0xc2a00000, v91
	v_cvt_pk_f16_f32 v98, v106, v107
	v_cvt_pk_f16_f32 v99, v104, v105
	v_cvt_pk_f16_f32 v100, v108, v101
	v_cvt_pk_f16_f32 v101, v109, v110
	v_exp_f32_e32 v95, v95
	v_add_f32_e32 v94, 1.0, v94
	v_rcp_f32_e32 v90, v90
	v_mul_f32_e32 v91, 0xbfb8aa3b, v91
	s_waitcnt lgkmcnt(5)
	v_subrev_u32_e32 v242, s82, v242
	global_store_dwordx4 v242, v[238:241], s[82:83] sc1
	ds_bpermute_b32 v232, v250, v98
	ds_bpermute_b32 v233, v250, v99
	ds_bpermute_b32 v234, v250, v100
	ds_bpermute_b32 v235, v250, v101
	ds_bpermute_b32 v236, v250, v102
	v_exp_f32_e32 v91, v91
	v_fma_f32 v90, v171, v90, v132
	v_rcp_f32_e32 v100, v94
	v_or_b32_e32 v98, 32, v152
	v_ashrrev_i32_e32 v99, 31, v98
	v_add_f32_e32 v94, 1.0, v95
	v_rcp_f32_e32 v101, v94
	v_lshlrev_b64 v[94:95], 12, v[98:99]
	v_fma_f32 v98, v180, v100, v136
	v_log_f32_e32 v100, v90
	v_add_f32_e32 v90, 1.0, v91
	v_mul_f32_e32 v91, v92, v117
	v_mul_f32_e32 v96, v96, v117
	v_mul_f32_e32 v97, v97, v117
	v_max_f32_e32 v91, 0xc2a00000, v91
	v_mul_f32_e32 v92, v93, v117
	v_max_f32_e32 v96, 0xc2a00000, v96
	v_max_f32_e32 v97, 0xc2a00000, v97
	v_mul_f32_e32 v91, 0xbfb8aa3b, v91
	v_max_f32_e32 v92, 0xc2a00000, v92
	v_mul_f32_e32 v96, 0xbfb8aa3b, v96
	v_mul_f32_e32 v97, 0xbfb8aa3b, v97
	v_exp_f32_e32 v91, v91
	v_mul_f32_e32 v92, 0xbfb8aa3b, v92
	v_exp_f32_e32 v96, v96
	v_exp_f32_e32 v97, v97
	v_exp_f32_e32 v92, v92
	v_mul_f32_e32 v82, v82, v117
	v_rcp_f32_e32 v90, v90
	v_add_f32_e32 v91, 1.0, v91
	v_max_f32_e32 v82, 0xc2a00000, v82
	v_add_f32_e32 v96, 1.0, v96
	v_add_f32_e32 v97, 1.0, v97
	v_rcp_f32_e32 v91, v91
	v_add_f32_e32 v92, 1.0, v92
	v_mul_f32_e32 v82, 0xbfb8aa3b, v82
	v_rcp_f32_e32 v96, v96
	v_rcp_f32_e32 v97, v97
	v_rcp_f32_e32 v92, v92
	v_exp_f32_e32 v82, v82
	v_fma_f32 v90, v170, v90, v133
	v_log_f32_e32 v93, v90
	v_fma_f32 v90, v169, v91, v134
	v_mul_f32_e32 v83, v83, v117
	v_fma_f32 v99, v179, v101, v137
	v_fma_f32 v96, v178, v96, v138
	v_fma_f32 v97, v177, v97, v139
	v_log_f32_e32 v101, v90
	v_fma_f32 v90, v155, v92, v135
	v_add_f32_e32 v82, 1.0, v82
	v_max_f32_e32 v83, 0xc2a00000, v83
	v_log_f32_e32 v98, v98
	v_log_f32_e32 v99, v99
	v_log_f32_e32 v96, v96
	v_log_f32_e32 v97, v97
	v_log_f32_e32 v102, v90
	v_rcp_f32_e32 v82, v82
	v_mul_f32_e32 v83, 0xbfb8aa3b, v83
	v_exp_f32_e32 v83, v83
	v_lshl_add_u64 v[94:95], s[42:43], 0, v[94:95]
	v_cvt_pk_f16_f32 v90, v98, v99
	v_cvt_pk_f16_f32 v91, v96, v97
	v_cvt_pk_f16_f32 v92, v100, v93
	v_cvt_pk_f16_f32 v93, v101, v102
	v_lshl_add_u64 v[94:95], v[94:95], 0, v[114:115]
	v_fma_f32 v82, v123, v82, v124
	s_waitcnt lgkmcnt(5)
	v_subrev_u32_e32 v248, s82, v248
	global_store_dwordx4 v248, v[244:247], s[82:83] sc1
	ds_bpermute_b32 v238, v250, v90
	ds_bpermute_b32 v239, v250, v91
	ds_bpermute_b32 v240, v250, v92
	ds_bpermute_b32 v241, v250, v93
	ds_bpermute_b32 v242, v250, v94
	v_mul_f32_e32 v86, v86, v117
	v_mul_f32_e32 v87, v87, v117
	v_log_f32_e32 v90, v82
	v_add_f32_e32 v82, 1.0, v83
	v_mul_f32_e32 v83, v84, v117
	v_max_f32_e32 v83, 0xc2a00000, v83
	v_mul_f32_e32 v84, v85, v117
	v_mul_f32_e32 v83, 0xbfb8aa3b, v83
	v_max_f32_e32 v84, 0xc2a00000, v84
	v_exp_f32_e32 v83, v83
	v_mul_f32_e32 v84, 0xbfb8aa3b, v84
	v_exp_f32_e32 v84, v84
	v_rcp_f32_e32 v82, v82
	v_add_f32_e32 v83, 1.0, v83
	v_rcp_f32_e32 v83, v83
	v_add_f32_e32 v84, 1.0, v84
	v_rcp_f32_e32 v84, v84
	v_mul_f32_e32 v88, v88, v117
	v_mul_f32_e32 v89, v89, v117
	v_max_f32_e32 v86, 0xc2a00000, v86
	v_max_f32_e32 v87, 0xc2a00000, v87
	v_max_f32_e32 v88, 0xc2a00000, v88
	v_max_f32_e32 v89, 0xc2a00000, v89
	v_fma_f32 v82, v120, v82, v125
	v_mul_f32_e32 v86, 0xbfb8aa3b, v86
	v_mul_f32_e32 v87, 0xbfb8aa3b, v87
	v_mul_f32_e32 v88, 0xbfb8aa3b, v88
	v_mul_f32_e32 v89, 0xbfb8aa3b, v89
	v_log_f32_e32 v91, v82
	v_fma_f32 v82, v118, v83, v126
	v_exp_f32_e32 v86, v86
	v_exp_f32_e32 v87, v87
	v_exp_f32_e32 v88, v88
	v_exp_f32_e32 v89, v89
	v_log_f32_e32 v92, v82
	v_fma_f32 v82, v119, v84, v127
	v_log_f32_e32 v93, v82
	ds_read2_b32 v[82:83], v176 offset0:48 offset1:128
	v_add_f32_e32 v86, 1.0, v86
	v_add_f32_e32 v87, 1.0, v87
	v_add_f32_e32 v88, 1.0, v88
	v_add_f32_e32 v89, 1.0, v89
	v_rcp_f32_e32 v86, v86
	v_rcp_f32_e32 v87, v87
	v_rcp_f32_e32 v88, v88
	v_rcp_f32_e32 v89, v89
	s_waitcnt lgkmcnt(0)
	v_mul_f32_e32 v74, v74, v82
	v_mul_f32_e32 v78, v78, v82
	v_max_f32_e32 v74, 0xc2a00000, v74
	v_max_f32_e32 v78, 0xc2a00000, v78
	v_mul_f32_e32 v74, 0xbfb8aa3b, v74
	v_fma_f32 v86, v153, v86, v128
	v_fma_f32 v87, v168, v87, v129
	v_fma_f32 v88, v121, v88, v130
	v_fma_f32 v89, v122, v89, v131
	v_mul_f32_e32 v78, 0xbfb8aa3b, v78
	v_exp_f32_e32 v74, v74
	v_log_f32_e32 v86, v86
	v_log_f32_e32 v87, v87
	v_log_f32_e32 v88, v88
	v_log_f32_e32 v89, v89
	v_exp_f32_e32 v78, v78
	v_mul_f32_e32 v79, v79, v82
	v_max_f32_e32 v79, 0xc2a00000, v79
	v_mul_f32_e32 v75, v75, v82
	v_mul_f32_e32 v79, 0xbfb8aa3b, v79
	v_add_f32_e32 v74, 1.0, v74
	v_max_f32_e32 v75, 0xc2a00000, v75
	v_cvt_pk_f16_f32 v84, v86, v87
	v_cvt_pk_f16_f32 v85, v88, v89
	v_cvt_pk_f16_f32 v86, v90, v91
	v_cvt_pk_f16_f32 v87, v92, v93
	v_exp_f32_e32 v79, v79
	v_add_f32_e32 v78, 1.0, v78
	v_rcp_f32_e32 v74, v74
	v_mul_f32_e32 v75, 0xbfb8aa3b, v75
	s_waitcnt lgkmcnt(6)
	v_subrev_u32_e32 v236, s82, v236
	global_store_dwordx4 v236, v[232:235], s[82:83] offset:64 sc1
	ds_bpermute_b32 v244, v250, v84
	ds_bpermute_b32 v245, v250, v85
	ds_bpermute_b32 v246, v250, v86
	ds_bpermute_b32 v247, v250, v87
	ds_bpermute_b32 v248, v250, v94
	v_exp_f32_e32 v75, v75
	v_mul_f32_e32 v80, v80, v82
	v_rcp_f32_e32 v86, v78
	v_or_b32_e32 v84, 48, v152
	v_mul_f32_e32 v81, v81, v82
	v_ashrrev_i32_e32 v85, 31, v84
	v_add_f32_e32 v78, 1.0, v79
	v_max_f32_e32 v80, 0xc2a00000, v80
	v_max_f32_e32 v81, 0xc2a00000, v81
	v_fma_f32 v74, v171, v74, v132
	v_rcp_f32_e32 v87, v78
	v_lshlrev_b64 v[78:79], 12, v[84:85]
	v_fma_f32 v84, v180, v86, v136
	v_mul_f32_e32 v80, 0xbfb8aa3b, v80
	v_mul_f32_e32 v81, 0xbfb8aa3b, v81
	v_log_f32_e32 v86, v74
	v_add_f32_e32 v74, 1.0, v75
	v_mul_f32_e32 v75, v76, v82
	v_exp_f32_e32 v80, v80
	v_exp_f32_e32 v81, v81
	v_max_f32_e32 v75, 0xc2a00000, v75
	v_mul_f32_e32 v76, v77, v82
	v_mul_f32_e32 v75, 0xbfb8aa3b, v75
	v_max_f32_e32 v76, 0xc2a00000, v76
	v_exp_f32_e32 v75, v75
	v_mul_f32_e32 v76, 0xbfb8aa3b, v76
	v_exp_f32_e32 v76, v76
	v_add_f32_e32 v80, 1.0, v80
	v_add_f32_e32 v81, 1.0, v81
	v_rcp_f32_e32 v80, v80
	v_rcp_f32_e32 v81, v81
	v_mul_f32_e32 v66, v66, v82
	v_rcp_f32_e32 v74, v74
	v_add_f32_e32 v75, 1.0, v75
	v_max_f32_e32 v66, 0xc2a00000, v66
	v_rcp_f32_e32 v75, v75
	v_add_f32_e32 v76, 1.0, v76
	v_mul_f32_e32 v66, 0xbfb8aa3b, v66
	v_rcp_f32_e32 v76, v76
	v_exp_f32_e32 v66, v66
	v_fma_f32 v80, v178, v80, v138
	v_fma_f32 v81, v177, v81, v139
	v_log_f32_e32 v80, v80
	v_log_f32_e32 v81, v81
	v_fma_f32 v74, v170, v74, v133
	v_log_f32_e32 v77, v74
	v_fma_f32 v74, v169, v75, v134
	v_mul_f32_e32 v70, v70, v82
	v_mul_f32_e32 v67, v67, v82
	v_fma_f32 v85, v179, v87, v137
	v_log_f32_e32 v87, v74
	v_fma_f32 v74, v155, v76, v135
	v_max_f32_e32 v70, 0xc2a00000, v70
	v_add_f32_e32 v66, 1.0, v66
	v_max_f32_e32 v67, 0xc2a00000, v67
	v_log_f32_e32 v84, v84
	v_log_f32_e32 v85, v85
	v_log_f32_e32 v88, v74
	v_mul_f32_e32 v70, 0xbfb8aa3b, v70
	v_rcp_f32_e32 v66, v66
	v_mul_f32_e32 v67, 0xbfb8aa3b, v67
	v_cvt_pk_f16_f32 v75, v80, v81
	v_exp_f32_e32 v80, v70
	v_mul_f32_e32 v70, v71, v82
	v_exp_f32_e32 v67, v67
	v_max_f32_e32 v70, 0xc2a00000, v70
	v_lshl_add_u64 v[78:79], s[42:43], 0, v[78:79]
	v_mul_f32_e32 v70, 0xbfb8aa3b, v70
	v_cvt_pk_f16_f32 v74, v84, v85
	v_cvt_pk_f16_f32 v76, v86, v77
	v_cvt_pk_f16_f32 v77, v87, v88
	v_exp_f32_e32 v81, v70
	v_lshl_add_u64 v[70:71], v[78:79], 0, v[114:115]
	v_fma_f32 v66, v123, v66, v124
	s_waitcnt lgkmcnt(6)
	v_subrev_u32_e32 v242, s82, v242
	global_store_dwordx4 v242, v[238:241], s[82:83] sc1
	ds_bpermute_b32 v232, v250, v74
	ds_bpermute_b32 v233, v250, v75
	ds_bpermute_b32 v234, v250, v76
	ds_bpermute_b32 v235, v250, v77
	ds_bpermute_b32 v236, v250, v70
	v_mul_f32_e32 v72, v72, v82
	v_mul_f32_e32 v73, v73, v82
	v_log_f32_e32 v76, v66
	v_add_f32_e32 v66, 1.0, v67
	v_mul_f32_e32 v67, v68, v82
	v_max_f32_e32 v67, 0xc2a00000, v67
	v_mul_f32_e32 v68, v69, v82
	v_max_f32_e32 v72, 0xc2a00000, v72
	v_max_f32_e32 v73, 0xc2a00000, v73
	v_mul_f32_e32 v67, 0xbfb8aa3b, v67
	v_max_f32_e32 v68, 0xc2a00000, v68
	v_mul_f32_e32 v72, 0xbfb8aa3b, v72
	v_mul_f32_e32 v73, 0xbfb8aa3b, v73
	v_exp_f32_e32 v67, v67
	v_mul_f32_e32 v68, 0xbfb8aa3b, v68
	v_exp_f32_e32 v72, v72
	v_exp_f32_e32 v73, v73
	v_exp_f32_e32 v68, v68
	v_mul_f32_e32 v58, v58, v83
	v_rcp_f32_e32 v66, v66
	v_add_f32_e32 v67, 1.0, v67
	v_max_f32_e32 v58, 0xc2a00000, v58
	v_add_f32_e32 v78, 1.0, v80
	v_add_f32_e32 v79, 1.0, v81
	v_add_f32_e32 v72, 1.0, v72
	v_add_f32_e32 v73, 1.0, v73
	v_rcp_f32_e32 v67, v67
	v_add_f32_e32 v68, 1.0, v68
	v_mul_f32_e32 v58, 0xbfb8aa3b, v58
	v_rcp_f32_e32 v78, v78
	v_rcp_f32_e32 v79, v79
	v_rcp_f32_e32 v72, v72
	v_rcp_f32_e32 v73, v73
	v_rcp_f32_e32 v68, v68
	v_exp_f32_e32 v58, v58
	v_fma_f32 v66, v120, v66, v125
	v_log_f32_e32 v69, v66
	v_fma_f32 v66, v118, v67, v126
	v_mul_f32_e32 v59, v59, v83
	v_fma_f32 v74, v153, v78, v128
	v_fma_f32 v75, v168, v79, v129
	v_fma_f32 v72, v121, v72, v130
	v_fma_f32 v73, v122, v73, v131
	v_log_f32_e32 v77, v66
	v_fma_f32 v66, v119, v68, v127
	v_add_f32_e32 v58, 1.0, v58
	v_max_f32_e32 v59, 0xc2a00000, v59
	v_log_f32_e32 v74, v74
	v_log_f32_e32 v75, v75
	v_log_f32_e32 v72, v72
	v_log_f32_e32 v73, v73
	v_log_f32_e32 v78, v66
	v_rcp_f32_e32 v58, v58
	v_mul_f32_e32 v59, 0xbfb8aa3b, v59
	v_exp_f32_e32 v59, v59
	v_mul_f32_e32 v64, v64, v83
	v_mul_f32_e32 v65, v65, v83
	v_max_f32_e32 v64, 0xc2a00000, v64
	v_max_f32_e32 v65, 0xc2a00000, v65
	v_cvt_pk_f16_f32 v66, v74, v75
	v_cvt_pk_f16_f32 v67, v72, v73
	v_cvt_pk_f16_f32 v68, v76, v69
	v_mul_f32_e32 v62, v62, v83
	v_mul_f32_e32 v63, v63, v83
	v_cvt_pk_f16_f32 v69, v77, v78
	v_mul_f32_e32 v64, 0xbfb8aa3b, v64
	v_mul_f32_e32 v65, 0xbfb8aa3b, v65
	v_fma_f32 v58, v171, v58, v132
	v_max_f32_e32 v62, 0xc2a00000, v62
	v_max_f32_e32 v63, 0xc2a00000, v63
	s_waitcnt lgkmcnt(5)
	v_subrev_u32_e32 v248, s82, v248
	global_store_dwordx4 v248, v[244:247], s[82:83] offset:64 sc1
	ds_bpermute_b32 v238, v250, v66
	ds_bpermute_b32 v239, v250, v67
	ds_bpermute_b32 v240, v250, v68
	ds_bpermute_b32 v241, v250, v69
	ds_bpermute_b32 v242, v250, v70
	v_exp_f32_e32 v64, v64
	v_exp_f32_e32 v65, v65
	v_log_f32_e32 v66, v58
	v_add_f32_e32 v58, 1.0, v59
	v_mul_f32_e32 v59, v60, v83
	v_mul_f32_e32 v62, 0xbfb8aa3b, v62
	v_mul_f32_e32 v63, 0xbfb8aa3b, v63
	v_max_f32_e32 v59, 0xc2a00000, v59
	v_mul_f32_e32 v60, v61, v83
	v_exp_f32_e32 v62, v62
	v_exp_f32_e32 v63, v63
	v_mul_f32_e32 v59, 0xbfb8aa3b, v59
	v_max_f32_e32 v60, 0xc2a00000, v60
	v_exp_f32_e32 v59, v59
	v_mul_f32_e32 v60, 0xbfb8aa3b, v60
	v_add_f32_e32 v64, 1.0, v64
	v_add_f32_e32 v65, 1.0, v65
	v_exp_f32_e32 v60, v60
	v_rcp_f32_e32 v64, v64
	v_rcp_f32_e32 v65, v65
	v_add_f32_e32 v62, 1.0, v62
	v_add_f32_e32 v63, 1.0, v63
	v_mul_f32_e32 v50, v50, v83
	v_rcp_f32_e32 v62, v62
	v_rcp_f32_e32 v63, v63
	v_rcp_f32_e32 v58, v58
	v_add_f32_e32 v59, 1.0, v59
	v_max_f32_e32 v50, 0xc2a00000, v50
	v_rcp_f32_e32 v59, v59
	v_add_f32_e32 v60, 1.0, v60
	v_mul_f32_e32 v50, 0xbfb8aa3b, v50
	v_fma_f32 v64, v178, v64, v138
	v_fma_f32 v65, v177, v65, v139
	v_rcp_f32_e32 v60, v60
	v_exp_f32_e32 v50, v50
	v_log_f32_e32 v64, v64
	v_log_f32_e32 v65, v65
	v_fma_f32 v62, v180, v62, v136
	v_fma_f32 v63, v179, v63, v137
	v_fma_f32 v58, v170, v58, v133
	v_mul_f32_e32 v54, v54, v83
	v_log_f32_e32 v62, v62
	v_log_f32_e32 v63, v63
	v_log_f32_e32 v61, v58
	v_fma_f32 v58, v169, v59, v134
	v_max_f32_e32 v54, 0xc2a00000, v54
	v_mul_f32_e32 v51, v51, v83
	v_log_f32_e32 v67, v58
	v_fma_f32 v58, v155, v60, v135
	v_mul_f32_e32 v54, 0xbfb8aa3b, v54
	v_add_f32_e32 v50, 1.0, v50
	v_max_f32_e32 v51, 0xc2a00000, v51
	v_log_f32_e32 v68, v58
	v_cvt_pk_f16_f32 v59, v64, v65
	v_exp_f32_e32 v64, v54
	v_mul_f32_e32 v54, v55, v83
	v_rcp_f32_e32 v50, v50
	v_mul_f32_e32 v51, 0xbfb8aa3b, v51
	v_max_f32_e32 v54, 0xc2a00000, v54
	v_exp_f32_e32 v51, v51
	v_cvt_pk_f16_f32 v58, v62, v63
	v_lshl_add_u64 v[62:63], v[166:167], 0, s[14:15]
	v_mul_f32_e32 v54, 0xbfb8aa3b, v54
	s_mov_b32 s14, 0x80000
	v_exp_f32_e32 v65, v54
	v_add_co_u32_e32 v54, vcc, s14, v166
	v_cvt_pk_f16_f32 v60, v66, v61
	v_cvt_pk_f16_f32 v61, v67, v68
	v_addc_co_u32_e32 v55, vcc, 0, v167, vcc
	v_fma_f32 v50, v123, v50, v124
	s_waitcnt lgkmcnt(5)
	v_subrev_u32_e32 v236, s82, v236
	global_store_dwordx4 v236, v[232:235], s[82:83] sc1
	ds_bpermute_b32 v244, v250, v58
	ds_bpermute_b32 v245, v250, v59
	ds_bpermute_b32 v246, v250, v60
	ds_bpermute_b32 v247, v250, v61
	ds_bpermute_b32 v248, v250, v54
	v_mul_f32_e32 v56, v56, v83
	v_mul_f32_e32 v57, v57, v83
	v_log_f32_e32 v58, v50
	v_add_f32_e32 v50, 1.0, v51
	v_mul_f32_e32 v51, v52, v83
	v_max_f32_e32 v51, 0xc2a00000, v51
	v_mul_f32_e32 v51, 0xbfb8aa3b, v51
	v_exp_f32_e32 v51, v51
	v_rcp_f32_e32 v50, v50
	v_mul_f32_e32 v52, v53, v83
	v_max_f32_e32 v56, 0xc2a00000, v56
	v_add_f32_e32 v51, 1.0, v51
	v_rcp_f32_e32 v51, v51
	v_fma_f32 v50, v120, v50, v125
	v_log_f32_e32 v59, v50
	v_max_f32_e32 v57, 0xc2a00000, v57
	v_fma_f32 v50, v118, v51, v126
	v_log_f32_e32 v60, v50
	ds_read2_b32 v[50:51], v176 offset0:144 offset1:160
	v_max_f32_e32 v52, 0xc2a00000, v52
	v_mul_f32_e32 v56, 0xbfb8aa3b, v56
	v_mul_f32_e32 v57, 0xbfb8aa3b, v57
	v_mul_f32_e32 v52, 0xbfb8aa3b, v52
	v_exp_f32_e32 v56, v56
	v_exp_f32_e32 v57, v57
	v_exp_f32_e32 v52, v52
	s_waitcnt lgkmcnt(0)
	v_mul_f32_e32 v42, v42, v50
	v_max_f32_e32 v42, 0xc2a00000, v42
	v_add_f32_e32 v64, 1.0, v64
	v_add_f32_e32 v65, 1.0, v65
	v_add_f32_e32 v56, 1.0, v56
	v_add_f32_e32 v57, 1.0, v57
	v_add_f32_e32 v52, 1.0, v52
	v_mul_f32_e32 v42, 0xbfb8aa3b, v42
	v_rcp_f32_e32 v64, v64
	v_rcp_f32_e32 v65, v65
	v_rcp_f32_e32 v56, v56
	v_rcp_f32_e32 v57, v57
	v_rcp_f32_e32 v52, v52
	v_exp_f32_e32 v42, v42
	v_mul_f32_e32 v43, v43, v50
	v_fma_f32 v54, v153, v64, v128
	v_fma_f32 v55, v168, v65, v129
	v_fma_f32 v56, v121, v56, v130
	v_fma_f32 v57, v122, v57, v131
	v_fma_f32 v52, v119, v52, v127
	v_add_f32_e32 v42, 1.0, v42
	v_max_f32_e32 v43, 0xc2a00000, v43
	v_log_f32_e32 v54, v54
	v_log_f32_e32 v55, v55
	v_log_f32_e32 v56, v56
	v_log_f32_e32 v57, v57
	v_log_f32_e32 v61, v52
	v_rcp_f32_e32 v42, v42
	v_mul_f32_e32 v43, 0xbfb8aa3b, v43
	v_exp_f32_e32 v43, v43
	v_mul_f32_e32 v48, v48, v50
	v_mul_f32_e32 v49, v49, v50
	v_max_f32_e32 v48, 0xc2a00000, v48
	v_max_f32_e32 v49, 0xc2a00000, v49
	v_cvt_pk_f16_f32 v52, v54, v55
	v_cvt_pk_f16_f32 v53, v56, v57
	v_cvt_pk_f16_f32 v54, v58, v59
	v_mul_f32_e32 v46, v46, v50
	v_mul_f32_e32 v47, v47, v50
	v_cvt_pk_f16_f32 v55, v60, v61
	v_mul_f32_e32 v48, 0xbfb8aa3b, v48
	v_mul_f32_e32 v49, 0xbfb8aa3b, v49
	v_fma_f32 v42, v171, v42, v132
	v_max_f32_e32 v46, 0xc2a00000, v46
	v_max_f32_e32 v47, 0xc2a00000, v47
	s_waitcnt lgkmcnt(6)
	v_subrev_u32_e32 v242, s82, v242
	global_store_dwordx4 v242, v[238:241], s[82:83] offset:64 sc1
	ds_bpermute_b32 v232, v250, v52
	ds_bpermute_b32 v233, v250, v53
	ds_bpermute_b32 v234, v250, v54
	ds_bpermute_b32 v235, v250, v55
	ds_bpermute_b32 v236, v250, v62
	v_exp_f32_e32 v48, v48
	v_exp_f32_e32 v49, v49
	v_log_f32_e32 v52, v42
	v_add_f32_e32 v42, 1.0, v43
	v_mul_f32_e32 v43, v44, v50
	v_mul_f32_e32 v46, 0xbfb8aa3b, v46
	v_mul_f32_e32 v47, 0xbfb8aa3b, v47
	v_max_f32_e32 v43, 0xc2a00000, v43
	v_mul_f32_e32 v44, v45, v50
	v_exp_f32_e32 v46, v46
	v_exp_f32_e32 v47, v47
	v_mul_f32_e32 v43, 0xbfb8aa3b, v43
	v_max_f32_e32 v44, 0xc2a00000, v44
	v_exp_f32_e32 v43, v43
	v_mul_f32_e32 v44, 0xbfb8aa3b, v44
	v_add_f32_e32 v48, 1.0, v48
	v_add_f32_e32 v49, 1.0, v49
	v_exp_f32_e32 v44, v44
	v_rcp_f32_e32 v48, v48
	v_rcp_f32_e32 v49, v49
	v_add_f32_e32 v46, 1.0, v46
	v_add_f32_e32 v47, 1.0, v47
	v_mul_f32_e32 v34, v34, v50
	v_rcp_f32_e32 v46, v46
	v_rcp_f32_e32 v47, v47
	v_rcp_f32_e32 v42, v42
	v_add_f32_e32 v43, 1.0, v43
	v_max_f32_e32 v34, 0xc2a00000, v34
	v_rcp_f32_e32 v43, v43
	v_add_f32_e32 v44, 1.0, v44
	v_mul_f32_e32 v34, 0xbfb8aa3b, v34
	v_fma_f32 v48, v178, v48, v138
	v_fma_f32 v49, v177, v49, v139
	v_rcp_f32_e32 v44, v44
	v_exp_f32_e32 v34, v34
	v_log_f32_e32 v48, v48
	v_log_f32_e32 v49, v49
	v_fma_f32 v46, v180, v46, v136
	v_fma_f32 v47, v179, v47, v137
	v_fma_f32 v42, v170, v42, v133
	v_mul_f32_e32 v38, v38, v50
	v_log_f32_e32 v46, v46
	v_log_f32_e32 v47, v47
	v_log_f32_e32 v45, v42
	v_fma_f32 v42, v169, v43, v134
	v_max_f32_e32 v38, 0xc2a00000, v38
	v_mul_f32_e32 v35, v35, v50
	v_log_f32_e32 v53, v42
	v_fma_f32 v42, v155, v44, v135
	v_mul_f32_e32 v38, 0xbfb8aa3b, v38
	v_add_f32_e32 v34, 1.0, v34
	v_max_f32_e32 v35, 0xc2a00000, v35
	v_log_f32_e32 v54, v42
	v_cvt_pk_f16_f32 v43, v48, v49
	v_exp_f32_e32 v48, v38
	v_mul_f32_e32 v38, v39, v50
	v_rcp_f32_e32 v34, v34
	v_mul_f32_e32 v35, 0xbfb8aa3b, v35
	s_mov_b64 s[14:15], 0x90000
	v_max_f32_e32 v38, 0xc2a00000, v38
	v_exp_f32_e32 v35, v35
	v_cvt_pk_f16_f32 v42, v46, v47
	v_lshl_add_u64 v[46:47], v[166:167], 0, s[14:15]
	v_mul_f32_e32 v38, 0xbfb8aa3b, v38
	s_mov_b32 s14, 0x90000
	v_exp_f32_e32 v49, v38
	v_add_co_u32_e32 v38, vcc, s14, v166
	v_cvt_pk_f16_f32 v44, v52, v45
	v_cvt_pk_f16_f32 v45, v53, v54
	v_addc_co_u32_e32 v39, vcc, 0, v167, vcc
	v_fma_f32 v34, v123, v34, v124
	s_waitcnt lgkmcnt(6)
	v_subrev_u32_e32 v248, s82, v248
	global_store_dwordx4 v248, v[244:247], s[82:83] sc1
	ds_bpermute_b32 v238, v250, v42
	ds_bpermute_b32 v239, v250, v43
	ds_bpermute_b32 v240, v250, v44
	ds_bpermute_b32 v241, v250, v45
	ds_bpermute_b32 v242, v250, v38
	v_mul_f32_e32 v40, v40, v50
	v_mul_f32_e32 v41, v41, v50
	v_log_f32_e32 v42, v34
	v_add_f32_e32 v34, 1.0, v35
	v_mul_f32_e32 v35, v36, v50
	v_max_f32_e32 v35, 0xc2a00000, v35
	v_mul_f32_e32 v36, v37, v50
	v_max_f32_e32 v40, 0xc2a00000, v40
	v_max_f32_e32 v41, 0xc2a00000, v41
	v_mul_f32_e32 v35, 0xbfb8aa3b, v35
	v_max_f32_e32 v36, 0xc2a00000, v36
	v_mul_f32_e32 v40, 0xbfb8aa3b, v40
	v_mul_f32_e32 v41, 0xbfb8aa3b, v41
	v_exp_f32_e32 v35, v35
	v_mul_f32_e32 v36, 0xbfb8aa3b, v36
	v_exp_f32_e32 v40, v40
	v_exp_f32_e32 v41, v41
	v_exp_f32_e32 v36, v36
	v_mul_f32_e32 v26, v26, v51
	v_rcp_f32_e32 v34, v34
	v_add_f32_e32 v35, 1.0, v35
	v_max_f32_e32 v26, 0xc2a00000, v26
	v_add_f32_e32 v48, 1.0, v48
	v_add_f32_e32 v49, 1.0, v49
	v_add_f32_e32 v40, 1.0, v40
	v_add_f32_e32 v41, 1.0, v41
	v_rcp_f32_e32 v35, v35
	v_add_f32_e32 v36, 1.0, v36
	v_mul_f32_e32 v26, 0xbfb8aa3b, v26
	v_rcp_f32_e32 v48, v48
	v_rcp_f32_e32 v49, v49
	v_rcp_f32_e32 v40, v40
	v_rcp_f32_e32 v41, v41
	v_rcp_f32_e32 v36, v36
	v_exp_f32_e32 v26, v26
	v_fma_f32 v34, v120, v34, v125
	v_log_f32_e32 v37, v34
	v_fma_f32 v34, v118, v35, v126
	v_mul_f32_e32 v27, v27, v51
	v_fma_f32 v38, v153, v48, v128
	v_fma_f32 v39, v168, v49, v129
	v_fma_f32 v40, v121, v40, v130
	v_fma_f32 v41, v122, v41, v131
	v_log_f32_e32 v43, v34
	v_fma_f32 v34, v119, v36, v127
	v_add_f32_e32 v26, 1.0, v26
	v_max_f32_e32 v27, 0xc2a00000, v27
	v_log_f32_e32 v38, v38
	v_log_f32_e32 v39, v39
	v_log_f32_e32 v40, v40
	v_log_f32_e32 v41, v41
	v_log_f32_e32 v44, v34
	v_rcp_f32_e32 v26, v26
	v_mul_f32_e32 v27, 0xbfb8aa3b, v27
	v_exp_f32_e32 v27, v27
	v_mul_f32_e32 v32, v32, v51
	v_mul_f32_e32 v33, v33, v51
	v_max_f32_e32 v32, 0xc2a00000, v32
	v_max_f32_e32 v33, 0xc2a00000, v33
	v_cvt_pk_f16_f32 v34, v38, v39
	v_cvt_pk_f16_f32 v35, v40, v41
	v_cvt_pk_f16_f32 v36, v42, v37
	v_mul_f32_e32 v30, v30, v51
	v_mul_f32_e32 v31, v31, v51
	v_cvt_pk_f16_f32 v37, v43, v44
	v_mul_f32_e32 v32, 0xbfb8aa3b, v32
	v_mul_f32_e32 v33, 0xbfb8aa3b, v33
	v_fma_f32 v26, v171, v26, v132
	v_max_f32_e32 v30, 0xc2a00000, v30
	v_max_f32_e32 v31, 0xc2a00000, v31
	s_waitcnt lgkmcnt(5)
	v_subrev_u32_e32 v236, s82, v236
	global_store_dwordx4 v236, v[232:235], s[82:83] offset:64 sc1
	ds_bpermute_b32 v244, v250, v34
	ds_bpermute_b32 v245, v250, v35
	ds_bpermute_b32 v246, v250, v36
	ds_bpermute_b32 v247, v250, v37
	ds_bpermute_b32 v248, v250, v46
	v_exp_f32_e32 v32, v32
	v_exp_f32_e32 v33, v33
	v_log_f32_e32 v34, v26
	v_add_f32_e32 v26, 1.0, v27
	v_mul_f32_e32 v27, v28, v51
	v_mul_f32_e32 v30, 0xbfb8aa3b, v30
	v_mul_f32_e32 v31, 0xbfb8aa3b, v31
	v_max_f32_e32 v27, 0xc2a00000, v27
	v_mul_f32_e32 v28, v29, v51
	v_exp_f32_e32 v30, v30
	v_exp_f32_e32 v31, v31
	v_mul_f32_e32 v27, 0xbfb8aa3b, v27
	v_max_f32_e32 v28, 0xc2a00000, v28
	v_exp_f32_e32 v27, v27
	v_mul_f32_e32 v28, 0xbfb8aa3b, v28
	v_add_f32_e32 v32, 1.0, v32
	v_add_f32_e32 v33, 1.0, v33
	v_exp_f32_e32 v28, v28
	v_rcp_f32_e32 v32, v32
	v_rcp_f32_e32 v33, v33
	v_add_f32_e32 v30, 1.0, v30
	v_add_f32_e32 v31, 1.0, v31
	v_mul_f32_e32 v18, v18, v51
	v_rcp_f32_e32 v30, v30
	v_rcp_f32_e32 v31, v31
	v_rcp_f32_e32 v26, v26
	v_add_f32_e32 v27, 1.0, v27
	v_max_f32_e32 v18, 0xc2a00000, v18
	v_rcp_f32_e32 v27, v27
	v_add_f32_e32 v28, 1.0, v28
	v_mul_f32_e32 v18, 0xbfb8aa3b, v18
	v_fma_f32 v32, v178, v32, v138
	v_fma_f32 v33, v177, v33, v139
	v_rcp_f32_e32 v28, v28
	v_exp_f32_e32 v18, v18
	v_log_f32_e32 v32, v32
	v_log_f32_e32 v33, v33
	v_fma_f32 v30, v180, v30, v136
	v_fma_f32 v31, v179, v31, v137
	v_fma_f32 v26, v170, v26, v133
	v_mul_f32_e32 v22, v22, v51
	v_log_f32_e32 v30, v30
	v_log_f32_e32 v31, v31
	v_log_f32_e32 v29, v26
	v_fma_f32 v26, v169, v27, v134
	v_max_f32_e32 v22, 0xc2a00000, v22
	v_mul_f32_e32 v19, v19, v51
	v_log_f32_e32 v35, v26
	v_fma_f32 v26, v155, v28, v135
	v_mul_f32_e32 v22, 0xbfb8aa3b, v22
	v_add_f32_e32 v18, 1.0, v18
	v_max_f32_e32 v19, 0xc2a00000, v19
	v_log_f32_e32 v36, v26
	v_cvt_pk_f16_f32 v27, v32, v33
	v_exp_f32_e32 v32, v22
	v_mul_f32_e32 v22, v23, v51
	v_rcp_f32_e32 v18, v18
	v_mul_f32_e32 v19, 0xbfb8aa3b, v19
	s_mov_b64 s[14:15], 0xa0000
	v_max_f32_e32 v22, 0xc2a00000, v22
	v_exp_f32_e32 v19, v19
	v_cvt_pk_f16_f32 v26, v30, v31
	v_lshl_add_u64 v[30:31], v[166:167], 0, s[14:15]
	v_mul_f32_e32 v22, 0xbfb8aa3b, v22
	s_mov_b32 s14, 0xa0000
	v_exp_f32_e32 v33, v22
	v_add_co_u32_e32 v22, vcc, s14, v166
	v_cvt_pk_f16_f32 v28, v34, v29
	v_cvt_pk_f16_f32 v29, v35, v36
	v_addc_co_u32_e32 v23, vcc, 0, v167, vcc
	v_fma_f32 v18, v123, v18, v124
	s_waitcnt lgkmcnt(5)
	v_subrev_u32_e32 v242, s82, v242
	global_store_dwordx4 v242, v[238:241], s[82:83] sc1
	ds_bpermute_b32 v232, v250, v26
	ds_bpermute_b32 v233, v250, v27
	ds_bpermute_b32 v234, v250, v28
	ds_bpermute_b32 v235, v250, v29
	ds_bpermute_b32 v236, v250, v22
	v_mul_f32_e32 v24, v24, v51
	v_mul_f32_e32 v25, v25, v51
	v_log_f32_e32 v26, v18
	v_add_f32_e32 v18, 1.0, v19
	v_mul_f32_e32 v19, v20, v51
	v_max_f32_e32 v19, 0xc2a00000, v19
	v_mul_f32_e32 v20, v21, v51
	ds_read_b32 v28, v176 offset:704
	v_max_f32_e32 v24, 0xc2a00000, v24
	v_max_f32_e32 v25, 0xc2a00000, v25
	v_mul_f32_e32 v19, 0xbfb8aa3b, v19
	v_max_f32_e32 v20, 0xc2a00000, v20
	v_mul_f32_e32 v24, 0xbfb8aa3b, v24
	v_mul_f32_e32 v25, 0xbfb8aa3b, v25
	v_exp_f32_e32 v19, v19
	v_mul_f32_e32 v20, 0xbfb8aa3b, v20
	v_exp_f32_e32 v24, v24
	v_exp_f32_e32 v25, v25
	v_exp_f32_e32 v20, v20
	s_waitcnt lgkmcnt(0)
	v_mul_f32_e32 v10, v10, v28
	v_rcp_f32_e32 v18, v18
	v_add_f32_e32 v19, 1.0, v19
	v_max_f32_e32 v10, 0xc2a00000, v10
	v_add_f32_e32 v32, 1.0, v32
	v_add_f32_e32 v33, 1.0, v33
	v_add_f32_e32 v24, 1.0, v24
	v_add_f32_e32 v25, 1.0, v25
	v_rcp_f32_e32 v19, v19
	v_add_f32_e32 v20, 1.0, v20
	v_mul_f32_e32 v10, 0xbfb8aa3b, v10
	v_rcp_f32_e32 v32, v32
	v_rcp_f32_e32 v33, v33
	v_rcp_f32_e32 v24, v24
	v_rcp_f32_e32 v25, v25
	v_rcp_f32_e32 v20, v20
	v_exp_f32_e32 v10, v10
	v_fma_f32 v18, v120, v18, v125
	v_log_f32_e32 v21, v18
	v_fma_f32 v18, v118, v19, v126
	v_mul_f32_e32 v11, v11, v28
	v_fma_f32 v22, v153, v32, v128
	v_fma_f32 v23, v168, v33, v129
	v_fma_f32 v24, v121, v24, v130
	v_fma_f32 v25, v122, v25, v131
	v_log_f32_e32 v27, v18
	v_fma_f32 v18, v119, v20, v127
	v_add_f32_e32 v10, 1.0, v10
	v_max_f32_e32 v11, 0xc2a00000, v11
	v_log_f32_e32 v22, v22
	v_log_f32_e32 v23, v23
	v_log_f32_e32 v24, v24
	v_log_f32_e32 v25, v25
	v_log_f32_e32 v29, v18
	v_rcp_f32_e32 v10, v10
	v_mul_f32_e32 v11, 0xbfb8aa3b, v11
	v_mul_f32_e32 v14, v14, v28
	v_mul_f32_e32 v15, v15, v28
	v_exp_f32_e32 v11, v11
	v_max_f32_e32 v14, 0xc2a00000, v14
	v_max_f32_e32 v15, 0xc2a00000, v15
	v_mul_f32_e32 v14, 0xbfb8aa3b, v14
	v_mul_f32_e32 v15, 0xbfb8aa3b, v15
	v_cvt_pk_f16_f32 v18, v22, v23
	v_cvt_pk_f16_f32 v19, v24, v25
	v_cvt_pk_f16_f32 v20, v26, v21
	v_exp_f32_e32 v14, v14
	v_exp_f32_e32 v15, v15
	v_cvt_pk_f16_f32 v21, v27, v29
	v_fma_f32 v10, v171, v10, v132
	s_waitcnt lgkmcnt(6)
	v_subrev_u32_e32 v248, s82, v248
	global_store_dwordx4 v248, v[244:247], s[82:83] offset:64 sc1
	ds_bpermute_b32 v238, v250, v18
	ds_bpermute_b32 v239, v250, v19
	ds_bpermute_b32 v240, v250, v20
	ds_bpermute_b32 v241, v250, v21
	ds_bpermute_b32 v242, v250, v30
	v_add_f32_e32 v14, 1.0, v14
	v_add_f32_e32 v15, 1.0, v15
	v_log_f32_e32 v18, v10
	v_add_f32_e32 v10, 1.0, v11
	v_mul_f32_e32 v11, v12, v28
	v_max_f32_e32 v11, 0xc2a00000, v11
	v_mul_f32_e32 v11, 0xbfb8aa3b, v11
	v_exp_f32_e32 v11, v11
	v_rcp_f32_e32 v14, v14
	v_rcp_f32_e32 v15, v15
	v_mul_f32_e32 v16, v16, v28
	v_mul_f32_e32 v17, v17, v28
	v_rcp_f32_e32 v10, v10
	v_mul_f32_e32 v12, v13, v28
	v_add_f32_e32 v11, 1.0, v11
	v_fma_f32 v14, v180, v14, v136
	v_fma_f32 v15, v179, v15, v137
	v_max_f32_e32 v16, 0xc2a00000, v16
	v_max_f32_e32 v17, 0xc2a00000, v17
	v_max_f32_e32 v12, 0xc2a00000, v12
	v_rcp_f32_e32 v11, v11
	v_log_f32_e32 v14, v14
	v_mul_f32_e32 v16, 0xbfb8aa3b, v16
	v_mul_f32_e32 v17, 0xbfb8aa3b, v17
	v_log_f32_e32 v15, v15
	v_mul_f32_e32 v12, 0xbfb8aa3b, v12
	v_exp_f32_e32 v16, v16
	v_exp_f32_e32 v17, v17
	v_exp_f32_e32 v12, v12
	v_mul_f32_e32 v6, v6, v28
	v_fma_f32 v10, v170, v10, v133
	v_max_f32_e32 v6, 0xc2a00000, v6
	v_log_f32_e32 v13, v10
	v_fma_f32 v10, v169, v11, v134
	v_mul_f32_e32 v6, 0xbfb8aa3b, v6
	v_log_f32_e32 v19, v10
	v_cvt_pk_f16_f32 v10, v14, v15
	v_exp_f32_e32 v14, v6
	v_mul_f32_e32 v6, v7, v28
	v_mul_f32_e32 v8, v8, v28
	v_mul_f32_e32 v9, v9, v28
	v_mul_f32_e32 v2, v2, v28
	v_mul_f32_e32 v3, v3, v28
	v_mul_f32_e32 v4, v4, v28
	v_mul_f32_e32 v5, v5, v28
	v_add_f32_e32 v16, 1.0, v16
	v_add_f32_e32 v17, 1.0, v17
	v_add_f32_e32 v12, 1.0, v12
	v_max_f32_e32 v6, 0xc2a00000, v6
	v_max_f32_e32 v8, 0xc2a00000, v8
	v_max_f32_e32 v9, 0xc2a00000, v9
	v_max_f32_e32 v2, 0xc2a00000, v2
	v_max_f32_e32 v3, 0xc2a00000, v3
	v_max_f32_e32 v4, 0xc2a00000, v4
	v_max_f32_e32 v5, 0xc2a00000, v5
	v_rcp_f32_e32 v16, v16
	v_rcp_f32_e32 v17, v17
	v_rcp_f32_e32 v12, v12
	v_mul_f32_e32 v6, 0xbfb8aa3b, v6
	v_mul_f32_e32 v8, 0xbfb8aa3b, v8
	v_mul_f32_e32 v9, 0xbfb8aa3b, v9
	v_mul_f32_e32 v2, 0xbfb8aa3b, v2
	v_mul_f32_e32 v3, 0xbfb8aa3b, v3
	v_mul_f32_e32 v4, 0xbfb8aa3b, v4
	v_mul_f32_e32 v5, 0xbfb8aa3b, v5
	v_exp_f32_e32 v15, v6
	v_exp_f32_e32 v8, v8
	v_exp_f32_e32 v9, v9
	v_exp_f32_e32 v2, v2
	v_exp_f32_e32 v3, v3
	v_exp_f32_e32 v4, v4
	v_exp_f32_e32 v5, v5
	v_fma_f32 v16, v178, v16, v138
	v_fmac_f32_e32 v139, v177, v17
	v_fmac_f32_e32 v135, v155, v12
	v_log_f32_e32 v16, v16
	v_log_f32_e32 v17, v139
	v_log_f32_e32 v20, v135
	v_add_f32_e32 v14, 1.0, v14
	v_add_f32_e32 v15, 1.0, v15
	v_add_f32_e32 v8, 1.0, v8
	v_add_f32_e32 v9, 1.0, v9
	v_add_f32_e32 v2, 1.0, v2
	v_add_f32_e32 v3, 1.0, v3
	v_add_f32_e32 v4, 1.0, v4
	v_add_f32_e32 v5, 1.0, v5
	s_mov_b64 s[14:15], 0xb0000
	v_rcp_f32_e32 v14, v14
	v_rcp_f32_e32 v15, v15
	v_rcp_f32_e32 v8, v8
	v_rcp_f32_e32 v9, v9
	v_rcp_f32_e32 v2, v2
	v_rcp_f32_e32 v3, v3
	v_rcp_f32_e32 v4, v4
	v_rcp_f32_e32 v5, v5
	v_lshl_add_u64 v[136:137], v[166:167], 0, s[14:15]
	s_mov_b32 s14, 0xb0000
	v_add_co_u32_e32 v6, vcc, s14, v166
	v_cvt_pk_f16_f32 v11, v16, v17
	v_cvt_pk_f16_f32 v12, v18, v13
	v_cvt_pk_f16_f32 v13, v19, v20
	v_addc_co_u32_e32 v7, vcc, 0, v167, vcc
	s_waitcnt lgkmcnt(6)
	v_subrev_u32_e32 v236, s82, v236
	global_store_dwordx4 v236, v[232:235], s[82:83] sc1
	ds_bpermute_b32 v244, v250, v10
	ds_bpermute_b32 v245, v250, v11
	ds_bpermute_b32 v246, v250, v12
	ds_bpermute_b32 v247, v250, v13
	ds_bpermute_b32 v248, v250, v6
	v_fma_f32 v6, v153, v14, v128
	v_fma_f32 v7, v168, v15, v129
	v_fma_f32 v8, v121, v8, v130
	v_fmac_f32_e32 v131, v122, v9
	v_fma_f32 v2, v123, v2, v124
	v_fma_f32 v3, v120, v3, v125
	v_fma_f32 v4, v118, v4, v126
	v_fmac_f32_e32 v127, v119, v5
	v_log_f32_e32 v6, v6
	v_log_f32_e32 v7, v7
	v_log_f32_e32 v8, v8
	v_log_f32_e32 v9, v131
	v_log_f32_e32 v2, v2
	v_log_f32_e32 v3, v3
	v_log_f32_e32 v4, v4
	v_log_f32_e32 v5, v127
	v_cvt_pk_f16_f32 v196, v181, v182
	v_cvt_pk_f16_f32 v132, v6, v7
	v_cvt_pk_f16_f32 v133, v8, v9
	v_cvt_pk_f16_f32 v134, v2, v3
	v_cvt_pk_f16_f32 v135, v4, v5
	s_waitcnt lgkmcnt(5)
	v_subrev_u32_e32 v242, s82, v242
	global_store_dwordx4 v242, v[238:241], s[82:83] offset:64 sc1
	ds_bpermute_b32 v232, v250, v194
	ds_bpermute_b32 v233, v250, v195
	ds_bpermute_b32 v234, v250, v196
	ds_bpermute_b32 v235, v250, v197
	ds_bpermute_b32 v236, v250, v166
	s_andn2_b64 vcc, exec, s[38:39]
	s_mov_b64 s[28:29], -1
	s_waitcnt lgkmcnt(5)
	v_subrev_u32_e32 v248, s82, v248
	global_store_dwordx4 v248, v[244:247], s[82:83] sc1
	ds_bpermute_b32 v238, v250, v132
	ds_bpermute_b32 v239, v250, v133
	ds_bpermute_b32 v240, v250, v134
	ds_bpermute_b32 v241, v250, v135
	ds_bpermute_b32 v242, v250, v136
	s_waitcnt lgkmcnt(5)
	v_subrev_u32_e32 v236, s82, v236
	global_store_dwordx4 v236, v[232:235], s[82:83] offset:64 sc1
	s_waitcnt lgkmcnt(0)
	v_subrev_u32_e32 v242, s82, v242
	global_store_dwordx4 v242, v[238:241], s[82:83] offset:64 sc1
	s_cbranch_vccnz .LBB0_338

.LBB0_509:
	s_ashr_i32 s57, s56, 31
	s_lshl_b64 s[14:15], s[56:57], 25
	s_add_u32 s14, s24, s14
	s_addc_u32 s15, s37, s15
	v_lshlrev_b32_e32 v114, 1, v177
	v_ashrrev_i32_e32 v153, 31, v152
	v_lshl_add_u64 v[132:133], s[14:15], 0, v[114:115]
	v_lshlrev_b64 v[136:137], 12, v[152:153]
	v_mov_b32_e32 v155, v154
	v_lshl_add_u64 v[136:137], v[132:133], 0, v[136:137]
	v_cvt_pk_bf16_f32 v166, v166, v167
	v_cvt_pk_bf16_f32 v167, v134, v135
	v_cvt_pk_bf16_f32 v168, v168, v169
	v_cvt_pk_bf16_f32 v169, v138, v139
	v_mov_b32_e32 v158, v154
	v_mov_b32_e32 v159, v154
	v_cndmask_b32_e64 v114, 0, 1, s[54:55]
	ds_bpermute_b32 v232, v250, v166
	ds_bpermute_b32 v233, v250, v167
	ds_bpermute_b32 v234, v250, v168
	ds_bpermute_b32 v235, v250, v169
	ds_bpermute_b32 v236, v250, v136
	v_pk_mul_f32 v[138:139], v[122:123], v[158:159]
	v_pk_mul_f32 v[134:135], v[120:121], v[154:155]
	v_pk_mul_f32 v[166:167], v[118:119], v[158:159]
	v_cmp_ne_u32_e64 s[40:41], 1, v114
	s_andn2_b64 vcc, exec, s[54:55]
	v_pk_mul_f32 v[168:169], v[116:117], v[154:155]
	s_waitcnt lgkmcnt(0)
	v_subrev_u32_e32 v236, s82, v236
	global_store_dwordx4 v236, v[232:235], s[82:83] sc1
	s_cbranch_vccnz .LBB0_511
	v_max_f32_e32 v114, v134, v134
	v_max_f32_e32 v134, 0xc2a00000, v114
	v_max_f32_e32 v114, v168, v168
	v_max_f32_e32 v158, 0xc2a00000, v114
	v_mul_f32_e32 v114, 0xbfb8aa3b, v134
	v_exp_f32_e32 v114, v114
	v_mul_f32_e32 v155, 0xbfb8aa3b, v158
	v_exp_f32_e32 v155, v155
	v_max_f32_e32 v135, v135, v135
	v_add_f32_e32 v114, 1.0, v114
	v_rcp_f32_e32 v160, v114
	v_add_f32_e32 v114, 1.0, v155
	v_max_f32_e32 v135, 0xc2a00000, v135
	v_max_f32_e32 v155, v169, v169
	v_max_f32_e32 v159, 0xc2a00000, v155
	v_mul_f32_e32 v155, 0xbfb8aa3b, v135
	v_exp_f32_e32 v155, v155
	v_mul_f32_e32 v161, 0xbfb8aa3b, v159
	v_exp_f32_e32 v169, v161
	v_max_f32_e32 v138, v138, v138
	v_rcp_f32_e32 v168, v114
	v_add_f32_e32 v114, 1.0, v155
	v_max_f32_e32 v138, 0xc2a00000, v138
	v_max_f32_e32 v155, v166, v166
	v_max_f32_e32 v166, 0xc2a00000, v155
	v_mul_f32_e32 v155, 0xbfb8aa3b, v138
	v_exp_f32_e32 v155, v155
	v_rcp_f32_e32 v161, v114
	v_add_f32_e32 v114, 1.0, v169
	v_mul_f32_e32 v169, 0xbfb8aa3b, v166
	v_exp_f32_e32 v171, v169
	v_max_f32_e32 v139, v139, v139
	v_rcp_f32_e32 v169, v114
	v_add_f32_e32 v114, 1.0, v155
	v_max_f32_e32 v139, 0xc2a00000, v139
	v_max_f32_e32 v155, v167, v167
	v_max_f32_e32 v167, 0xc2a00000, v155
	v_mul_f32_e32 v155, 0xbfb8aa3b, v139
	v_rcp_f32_e32 v170, v114
	v_add_f32_e32 v114, 1.0, v171
	v_exp_f32_e32 v155, v155
	v_mul_f32_e32 v171, 0xbfb8aa3b, v167
	v_exp_f32_e32 v179, v171
	v_rcp_f32_e32 v178, v114
	v_add_f32_e32 v114, 1.0, v155
	v_rcp_f32_e32 v171, v114
	v_add_f32_e32 v114, 1.0, v179
	v_rcp_f32_e32 v179, v114
	v_pk_mul_f32 v[134:135], v[134:135], v[160:161]
	v_pk_mul_f32 v[138:139], v[138:139], v[170:171]
	v_pk_mul_f32 v[168:169], v[158:159], v[168:169]
	v_pk_mul_f32 v[166:167], v[166:167], v[178:179]

.LBB0_541:
	s_and_b64 vcc, exec, s[40:41]
	s_cbranch_vccz .LBB0_540
	v_lshlrev_b32_e32 v155, 2, v177
	global_load_dwordx4 v[136:139], v155, s[42:43]
	global_load_dwordx4 v[132:135], v155, s[42:43] offset:16
	s_waitcnt lgkmcnt(0)
	v_mul_f32_e32 v160, v128, v154
	v_mul_f32_e32 v161, v129, v154
	v_mul_f32_e32 v166, v130, v154
	v_mul_f32_e32 v167, v131, v154
	v_mul_f32_e32 v168, v124, v154
	v_mul_f32_e32 v169, v125, v154
	v_mul_f32_e32 v170, v126, v154
	v_mul_f32_e32 v171, v127, v154
	global_load_dwordx4 v[124:127], v155, s[42:43] offset:144
	global_load_dwordx4 v[128:131], v155, s[42:43] offset:128
	v_ashrrev_i32_e32 v153, 31, v152
	v_lshlrev_b64 v[158:159], 12, v[152:153]
	v_max_f32_e32 v153, 0xc2a00000, v160
	v_max_f32_e32 v155, 0xc2a00000, v161
	v_max_f32_e32 v160, 0xc2a00000, v166
	v_max_f32_e32 v161, 0xc2a00000, v167
	v_max_f32_e32 v166, 0xc2a00000, v168
	v_max_f32_e32 v167, 0xc2a00000, v169
	v_max_f32_e32 v168, 0xc2a00000, v170
	v_max_f32_e32 v169, 0xc2a00000, v171
	v_mul_f32_e32 v153, 0xbfb8aa3b, v153
	v_mul_f32_e32 v155, 0xbfb8aa3b, v155
	v_mul_f32_e32 v168, 0xbfb8aa3b, v168
	v_mul_f32_e32 v169, 0xbfb8aa3b, v169
	v_exp_f32_e32 v153, v153
	v_exp_f32_e32 v155, v155
	v_mul_f32_e32 v160, 0xbfb8aa3b, v160
	v_mul_f32_e32 v161, 0xbfb8aa3b, v161
	v_exp_f32_e32 v168, v168
	v_exp_f32_e32 v169, v169
	v_exp_f32_e32 v160, v160
	v_exp_f32_e32 v161, v161
	v_mul_f32_e32 v120, v120, v154
	v_max_f32_e32 v120, 0xc2a00000, v120
	v_add_f32_e32 v153, 1.0, v153
	v_add_f32_e32 v155, 1.0, v155
	v_mul_f32_e32 v121, v121, v154
	v_lshlrev_b32_e32 v114, 1, v177
	v_mul_f32_e32 v166, 0xbfb8aa3b, v166
	v_mul_f32_e32 v167, 0xbfb8aa3b, v167
	v_lshl_add_u64 v[158:159], s[26:27], 0, v[158:159]
	v_add_f32_e32 v168, 1.0, v168
	v_add_f32_e32 v169, 1.0, v169
	v_rcp_f32_e32 v153, v153
	v_rcp_f32_e32 v181, v155
	v_mul_f32_e32 v120, 0xbfb8aa3b, v120
	v_max_f32_e32 v121, 0xc2a00000, v121
	v_exp_f32_e32 v170, v166
	v_exp_f32_e32 v171, v167
	v_lshl_add_u64 v[166:167], v[158:159], 0, v[114:115]
	v_add_f32_e32 v158, 1.0, v160
	v_add_f32_e32 v159, 1.0, v161
	v_rcp_f32_e32 v168, v168
	v_rcp_f32_e32 v182, v169
	v_exp_f32_e32 v120, v120
	v_mul_f32_e32 v121, 0xbfb8aa3b, v121
	v_rcp_f32_e32 v158, v158
	v_rcp_f32_e32 v159, v159
	v_exp_f32_e32 v121, v121
	v_add_f32_e32 v120, 1.0, v120
	v_rcp_f32_e32 v120, v120
	v_mul_f32_e32 v116, v116, v154
	v_add_f32_e32 v121, 1.0, v121
	v_rcp_f32_e32 v121, v121
	v_add_f32_e32 v160, 1.0, v170
	v_add_f32_e32 v161, 1.0, v171
	v_max_f32_e32 v116, 0xc2a00000, v116
	v_mul_f32_e32 v117, v117, v154
	v_rcp_f32_e32 v160, v160
	v_rcp_f32_e32 v161, v161
	v_mul_f32_e32 v116, 0xbfb8aa3b, v116
	v_max_f32_e32 v117, 0xc2a00000, v117
	v_exp_f32_e32 v116, v116
	v_mul_f32_e32 v117, 0xbfb8aa3b, v117
	v_exp_f32_e32 v117, v117
	s_mov_b64 s[14:15], 0x80000
	v_add_f32_e32 v116, 1.0, v116
	v_rcp_f32_e32 v116, v116
	v_add_f32_e32 v117, 1.0, v117
	s_waitcnt vmcnt(0)
	v_sub_f32_e32 v180, 1.0, v136
	v_sub_f32_e32 v179, 1.0, v137
	v_sub_f32_e32 v169, 1.0, v134
	v_sub_f32_e32 v155, 1.0, v135
	v_fma_f32 v153, v180, v153, v136
	v_fma_f32 v181, v179, v181, v137
	v_sub_f32_e32 v178, 1.0, v138
	v_sub_f32_e32 v177, 1.0, v139
	v_fma_f32 v168, v169, v168, v134
	v_fma_f32 v182, v155, v182, v135
	v_log_f32_e32 v153, v153
	v_log_f32_e32 v181, v181
	v_fma_f32 v158, v178, v158, v138
	v_fma_f32 v159, v177, v159, v139
	v_log_f32_e32 v168, v168
	v_log_f32_e32 v182, v182
	v_log_f32_e32 v158, v158
	v_log_f32_e32 v159, v159
	v_cvt_pk_f16_f32 v194, v153, v181
	v_sub_f32_e32 v153, 1.0, v128
	v_cvt_pk_f16_f32 v197, v168, v182
	v_fma_f32 v120, v153, v120, v128
	v_sub_f32_e32 v168, 1.0, v129
	v_cvt_pk_f16_f32 v195, v158, v159
	v_log_f32_e32 v158, v120
	v_fma_f32 v120, v168, v121, v129
	v_log_f32_e32 v159, v120
	v_mul_f32_e32 v120, v122, v154
	v_max_f32_e32 v120, 0xc2a00000, v120
	v_mul_f32_e32 v121, v123, v154
	v_mul_f32_e32 v120, 0xbfb8aa3b, v120
	v_max_f32_e32 v121, 0xc2a00000, v121
	v_exp_f32_e32 v120, v120
	v_mul_f32_e32 v121, 0xbfb8aa3b, v121
	v_exp_f32_e32 v122, v121
	v_sub_f32_e32 v171, 1.0, v132
	v_sub_f32_e32 v170, 1.0, v133
	v_add_f32_e32 v120, 1.0, v120
	v_fma_f32 v160, v171, v160, v132
	v_fma_f32 v161, v170, v161, v133
	v_rcp_f32_e32 v120, v120
	v_add_f32_e32 v122, 1.0, v122
	v_log_f32_e32 v160, v160
	v_log_f32_e32 v161, v161
	v_rcp_f32_e32 v123, v122
	v_sub_f32_e32 v121, 1.0, v130
	v_rcp_f32_e32 v117, v117
	v_fma_f32 v120, v121, v120, v130
	v_sub_f32_e32 v122, 1.0, v131
	v_cvt_pk_f16_f32 v196, v160, v161
	v_log_f32_e32 v160, v120
	v_fma_f32 v120, v122, v123, v131
	v_sub_f32_e32 v123, 1.0, v124
	v_log_f32_e32 v161, v120
	v_fma_f32 v116, v123, v116, v124
	v_sub_f32_e32 v120, 1.0, v125
	v_log_f32_e32 v181, v116
	v_fma_f32 v116, v120, v117, v125
	v_log_f32_e32 v182, v116
	v_mul_f32_e32 v116, v118, v154
	v_max_f32_e32 v116, 0xc2a00000, v116
	v_mul_f32_e32 v117, v119, v154
	v_mul_f32_e32 v116, 0xbfb8aa3b, v116
	v_max_f32_e32 v117, 0xc2a00000, v117
	v_exp_f32_e32 v116, v116
	v_mul_f32_e32 v117, 0xbfb8aa3b, v117
	v_exp_f32_e32 v117, v117
	v_sub_f32_e32 v118, 1.0, v126
	v_add_f32_e32 v116, 1.0, v116
	v_rcp_f32_e32 v116, v116
	v_add_f32_e32 v117, 1.0, v117
	v_rcp_f32_e32 v117, v117
	v_sub_f32_e32 v119, 1.0, v127
	v_fma_f32 v116, v118, v116, v126
	v_log_f32_e32 v154, v116
	v_fma_f32 v116, v119, v117, v127
	v_log_f32_e32 v183, v116
	ds_read2_b32 v[116:117], v176 offset0:16 offset1:32
	ds_bpermute_b32 v238, v250, v194
	ds_bpermute_b32 v239, v250, v195
	ds_bpermute_b32 v240, v250, v196
	ds_bpermute_b32 v241, v250, v197
	ds_bpermute_b32 v242, v250, v166
	s_waitcnt lgkmcnt(0)
	v_mul_f32_e32 v106, v106, v116
	v_max_f32_e32 v106, 0xc2a00000, v106
	v_mul_f32_e32 v106, 0xbfb8aa3b, v106
	v_exp_f32_e32 v106, v106
	v_mul_f32_e32 v110, v110, v116
	v_max_f32_e32 v110, 0xc2a00000, v110
	v_mul_f32_e32 v111, v111, v116
	v_mul_f32_e32 v110, 0xbfb8aa3b, v110
	v_max_f32_e32 v111, 0xc2a00000, v111
	v_mul_f32_e32 v107, v107, v116
	v_exp_f32_e32 v110, v110
	v_mul_f32_e32 v111, 0xbfb8aa3b, v111
	v_add_f32_e32 v106, 1.0, v106
	v_max_f32_e32 v107, 0xc2a00000, v107
	v_exp_f32_e32 v111, v111
	v_rcp_f32_e32 v106, v106
	v_mul_f32_e32 v107, 0xbfb8aa3b, v107
	v_exp_f32_e32 v107, v107
	v_cvt_pk_f16_f32 v194, v158, v159
	v_or_b32_e32 v158, 16, v152
	v_add_f32_e32 v110, 1.0, v110
	v_mul_f32_e32 v112, v112, v116
	v_mul_f32_e32 v113, v113, v116
	v_cvt_pk_f16_f32 v197, v154, v183
	v_ashrrev_i32_e32 v159, 31, v158
	v_rcp_f32_e32 v154, v110
	v_add_f32_e32 v110, 1.0, v111
	v_max_f32_e32 v112, 0xc2a00000, v112
	v_max_f32_e32 v113, 0xc2a00000, v113
	v_fma_f32 v106, v171, v106, v132
	v_cvt_pk_f16_f32 v195, v160, v161
	v_rcp_f32_e32 v160, v110
	v_lshlrev_b64 v[110:111], 12, v[158:159]
	v_mul_f32_e32 v112, 0xbfb8aa3b, v112
	v_mul_f32_e32 v113, 0xbfb8aa3b, v113
	v_log_f32_e32 v159, v106
	v_add_f32_e32 v106, 1.0, v107
	v_mul_f32_e32 v107, v108, v116
	v_exp_f32_e32 v112, v112
	v_exp_f32_e32 v113, v113
	v_max_f32_e32 v107, 0xc2a00000, v107
	v_mul_f32_e32 v108, v109, v116
	v_mul_f32_e32 v107, 0xbfb8aa3b, v107
	v_max_f32_e32 v108, 0xc2a00000, v108
	v_exp_f32_e32 v107, v107
	v_mul_f32_e32 v108, 0xbfb8aa3b, v108
	v_exp_f32_e32 v108, v108
	v_add_f32_e32 v112, 1.0, v112
	v_add_f32_e32 v113, 1.0, v113
	v_rcp_f32_e32 v112, v112
	v_rcp_f32_e32 v113, v113
	v_mul_f32_e32 v98, v98, v116
	v_rcp_f32_e32 v106, v106
	v_add_f32_e32 v107, 1.0, v107
	v_max_f32_e32 v98, 0xc2a00000, v98
	v_rcp_f32_e32 v107, v107
	v_add_f32_e32 v108, 1.0, v108
	v_mul_f32_e32 v98, 0xbfb8aa3b, v98
	v_rcp_f32_e32 v108, v108
	v_exp_f32_e32 v98, v98
	v_fma_f32 v112, v178, v112, v138
	v_fma_f32 v113, v177, v113, v139
	v_log_f32_e32 v112, v112
	v_log_f32_e32 v113, v113
	v_fma_f32 v106, v170, v106, v133
	v_log_f32_e32 v109, v106
	v_fma_f32 v106, v169, v107, v134
	v_mul_f32_e32 v102, v102, v116
	v_mul_f32_e32 v99, v99, v116
	v_fma_f32 v154, v180, v154, v136
	v_fma_f32 v158, v179, v160, v137
	v_log_f32_e32 v160, v106
	v_fma_f32 v106, v155, v108, v135
	v_max_f32_e32 v102, 0xc2a00000, v102
	v_add_f32_e32 v98, 1.0, v98
	v_max_f32_e32 v99, 0xc2a00000, v99
	v_log_f32_e32 v154, v154
	v_log_f32_e32 v158, v158
	v_log_f32_e32 v161, v106
	v_mul_f32_e32 v102, 0xbfb8aa3b, v102
	v_rcp_f32_e32 v98, v98
	v_mul_f32_e32 v99, 0xbfb8aa3b, v99
	v_cvt_pk_f16_f32 v107, v112, v113
	v_exp_f32_e32 v112, v102
	v_mul_f32_e32 v102, v103, v116
	v_exp_f32_e32 v99, v99
	v_max_f32_e32 v102, 0xc2a00000, v102
	v_lshl_add_u64 v[110:111], s[26:27], 0, v[110:111]
	v_mul_f32_e32 v102, 0xbfb8aa3b, v102
	v_cvt_pk_f16_f32 v106, v154, v158
	v_cvt_pk_f16_f32 v108, v159, v109
	v_cvt_pk_f16_f32 v109, v160, v161
	v_exp_f32_e32 v113, v102
	v_lshl_add_u64 v[102:103], v[110:111], 0, v[114:115]
	v_fma_f32 v98, v123, v98, v124
	ds_bpermute_b32 v244, v250, v106
	ds_bpermute_b32 v245, v250, v107
	ds_bpermute_b32 v246, v250, v108
	ds_bpermute_b32 v247, v250, v109
	ds_bpermute_b32 v248, v250, v102
	v_mul_f32_e32 v104, v104, v116
	v_mul_f32_e32 v105, v105, v116
	v_log_f32_e32 v108, v98
	v_add_f32_e32 v98, 1.0, v99
	v_mul_f32_e32 v99, v100, v116
	v_max_f32_e32 v99, 0xc2a00000, v99
	v_mul_f32_e32 v100, v101, v116
	v_max_f32_e32 v104, 0xc2a00000, v104
	v_max_f32_e32 v105, 0xc2a00000, v105
	v_mul_f32_e32 v99, 0xbfb8aa3b, v99
	v_max_f32_e32 v100, 0xc2a00000, v100
	v_mul_f32_e32 v104, 0xbfb8aa3b, v104
	v_mul_f32_e32 v105, 0xbfb8aa3b, v105
	v_exp_f32_e32 v99, v99
	v_mul_f32_e32 v100, 0xbfb8aa3b, v100
	v_exp_f32_e32 v104, v104
	v_exp_f32_e32 v105, v105
	v_exp_f32_e32 v100, v100
	v_rcp_f32_e32 v98, v98
	v_add_f32_e32 v99, 1.0, v99
	v_add_f32_e32 v110, 1.0, v112
	v_add_f32_e32 v111, 1.0, v113
	v_add_f32_e32 v104, 1.0, v104
	v_add_f32_e32 v105, 1.0, v105
	v_rcp_f32_e32 v99, v99
	v_add_f32_e32 v100, 1.0, v100
	v_rcp_f32_e32 v110, v110
	v_rcp_f32_e32 v111, v111
	v_rcp_f32_e32 v104, v104
	v_rcp_f32_e32 v105, v105
	v_rcp_f32_e32 v100, v100
	v_mul_f32_e32 v90, v90, v117
	v_fma_f32 v98, v120, v98, v125
	v_mul_f32_e32 v94, v94, v117
	v_max_f32_e32 v90, 0xc2a00000, v90
	v_log_f32_e32 v101, v98
	v_fma_f32 v98, v118, v99, v126
	v_max_f32_e32 v94, 0xc2a00000, v94
	v_mul_f32_e32 v90, 0xbfb8aa3b, v90
	v_fma_f32 v106, v153, v110, v128
	v_fma_f32 v107, v168, v111, v129
	v_fma_f32 v104, v121, v104, v130
	v_fma_f32 v105, v122, v105, v131
	v_log_f32_e32 v109, v98
	v_fma_f32 v98, v119, v100, v127
	v_mul_f32_e32 v94, 0xbfb8aa3b, v94
	v_exp_f32_e32 v90, v90
	v_log_f32_e32 v106, v106
	v_log_f32_e32 v107, v107
	v_log_f32_e32 v104, v104
	v_log_f32_e32 v105, v105
	v_log_f32_e32 v110, v98
	v_exp_f32_e32 v94, v94
	v_mul_f32_e32 v95, v95, v117
	v_max_f32_e32 v95, 0xc2a00000, v95
	v_mul_f32_e32 v91, v91, v117
	v_mul_f32_e32 v95, 0xbfb8aa3b, v95
	v_add_f32_e32 v90, 1.0, v90
	v_max_f32_e32 v91, 0xc2a00000, v91
	v_cvt_pk_f16_f32 v98, v106, v107
	v_cvt_pk_f16_f32 v99, v104, v105
	v_cvt_pk_f16_f32 v100, v108, v101
	v_cvt_pk_f16_f32 v101, v109, v110
	v_exp_f32_e32 v95, v95
	v_add_f32_e32 v94, 1.0, v94
	v_rcp_f32_e32 v90, v90
	v_mul_f32_e32 v91, 0xbfb8aa3b, v91
	s_waitcnt lgkmcnt(5)
	v_subrev_u32_e32 v242, s82, v242
	global_store_dwordx4 v242, v[238:241], s[82:83] sc1
	ds_bpermute_b32 v232, v250, v98
	ds_bpermute_b32 v233, v250, v99
	ds_bpermute_b32 v234, v250, v100
	ds_bpermute_b32 v235, v250, v101
	ds_bpermute_b32 v236, v250, v102
	v_exp_f32_e32 v91, v91
	v_fma_f32 v90, v171, v90, v132
	v_rcp_f32_e32 v100, v94
	v_or_b32_e32 v98, 32, v152
	v_ashrrev_i32_e32 v99, 31, v98
	v_add_f32_e32 v94, 1.0, v95
	v_rcp_f32_e32 v101, v94
	v_lshlrev_b64 v[94:95], 12, v[98:99]
	v_fma_f32 v98, v180, v100, v136
	v_log_f32_e32 v100, v90
	v_add_f32_e32 v90, 1.0, v91
	v_mul_f32_e32 v91, v92, v117
	v_mul_f32_e32 v96, v96, v117
	v_mul_f32_e32 v97, v97, v117
	v_max_f32_e32 v91, 0xc2a00000, v91
	v_mul_f32_e32 v92, v93, v117
	v_max_f32_e32 v96, 0xc2a00000, v96
	v_max_f32_e32 v97, 0xc2a00000, v97
	v_mul_f32_e32 v91, 0xbfb8aa3b, v91
	v_max_f32_e32 v92, 0xc2a00000, v92
	v_mul_f32_e32 v96, 0xbfb8aa3b, v96
	v_mul_f32_e32 v97, 0xbfb8aa3b, v97
	v_exp_f32_e32 v91, v91
	v_mul_f32_e32 v92, 0xbfb8aa3b, v92
	v_exp_f32_e32 v96, v96
	v_exp_f32_e32 v97, v97
	v_exp_f32_e32 v92, v92
	v_mul_f32_e32 v82, v82, v117
	v_rcp_f32_e32 v90, v90
	v_add_f32_e32 v91, 1.0, v91
	v_max_f32_e32 v82, 0xc2a00000, v82
	v_add_f32_e32 v96, 1.0, v96
	v_add_f32_e32 v97, 1.0, v97
	v_rcp_f32_e32 v91, v91
	v_add_f32_e32 v92, 1.0, v92
	v_mul_f32_e32 v82, 0xbfb8aa3b, v82
	v_rcp_f32_e32 v96, v96
	v_rcp_f32_e32 v97, v97
	v_rcp_f32_e32 v92, v92
	v_exp_f32_e32 v82, v82
	v_fma_f32 v90, v170, v90, v133
	v_log_f32_e32 v93, v90
	v_fma_f32 v90, v169, v91, v134
	v_mul_f32_e32 v83, v83, v117
	v_fma_f32 v99, v179, v101, v137
	v_fma_f32 v96, v178, v96, v138
	v_fma_f32 v97, v177, v97, v139
	v_log_f32_e32 v101, v90
	v_fma_f32 v90, v155, v92, v135
	v_add_f32_e32 v82, 1.0, v82
	v_max_f32_e32 v83, 0xc2a00000, v83
	v_log_f32_e32 v98, v98
	v_log_f32_e32 v99, v99
	v_log_f32_e32 v96, v96
	v_log_f32_e32 v97, v97
	v_log_f32_e32 v102, v90
	v_rcp_f32_e32 v82, v82
	v_mul_f32_e32 v83, 0xbfb8aa3b, v83
	v_exp_f32_e32 v83, v83
	v_lshl_add_u64 v[94:95], s[26:27], 0, v[94:95]
	v_cvt_pk_f16_f32 v90, v98, v99
	v_cvt_pk_f16_f32 v91, v96, v97
	v_cvt_pk_f16_f32 v92, v100, v93
	v_cvt_pk_f16_f32 v93, v101, v102
	v_lshl_add_u64 v[94:95], v[94:95], 0, v[114:115]
	v_fma_f32 v82, v123, v82, v124
	s_waitcnt lgkmcnt(5)
	v_subrev_u32_e32 v248, s82, v248
	global_store_dwordx4 v248, v[244:247], s[82:83] sc1
	ds_bpermute_b32 v238, v250, v90
	ds_bpermute_b32 v239, v250, v91
	ds_bpermute_b32 v240, v250, v92
	ds_bpermute_b32 v241, v250, v93
	ds_bpermute_b32 v242, v250, v94
	v_mul_f32_e32 v86, v86, v117
	v_mul_f32_e32 v87, v87, v117
	v_log_f32_e32 v90, v82
	v_add_f32_e32 v82, 1.0, v83
	v_mul_f32_e32 v83, v84, v117
	v_max_f32_e32 v83, 0xc2a00000, v83
	v_mul_f32_e32 v84, v85, v117
	v_mul_f32_e32 v83, 0xbfb8aa3b, v83
	v_max_f32_e32 v84, 0xc2a00000, v84
	v_exp_f32_e32 v83, v83
	v_mul_f32_e32 v84, 0xbfb8aa3b, v84
	v_exp_f32_e32 v84, v84
	v_rcp_f32_e32 v82, v82
	v_add_f32_e32 v83, 1.0, v83
	v_rcp_f32_e32 v83, v83
	v_add_f32_e32 v84, 1.0, v84
	v_rcp_f32_e32 v84, v84
	v_mul_f32_e32 v88, v88, v117
	v_mul_f32_e32 v89, v89, v117
	v_max_f32_e32 v86, 0xc2a00000, v86
	v_max_f32_e32 v87, 0xc2a00000, v87
	v_max_f32_e32 v88, 0xc2a00000, v88
	v_max_f32_e32 v89, 0xc2a00000, v89
	v_fma_f32 v82, v120, v82, v125
	v_mul_f32_e32 v86, 0xbfb8aa3b, v86
	v_mul_f32_e32 v87, 0xbfb8aa3b, v87
	v_mul_f32_e32 v88, 0xbfb8aa3b, v88
	v_mul_f32_e32 v89, 0xbfb8aa3b, v89
	v_log_f32_e32 v91, v82
	v_fma_f32 v82, v118, v83, v126
	v_exp_f32_e32 v86, v86
	v_exp_f32_e32 v87, v87
	v_exp_f32_e32 v88, v88
	v_exp_f32_e32 v89, v89
	v_log_f32_e32 v92, v82
	v_fma_f32 v82, v119, v84, v127
	v_log_f32_e32 v93, v82
	ds_read2_b32 v[82:83], v176 offset0:48 offset1:128
	v_add_f32_e32 v86, 1.0, v86
	v_add_f32_e32 v87, 1.0, v87
	v_add_f32_e32 v88, 1.0, v88
	v_add_f32_e32 v89, 1.0, v89
	v_rcp_f32_e32 v86, v86
	v_rcp_f32_e32 v87, v87
	v_rcp_f32_e32 v88, v88
	v_rcp_f32_e32 v89, v89
	s_waitcnt lgkmcnt(0)
	v_mul_f32_e32 v74, v74, v82
	v_mul_f32_e32 v78, v78, v82
	v_max_f32_e32 v74, 0xc2a00000, v74
	v_max_f32_e32 v78, 0xc2a00000, v78
	v_mul_f32_e32 v74, 0xbfb8aa3b, v74
	v_fma_f32 v86, v153, v86, v128
	v_fma_f32 v87, v168, v87, v129
	v_fma_f32 v88, v121, v88, v130
	v_fma_f32 v89, v122, v89, v131
	v_mul_f32_e32 v78, 0xbfb8aa3b, v78
	v_exp_f32_e32 v74, v74
	v_log_f32_e32 v86, v86
	v_log_f32_e32 v87, v87
	v_log_f32_e32 v88, v88
	v_log_f32_e32 v89, v89
	v_exp_f32_e32 v78, v78
	v_mul_f32_e32 v79, v79, v82
	v_max_f32_e32 v79, 0xc2a00000, v79
	v_mul_f32_e32 v75, v75, v82
	v_mul_f32_e32 v79, 0xbfb8aa3b, v79
	v_add_f32_e32 v74, 1.0, v74
	v_max_f32_e32 v75, 0xc2a00000, v75
	v_cvt_pk_f16_f32 v84, v86, v87
	v_cvt_pk_f16_f32 v85, v88, v89
	v_cvt_pk_f16_f32 v86, v90, v91
	v_cvt_pk_f16_f32 v87, v92, v93
	v_exp_f32_e32 v79, v79
	v_add_f32_e32 v78, 1.0, v78
	v_rcp_f32_e32 v74, v74
	v_mul_f32_e32 v75, 0xbfb8aa3b, v75
	s_waitcnt lgkmcnt(6)
	v_subrev_u32_e32 v236, s82, v236
	global_store_dwordx4 v236, v[232:235], s[82:83] offset:64 sc1
	ds_bpermute_b32 v244, v250, v84
	ds_bpermute_b32 v245, v250, v85
	ds_bpermute_b32 v246, v250, v86
	ds_bpermute_b32 v247, v250, v87
	ds_bpermute_b32 v248, v250, v94
	v_exp_f32_e32 v75, v75
	v_mul_f32_e32 v80, v80, v82
	v_rcp_f32_e32 v86, v78
	v_or_b32_e32 v84, 48, v152
	v_mul_f32_e32 v81, v81, v82
	v_ashrrev_i32_e32 v85, 31, v84
	v_add_f32_e32 v78, 1.0, v79
	v_max_f32_e32 v80, 0xc2a00000, v80
	v_max_f32_e32 v81, 0xc2a00000, v81
	v_fma_f32 v74, v171, v74, v132
	v_rcp_f32_e32 v87, v78
	v_lshlrev_b64 v[78:79], 12, v[84:85]
	v_fma_f32 v84, v180, v86, v136
	v_mul_f32_e32 v80, 0xbfb8aa3b, v80
	v_mul_f32_e32 v81, 0xbfb8aa3b, v81
	v_log_f32_e32 v86, v74
	v_add_f32_e32 v74, 1.0, v75
	v_mul_f32_e32 v75, v76, v82
	v_exp_f32_e32 v80, v80
	v_exp_f32_e32 v81, v81
	v_max_f32_e32 v75, 0xc2a00000, v75
	v_mul_f32_e32 v76, v77, v82
	v_mul_f32_e32 v75, 0xbfb8aa3b, v75
	v_max_f32_e32 v76, 0xc2a00000, v76
	v_exp_f32_e32 v75, v75
	v_mul_f32_e32 v76, 0xbfb8aa3b, v76
	v_exp_f32_e32 v76, v76
	v_add_f32_e32 v80, 1.0, v80
	v_add_f32_e32 v81, 1.0, v81
	v_rcp_f32_e32 v80, v80
	v_rcp_f32_e32 v81, v81
	v_mul_f32_e32 v66, v66, v82
	v_rcp_f32_e32 v74, v74
	v_add_f32_e32 v75, 1.0, v75
	v_max_f32_e32 v66, 0xc2a00000, v66
	v_rcp_f32_e32 v75, v75
	v_add_f32_e32 v76, 1.0, v76
	v_mul_f32_e32 v66, 0xbfb8aa3b, v66
	v_rcp_f32_e32 v76, v76
	v_exp_f32_e32 v66, v66
	v_fma_f32 v80, v178, v80, v138
	v_fma_f32 v81, v177, v81, v139
	v_log_f32_e32 v80, v80
	v_log_f32_e32 v81, v81
	v_fma_f32 v74, v170, v74, v133
	v_log_f32_e32 v77, v74
	v_fma_f32 v74, v169, v75, v134
	v_mul_f32_e32 v70, v70, v82
	v_mul_f32_e32 v67, v67, v82
	v_fma_f32 v85, v179, v87, v137
	v_log_f32_e32 v87, v74
	v_fma_f32 v74, v155, v76, v135
	v_max_f32_e32 v70, 0xc2a00000, v70
	v_add_f32_e32 v66, 1.0, v66
	v_max_f32_e32 v67, 0xc2a00000, v67
	v_log_f32_e32 v84, v84
	v_log_f32_e32 v85, v85
	v_log_f32_e32 v88, v74
	v_mul_f32_e32 v70, 0xbfb8aa3b, v70
	v_rcp_f32_e32 v66, v66
	v_mul_f32_e32 v67, 0xbfb8aa3b, v67
	v_cvt_pk_f16_f32 v75, v80, v81
	v_exp_f32_e32 v80, v70
	v_mul_f32_e32 v70, v71, v82
	v_exp_f32_e32 v67, v67
	v_max_f32_e32 v70, 0xc2a00000, v70
	v_lshl_add_u64 v[78:79], s[26:27], 0, v[78:79]
	v_mul_f32_e32 v70, 0xbfb8aa3b, v70
	v_cvt_pk_f16_f32 v74, v84, v85
	v_cvt_pk_f16_f32 v76, v86, v77
	v_cvt_pk_f16_f32 v77, v87, v88
	v_exp_f32_e32 v81, v70
	v_lshl_add_u64 v[70:71], v[78:79], 0, v[114:115]
	v_fma_f32 v66, v123, v66, v124
	s_waitcnt lgkmcnt(6)
	v_subrev_u32_e32 v242, s82, v242
	global_store_dwordx4 v242, v[238:241], s[82:83] sc1
	ds_bpermute_b32 v232, v250, v74
	ds_bpermute_b32 v233, v250, v75
	ds_bpermute_b32 v234, v250, v76
	ds_bpermute_b32 v235, v250, v77
	ds_bpermute_b32 v236, v250, v70
	v_mul_f32_e32 v72, v72, v82
	v_mul_f32_e32 v73, v73, v82
	v_log_f32_e32 v76, v66
	v_add_f32_e32 v66, 1.0, v67
	v_mul_f32_e32 v67, v68, v82
	v_max_f32_e32 v67, 0xc2a00000, v67
	v_mul_f32_e32 v68, v69, v82
	v_max_f32_e32 v72, 0xc2a00000, v72
	v_max_f32_e32 v73, 0xc2a00000, v73
	v_mul_f32_e32 v67, 0xbfb8aa3b, v67
	v_max_f32_e32 v68, 0xc2a00000, v68
	v_mul_f32_e32 v72, 0xbfb8aa3b, v72
	v_mul_f32_e32 v73, 0xbfb8aa3b, v73
	v_exp_f32_e32 v67, v67
	v_mul_f32_e32 v68, 0xbfb8aa3b, v68
	v_exp_f32_e32 v72, v72
	v_exp_f32_e32 v73, v73
	v_exp_f32_e32 v68, v68
	v_mul_f32_e32 v58, v58, v83
	v_rcp_f32_e32 v66, v66
	v_add_f32_e32 v67, 1.0, v67
	v_max_f32_e32 v58, 0xc2a00000, v58
	v_add_f32_e32 v78, 1.0, v80
	v_add_f32_e32 v79, 1.0, v81
	v_add_f32_e32 v72, 1.0, v72
	v_add_f32_e32 v73, 1.0, v73
	v_rcp_f32_e32 v67, v67
	v_add_f32_e32 v68, 1.0, v68
	v_mul_f32_e32 v58, 0xbfb8aa3b, v58
	v_rcp_f32_e32 v78, v78
	v_rcp_f32_e32 v79, v79
	v_rcp_f32_e32 v72, v72
	v_rcp_f32_e32 v73, v73
	v_rcp_f32_e32 v68, v68
	v_exp_f32_e32 v58, v58
	v_fma_f32 v66, v120, v66, v125
	v_log_f32_e32 v69, v66
	v_fma_f32 v66, v118, v67, v126
	v_mul_f32_e32 v59, v59, v83
	v_fma_f32 v74, v153, v78, v128
	v_fma_f32 v75, v168, v79, v129
	v_fma_f32 v72, v121, v72, v130
	v_fma_f32 v73, v122, v73, v131
	v_log_f32_e32 v77, v66
	v_fma_f32 v66, v119, v68, v127
	v_add_f32_e32 v58, 1.0, v58
	v_max_f32_e32 v59, 0xc2a00000, v59
	v_log_f32_e32 v74, v74
	v_log_f32_e32 v75, v75
	v_log_f32_e32 v72, v72
	v_log_f32_e32 v73, v73
	v_log_f32_e32 v78, v66
	v_rcp_f32_e32 v58, v58
	v_mul_f32_e32 v59, 0xbfb8aa3b, v59
	v_exp_f32_e32 v59, v59
	v_mul_f32_e32 v64, v64, v83
	v_mul_f32_e32 v65, v65, v83
	v_max_f32_e32 v64, 0xc2a00000, v64
	v_max_f32_e32 v65, 0xc2a00000, v65
	v_cvt_pk_f16_f32 v66, v74, v75
	v_cvt_pk_f16_f32 v67, v72, v73
	v_cvt_pk_f16_f32 v68, v76, v69
	v_mul_f32_e32 v62, v62, v83
	v_mul_f32_e32 v63, v63, v83
	v_cvt_pk_f16_f32 v69, v77, v78
	v_mul_f32_e32 v64, 0xbfb8aa3b, v64
	v_mul_f32_e32 v65, 0xbfb8aa3b, v65
	v_fma_f32 v58, v171, v58, v132
	v_max_f32_e32 v62, 0xc2a00000, v62
	v_max_f32_e32 v63, 0xc2a00000, v63
	s_waitcnt lgkmcnt(5)
	v_subrev_u32_e32 v248, s82, v248
	global_store_dwordx4 v248, v[244:247], s[82:83] offset:64 sc1
	ds_bpermute_b32 v238, v250, v66
	ds_bpermute_b32 v239, v250, v67
	ds_bpermute_b32 v240, v250, v68
	ds_bpermute_b32 v241, v250, v69
	ds_bpermute_b32 v242, v250, v70
	v_exp_f32_e32 v64, v64
	v_exp_f32_e32 v65, v65
	v_log_f32_e32 v66, v58
	v_add_f32_e32 v58, 1.0, v59
	v_mul_f32_e32 v59, v60, v83
	v_mul_f32_e32 v62, 0xbfb8aa3b, v62
	v_mul_f32_e32 v63, 0xbfb8aa3b, v63
	v_max_f32_e32 v59, 0xc2a00000, v59
	v_mul_f32_e32 v60, v61, v83
	v_exp_f32_e32 v62, v62
	v_exp_f32_e32 v63, v63
	v_mul_f32_e32 v59, 0xbfb8aa3b, v59
	v_max_f32_e32 v60, 0xc2a00000, v60
	v_exp_f32_e32 v59, v59
	v_mul_f32_e32 v60, 0xbfb8aa3b, v60
	v_add_f32_e32 v64, 1.0, v64
	v_add_f32_e32 v65, 1.0, v65
	v_exp_f32_e32 v60, v60
	v_rcp_f32_e32 v64, v64
	v_rcp_f32_e32 v65, v65
	v_add_f32_e32 v62, 1.0, v62
	v_add_f32_e32 v63, 1.0, v63
	v_mul_f32_e32 v50, v50, v83
	v_rcp_f32_e32 v62, v62
	v_rcp_f32_e32 v63, v63
	v_rcp_f32_e32 v58, v58
	v_add_f32_e32 v59, 1.0, v59
	v_max_f32_e32 v50, 0xc2a00000, v50
	v_rcp_f32_e32 v59, v59
	v_add_f32_e32 v60, 1.0, v60
	v_mul_f32_e32 v50, 0xbfb8aa3b, v50
	v_fma_f32 v64, v178, v64, v138
	v_fma_f32 v65, v177, v65, v139
	v_rcp_f32_e32 v60, v60
	v_exp_f32_e32 v50, v50
	v_log_f32_e32 v64, v64
	v_log_f32_e32 v65, v65
	v_fma_f32 v62, v180, v62, v136
	v_fma_f32 v63, v179, v63, v137
	v_fma_f32 v58, v170, v58, v133
	v_mul_f32_e32 v54, v54, v83
	v_log_f32_e32 v62, v62
	v_log_f32_e32 v63, v63
	v_log_f32_e32 v61, v58
	v_fma_f32 v58, v169, v59, v134
	v_max_f32_e32 v54, 0xc2a00000, v54
	v_mul_f32_e32 v51, v51, v83
	v_log_f32_e32 v67, v58
	v_fma_f32 v58, v155, v60, v135
	v_mul_f32_e32 v54, 0xbfb8aa3b, v54
	v_add_f32_e32 v50, 1.0, v50
	v_max_f32_e32 v51, 0xc2a00000, v51
	v_log_f32_e32 v68, v58
	v_cvt_pk_f16_f32 v59, v64, v65
	v_exp_f32_e32 v64, v54
	v_mul_f32_e32 v54, v55, v83
	v_rcp_f32_e32 v50, v50
	v_mul_f32_e32 v51, 0xbfb8aa3b, v51
	v_max_f32_e32 v54, 0xc2a00000, v54
	v_exp_f32_e32 v51, v51
	v_cvt_pk_f16_f32 v58, v62, v63
	v_lshl_add_u64 v[62:63], v[166:167], 0, s[14:15]
	v_mul_f32_e32 v54, 0xbfb8aa3b, v54
	s_mov_b32 s14, 0x80000
	v_exp_f32_e32 v65, v54
	v_add_co_u32_e32 v54, vcc, s14, v166
	v_cvt_pk_f16_f32 v60, v66, v61
	v_cvt_pk_f16_f32 v61, v67, v68
	v_addc_co_u32_e32 v55, vcc, 0, v167, vcc
	v_fma_f32 v50, v123, v50, v124
	s_waitcnt lgkmcnt(5)
	v_subrev_u32_e32 v236, s82, v236
	global_store_dwordx4 v236, v[232:235], s[82:83] sc1
	ds_bpermute_b32 v244, v250, v58
	ds_bpermute_b32 v245, v250, v59
	ds_bpermute_b32 v246, v250, v60
	ds_bpermute_b32 v247, v250, v61
	ds_bpermute_b32 v248, v250, v54
	v_mul_f32_e32 v56, v56, v83
	v_mul_f32_e32 v57, v57, v83
	v_log_f32_e32 v58, v50
	v_add_f32_e32 v50, 1.0, v51
	v_mul_f32_e32 v51, v52, v83
	v_max_f32_e32 v51, 0xc2a00000, v51
	v_mul_f32_e32 v51, 0xbfb8aa3b, v51
	v_exp_f32_e32 v51, v51
	v_rcp_f32_e32 v50, v50
	v_mul_f32_e32 v52, v53, v83
	v_max_f32_e32 v56, 0xc2a00000, v56
	v_add_f32_e32 v51, 1.0, v51
	v_rcp_f32_e32 v51, v51
	v_fma_f32 v50, v120, v50, v125
	v_log_f32_e32 v59, v50
	v_max_f32_e32 v57, 0xc2a00000, v57
	v_fma_f32 v50, v118, v51, v126
	v_log_f32_e32 v60, v50
	ds_read2_b32 v[50:51], v176 offset0:144 offset1:160
	v_max_f32_e32 v52, 0xc2a00000, v52
	v_mul_f32_e32 v56, 0xbfb8aa3b, v56
	v_mul_f32_e32 v57, 0xbfb8aa3b, v57
	v_mul_f32_e32 v52, 0xbfb8aa3b, v52
	v_exp_f32_e32 v56, v56
	v_exp_f32_e32 v57, v57
	v_exp_f32_e32 v52, v52
	s_waitcnt lgkmcnt(0)
	v_mul_f32_e32 v42, v42, v50
	v_max_f32_e32 v42, 0xc2a00000, v42
	v_add_f32_e32 v64, 1.0, v64
	v_add_f32_e32 v65, 1.0, v65
	v_add_f32_e32 v56, 1.0, v56
	v_add_f32_e32 v57, 1.0, v57
	v_add_f32_e32 v52, 1.0, v52
	v_mul_f32_e32 v42, 0xbfb8aa3b, v42
	v_rcp_f32_e32 v64, v64
	v_rcp_f32_e32 v65, v65
	v_rcp_f32_e32 v56, v56
	v_rcp_f32_e32 v57, v57
	v_rcp_f32_e32 v52, v52
	v_exp_f32_e32 v42, v42
	v_mul_f32_e32 v43, v43, v50
	v_fma_f32 v54, v153, v64, v128
	v_fma_f32 v55, v168, v65, v129
	v_fma_f32 v56, v121, v56, v130
	v_fma_f32 v57, v122, v57, v131
	v_fma_f32 v52, v119, v52, v127
	v_add_f32_e32 v42, 1.0, v42
	v_max_f32_e32 v43, 0xc2a00000, v43
	v_log_f32_e32 v54, v54
	v_log_f32_e32 v55, v55
	v_log_f32_e32 v56, v56
	v_log_f32_e32 v57, v57
	v_log_f32_e32 v61, v52
	v_rcp_f32_e32 v42, v42
	v_mul_f32_e32 v43, 0xbfb8aa3b, v43
	v_exp_f32_e32 v43, v43
	v_mul_f32_e32 v48, v48, v50
	v_mul_f32_e32 v49, v49, v50
	v_max_f32_e32 v48, 0xc2a00000, v48
	v_max_f32_e32 v49, 0xc2a00000, v49
	v_cvt_pk_f16_f32 v52, v54, v55
	v_cvt_pk_f16_f32 v53, v56, v57
	v_cvt_pk_f16_f32 v54, v58, v59
	v_mul_f32_e32 v46, v46, v50
	v_mul_f32_e32 v47, v47, v50
	v_cvt_pk_f16_f32 v55, v60, v61
	v_mul_f32_e32 v48, 0xbfb8aa3b, v48
	v_mul_f32_e32 v49, 0xbfb8aa3b, v49
	v_fma_f32 v42, v171, v42, v132
	v_max_f32_e32 v46, 0xc2a00000, v46
	v_max_f32_e32 v47, 0xc2a00000, v47
	s_waitcnt lgkmcnt(6)
	v_subrev_u32_e32 v242, s82, v242
	global_store_dwordx4 v242, v[238:241], s[82:83] offset:64 sc1
	ds_bpermute_b32 v232, v250, v52
	ds_bpermute_b32 v233, v250, v53
	ds_bpermute_b32 v234, v250, v54
	ds_bpermute_b32 v235, v250, v55
	ds_bpermute_b32 v236, v250, v62
	v_exp_f32_e32 v48, v48
	v_exp_f32_e32 v49, v49
	v_log_f32_e32 v52, v42
	v_add_f32_e32 v42, 1.0, v43
	v_mul_f32_e32 v43, v44, v50
	v_mul_f32_e32 v46, 0xbfb8aa3b, v46
	v_mul_f32_e32 v47, 0xbfb8aa3b, v47
	v_max_f32_e32 v43, 0xc2a00000, v43
	v_mul_f32_e32 v44, v45, v50
	v_exp_f32_e32 v46, v46
	v_exp_f32_e32 v47, v47
	v_mul_f32_e32 v43, 0xbfb8aa3b, v43
	v_max_f32_e32 v44, 0xc2a00000, v44
	v_exp_f32_e32 v43, v43
	v_mul_f32_e32 v44, 0xbfb8aa3b, v44
	v_add_f32_e32 v48, 1.0, v48
	v_add_f32_e32 v49, 1.0, v49
	v_exp_f32_e32 v44, v44
	v_rcp_f32_e32 v48, v48
	v_rcp_f32_e32 v49, v49
	v_add_f32_e32 v46, 1.0, v46
	v_add_f32_e32 v47, 1.0, v47
	v_mul_f32_e32 v34, v34, v50
	v_rcp_f32_e32 v46, v46
	v_rcp_f32_e32 v47, v47
	v_rcp_f32_e32 v42, v42
	v_add_f32_e32 v43, 1.0, v43
	v_max_f32_e32 v34, 0xc2a00000, v34
	v_rcp_f32_e32 v43, v43
	v_add_f32_e32 v44, 1.0, v44
	v_mul_f32_e32 v34, 0xbfb8aa3b, v34
	v_fma_f32 v48, v178, v48, v138
	v_fma_f32 v49, v177, v49, v139
	v_rcp_f32_e32 v44, v44
	v_exp_f32_e32 v34, v34
	v_log_f32_e32 v48, v48
	v_log_f32_e32 v49, v49
	v_fma_f32 v46, v180, v46, v136
	v_fma_f32 v47, v179, v47, v137
	v_fma_f32 v42, v170, v42, v133
	v_mul_f32_e32 v38, v38, v50
	v_log_f32_e32 v46, v46
	v_log_f32_e32 v47, v47
	v_log_f32_e32 v45, v42
	v_fma_f32 v42, v169, v43, v134
	v_max_f32_e32 v38, 0xc2a00000, v38
	v_mul_f32_e32 v35, v35, v50
	v_log_f32_e32 v53, v42
	v_fma_f32 v42, v155, v44, v135
	v_mul_f32_e32 v38, 0xbfb8aa3b, v38
	v_add_f32_e32 v34, 1.0, v34
	v_max_f32_e32 v35, 0xc2a00000, v35
	v_log_f32_e32 v54, v42
	v_cvt_pk_f16_f32 v43, v48, v49
	v_exp_f32_e32 v48, v38
	v_mul_f32_e32 v38, v39, v50
	v_rcp_f32_e32 v34, v34
	v_mul_f32_e32 v35, 0xbfb8aa3b, v35
	s_mov_b64 s[14:15], 0x90000
	v_max_f32_e32 v38, 0xc2a00000, v38
	v_exp_f32_e32 v35, v35
	v_cvt_pk_f16_f32 v42, v46, v47
	v_lshl_add_u64 v[46:47], v[166:167], 0, s[14:15]
	v_mul_f32_e32 v38, 0xbfb8aa3b, v38
	s_mov_b32 s14, 0x90000
	v_exp_f32_e32 v49, v38
	v_add_co_u32_e32 v38, vcc, s14, v166
	v_cvt_pk_f16_f32 v44, v52, v45
	v_cvt_pk_f16_f32 v45, v53, v54
	v_addc_co_u32_e32 v39, vcc, 0, v167, vcc
	v_fma_f32 v34, v123, v34, v124
	s_waitcnt lgkmcnt(6)
	v_subrev_u32_e32 v248, s82, v248
	global_store_dwordx4 v248, v[244:247], s[82:83] sc1
	ds_bpermute_b32 v238, v250, v42
	ds_bpermute_b32 v239, v250, v43
	ds_bpermute_b32 v240, v250, v44
	ds_bpermute_b32 v241, v250, v45
	ds_bpermute_b32 v242, v250, v38
	v_mul_f32_e32 v40, v40, v50
	v_mul_f32_e32 v41, v41, v50
	v_log_f32_e32 v42, v34
	v_add_f32_e32 v34, 1.0, v35
	v_mul_f32_e32 v35, v36, v50
	v_max_f32_e32 v35, 0xc2a00000, v35
	v_mul_f32_e32 v36, v37, v50
	v_max_f32_e32 v40, 0xc2a00000, v40
	v_max_f32_e32 v41, 0xc2a00000, v41
	v_mul_f32_e32 v35, 0xbfb8aa3b, v35
	v_max_f32_e32 v36, 0xc2a00000, v36
	v_mul_f32_e32 v40, 0xbfb8aa3b, v40
	v_mul_f32_e32 v41, 0xbfb8aa3b, v41
	v_exp_f32_e32 v35, v35
	v_mul_f32_e32 v36, 0xbfb8aa3b, v36
	v_exp_f32_e32 v40, v40
	v_exp_f32_e32 v41, v41
	v_exp_f32_e32 v36, v36
	v_mul_f32_e32 v26, v26, v51
	v_rcp_f32_e32 v34, v34
	v_add_f32_e32 v35, 1.0, v35
	v_max_f32_e32 v26, 0xc2a00000, v26
	v_add_f32_e32 v48, 1.0, v48
	v_add_f32_e32 v49, 1.0, v49
	v_add_f32_e32 v40, 1.0, v40
	v_add_f32_e32 v41, 1.0, v41
	v_rcp_f32_e32 v35, v35
	v_add_f32_e32 v36, 1.0, v36
	v_mul_f32_e32 v26, 0xbfb8aa3b, v26
	v_rcp_f32_e32 v48, v48
	v_rcp_f32_e32 v49, v49
	v_rcp_f32_e32 v40, v40
	v_rcp_f32_e32 v41, v41
	v_rcp_f32_e32 v36, v36
	v_exp_f32_e32 v26, v26
	v_fma_f32 v34, v120, v34, v125
	v_log_f32_e32 v37, v34
	v_fma_f32 v34, v118, v35, v126
	v_mul_f32_e32 v27, v27, v51
	v_fma_f32 v38, v153, v48, v128
	v_fma_f32 v39, v168, v49, v129
	v_fma_f32 v40, v121, v40, v130
	v_fma_f32 v41, v122, v41, v131
	v_log_f32_e32 v43, v34
	v_fma_f32 v34, v119, v36, v127
	v_add_f32_e32 v26, 1.0, v26
	v_max_f32_e32 v27, 0xc2a00000, v27
	v_log_f32_e32 v38, v38
	v_log_f32_e32 v39, v39
	v_log_f32_e32 v40, v40
	v_log_f32_e32 v41, v41
	v_log_f32_e32 v44, v34
	v_rcp_f32_e32 v26, v26
	v_mul_f32_e32 v27, 0xbfb8aa3b, v27
	v_exp_f32_e32 v27, v27
	v_mul_f32_e32 v32, v32, v51
	v_mul_f32_e32 v33, v33, v51
	v_max_f32_e32 v32, 0xc2a00000, v32
	v_max_f32_e32 v33, 0xc2a00000, v33
	v_cvt_pk_f16_f32 v34, v38, v39
	v_cvt_pk_f16_f32 v35, v40, v41
	v_cvt_pk_f16_f32 v36, v42, v37
	v_mul_f32_e32 v30, v30, v51
	v_mul_f32_e32 v31, v31, v51
	v_cvt_pk_f16_f32 v37, v43, v44
	v_mul_f32_e32 v32, 0xbfb8aa3b, v32
	v_mul_f32_e32 v33, 0xbfb8aa3b, v33
	v_fma_f32 v26, v171, v26, v132
	v_max_f32_e32 v30, 0xc2a00000, v30
	v_max_f32_e32 v31, 0xc2a00000, v31
	s_waitcnt lgkmcnt(5)
	v_subrev_u32_e32 v236, s82, v236
	global_store_dwordx4 v236, v[232:235], s[82:83] offset:64 sc1
	ds_bpermute_b32 v244, v250, v34
	ds_bpermute_b32 v245, v250, v35
	ds_bpermute_b32 v246, v250, v36
	ds_bpermute_b32 v247, v250, v37
	ds_bpermute_b32 v248, v250, v46
	v_exp_f32_e32 v32, v32
	v_exp_f32_e32 v33, v33
	v_log_f32_e32 v34, v26
	v_add_f32_e32 v26, 1.0, v27
	v_mul_f32_e32 v27, v28, v51
	v_mul_f32_e32 v30, 0xbfb8aa3b, v30
	v_mul_f32_e32 v31, 0xbfb8aa3b, v31
	v_max_f32_e32 v27, 0xc2a00000, v27
	v_mul_f32_e32 v28, v29, v51
	v_exp_f32_e32 v30, v30
	v_exp_f32_e32 v31, v31
	v_mul_f32_e32 v27, 0xbfb8aa3b, v27
	v_max_f32_e32 v28, 0xc2a00000, v28
	v_exp_f32_e32 v27, v27
	v_mul_f32_e32 v28, 0xbfb8aa3b, v28
	v_add_f32_e32 v32, 1.0, v32
	v_add_f32_e32 v33, 1.0, v33
	v_exp_f32_e32 v28, v28
	v_rcp_f32_e32 v32, v32
	v_rcp_f32_e32 v33, v33
	v_add_f32_e32 v30, 1.0, v30
	v_add_f32_e32 v31, 1.0, v31
	v_mul_f32_e32 v18, v18, v51
	v_rcp_f32_e32 v30, v30
	v_rcp_f32_e32 v31, v31
	v_rcp_f32_e32 v26, v26
	v_add_f32_e32 v27, 1.0, v27
	v_max_f32_e32 v18, 0xc2a00000, v18
	v_rcp_f32_e32 v27, v27
	v_add_f32_e32 v28, 1.0, v28
	v_mul_f32_e32 v18, 0xbfb8aa3b, v18
	v_fma_f32 v32, v178, v32, v138
	v_fma_f32 v33, v177, v33, v139
	v_rcp_f32_e32 v28, v28
	v_exp_f32_e32 v18, v18
	v_log_f32_e32 v32, v32
	v_log_f32_e32 v33, v33
	v_fma_f32 v30, v180, v30, v136
	v_fma_f32 v31, v179, v31, v137
	v_fma_f32 v26, v170, v26, v133
	v_mul_f32_e32 v22, v22, v51
	v_log_f32_e32 v30, v30
	v_log_f32_e32 v31, v31
	v_log_f32_e32 v29, v26
	v_fma_f32 v26, v169, v27, v134
	v_max_f32_e32 v22, 0xc2a00000, v22
	v_mul_f32_e32 v19, v19, v51
	v_log_f32_e32 v35, v26
	v_fma_f32 v26, v155, v28, v135
	v_mul_f32_e32 v22, 0xbfb8aa3b, v22
	v_add_f32_e32 v18, 1.0, v18
	v_max_f32_e32 v19, 0xc2a00000, v19
	v_log_f32_e32 v36, v26
	v_cvt_pk_f16_f32 v27, v32, v33
	v_exp_f32_e32 v32, v22
	v_mul_f32_e32 v22, v23, v51
	v_rcp_f32_e32 v18, v18
	v_mul_f32_e32 v19, 0xbfb8aa3b, v19
	s_mov_b64 s[14:15], 0xa0000
	v_max_f32_e32 v22, 0xc2a00000, v22
	v_exp_f32_e32 v19, v19
	v_cvt_pk_f16_f32 v26, v30, v31
	v_lshl_add_u64 v[30:31], v[166:167], 0, s[14:15]
	v_mul_f32_e32 v22, 0xbfb8aa3b, v22
	s_mov_b32 s14, 0xa0000
	v_exp_f32_e32 v33, v22
	v_add_co_u32_e32 v22, vcc, s14, v166
	v_cvt_pk_f16_f32 v28, v34, v29
	v_cvt_pk_f16_f32 v29, v35, v36
	v_addc_co_u32_e32 v23, vcc, 0, v167, vcc
	v_fma_f32 v18, v123, v18, v124
	s_waitcnt lgkmcnt(5)
	v_subrev_u32_e32 v242, s82, v242
	global_store_dwordx4 v242, v[238:241], s[82:83] sc1
	ds_bpermute_b32 v232, v250, v26
	ds_bpermute_b32 v233, v250, v27
	ds_bpermute_b32 v234, v250, v28
	ds_bpermute_b32 v235, v250, v29
	ds_bpermute_b32 v236, v250, v22
	v_mul_f32_e32 v24, v24, v51
	v_mul_f32_e32 v25, v25, v51
	v_log_f32_e32 v26, v18
	v_add_f32_e32 v18, 1.0, v19
	v_mul_f32_e32 v19, v20, v51
	v_max_f32_e32 v19, 0xc2a00000, v19
	v_mul_f32_e32 v20, v21, v51
	ds_read_b32 v28, v176 offset:704
	v_max_f32_e32 v24, 0xc2a00000, v24
	v_max_f32_e32 v25, 0xc2a00000, v25
	v_mul_f32_e32 v19, 0xbfb8aa3b, v19
	v_max_f32_e32 v20, 0xc2a00000, v20
	v_mul_f32_e32 v24, 0xbfb8aa3b, v24
	v_mul_f32_e32 v25, 0xbfb8aa3b, v25
	v_exp_f32_e32 v19, v19
	v_mul_f32_e32 v20, 0xbfb8aa3b, v20
	v_exp_f32_e32 v24, v24
	v_exp_f32_e32 v25, v25
	v_exp_f32_e32 v20, v20
	s_waitcnt lgkmcnt(0)
	v_mul_f32_e32 v10, v10, v28
	v_rcp_f32_e32 v18, v18
	v_add_f32_e32 v19, 1.0, v19
	v_max_f32_e32 v10, 0xc2a00000, v10
	v_add_f32_e32 v32, 1.0, v32
	v_add_f32_e32 v33, 1.0, v33
	v_add_f32_e32 v24, 1.0, v24
	v_add_f32_e32 v25, 1.0, v25
	v_rcp_f32_e32 v19, v19
	v_add_f32_e32 v20, 1.0, v20
	v_mul_f32_e32 v10, 0xbfb8aa3b, v10
	v_rcp_f32_e32 v32, v32
	v_rcp_f32_e32 v33, v33
	v_rcp_f32_e32 v24, v24
	v_rcp_f32_e32 v25, v25
	v_rcp_f32_e32 v20, v20
	v_exp_f32_e32 v10, v10
	v_fma_f32 v18, v120, v18, v125
	v_log_f32_e32 v21, v18
	v_fma_f32 v18, v118, v19, v126
	v_mul_f32_e32 v11, v11, v28
	v_fma_f32 v22, v153, v32, v128
	v_fma_f32 v23, v168, v33, v129
	v_fma_f32 v24, v121, v24, v130
	v_fma_f32 v25, v122, v25, v131
	v_log_f32_e32 v27, v18
	v_fma_f32 v18, v119, v20, v127
	v_add_f32_e32 v10, 1.0, v10
	v_max_f32_e32 v11, 0xc2a00000, v11
	v_log_f32_e32 v22, v22
	v_log_f32_e32 v23, v23
	v_log_f32_e32 v24, v24
	v_log_f32_e32 v25, v25
	v_log_f32_e32 v29, v18
	v_rcp_f32_e32 v10, v10
	v_mul_f32_e32 v11, 0xbfb8aa3b, v11
	v_mul_f32_e32 v14, v14, v28
	v_mul_f32_e32 v15, v15, v28
	v_exp_f32_e32 v11, v11
	v_max_f32_e32 v14, 0xc2a00000, v14
	v_max_f32_e32 v15, 0xc2a00000, v15
	v_mul_f32_e32 v14, 0xbfb8aa3b, v14
	v_mul_f32_e32 v15, 0xbfb8aa3b, v15
	v_cvt_pk_f16_f32 v18, v22, v23
	v_cvt_pk_f16_f32 v19, v24, v25
	v_cvt_pk_f16_f32 v20, v26, v21
	v_exp_f32_e32 v14, v14
	v_exp_f32_e32 v15, v15
	v_cvt_pk_f16_f32 v21, v27, v29
	v_fma_f32 v10, v171, v10, v132
	s_waitcnt lgkmcnt(6)
	v_subrev_u32_e32 v248, s82, v248
	global_store_dwordx4 v248, v[244:247], s[82:83] offset:64 sc1
	ds_bpermute_b32 v238, v250, v18
	ds_bpermute_b32 v239, v250, v19
	ds_bpermute_b32 v240, v250, v20
	ds_bpermute_b32 v241, v250, v21
	ds_bpermute_b32 v242, v250, v30
	v_add_f32_e32 v14, 1.0, v14
	v_add_f32_e32 v15, 1.0, v15
	v_log_f32_e32 v18, v10
	v_add_f32_e32 v10, 1.0, v11
	v_mul_f32_e32 v11, v12, v28
	v_max_f32_e32 v11, 0xc2a00000, v11
	v_mul_f32_e32 v11, 0xbfb8aa3b, v11
	v_exp_f32_e32 v11, v11
	v_rcp_f32_e32 v14, v14
	v_rcp_f32_e32 v15, v15
	v_mul_f32_e32 v16, v16, v28
	v_mul_f32_e32 v17, v17, v28
	v_rcp_f32_e32 v10, v10
	v_mul_f32_e32 v12, v13, v28
	v_add_f32_e32 v11, 1.0, v11
	v_fma_f32 v14, v180, v14, v136
	v_fma_f32 v15, v179, v15, v137
	v_max_f32_e32 v16, 0xc2a00000, v16
	v_max_f32_e32 v17, 0xc2a00000, v17
	v_max_f32_e32 v12, 0xc2a00000, v12
	v_rcp_f32_e32 v11, v11
	v_log_f32_e32 v14, v14
	v_mul_f32_e32 v16, 0xbfb8aa3b, v16
	v_mul_f32_e32 v17, 0xbfb8aa3b, v17
	v_log_f32_e32 v15, v15
	v_mul_f32_e32 v12, 0xbfb8aa3b, v12
	v_exp_f32_e32 v16, v16
	v_exp_f32_e32 v17, v17
	v_exp_f32_e32 v12, v12
	v_mul_f32_e32 v6, v6, v28
	v_fma_f32 v10, v170, v10, v133
	v_max_f32_e32 v6, 0xc2a00000, v6
	v_log_f32_e32 v13, v10
	v_fma_f32 v10, v169, v11, v134
	v_mul_f32_e32 v6, 0xbfb8aa3b, v6
	v_log_f32_e32 v19, v10
	v_cvt_pk_f16_f32 v10, v14, v15
	v_exp_f32_e32 v14, v6
	v_mul_f32_e32 v6, v7, v28
	v_mul_f32_e32 v8, v8, v28
	v_mul_f32_e32 v9, v9, v28
	v_mul_f32_e32 v2, v2, v28
	v_mul_f32_e32 v3, v3, v28
	v_mul_f32_e32 v4, v4, v28
	v_mul_f32_e32 v5, v5, v28
	v_add_f32_e32 v16, 1.0, v16
	v_add_f32_e32 v17, 1.0, v17
	v_add_f32_e32 v12, 1.0, v12
	v_max_f32_e32 v6, 0xc2a00000, v6
	v_max_f32_e32 v8, 0xc2a00000, v8
	v_max_f32_e32 v9, 0xc2a00000, v9
	v_max_f32_e32 v2, 0xc2a00000, v2
	v_max_f32_e32 v3, 0xc2a00000, v3
	v_max_f32_e32 v4, 0xc2a00000, v4
	v_max_f32_e32 v5, 0xc2a00000, v5
	v_rcp_f32_e32 v16, v16
	v_rcp_f32_e32 v17, v17
	v_rcp_f32_e32 v12, v12
	v_mul_f32_e32 v6, 0xbfb8aa3b, v6
	v_mul_f32_e32 v8, 0xbfb8aa3b, v8
	v_mul_f32_e32 v9, 0xbfb8aa3b, v9
	v_mul_f32_e32 v2, 0xbfb8aa3b, v2
	v_mul_f32_e32 v3, 0xbfb8aa3b, v3
	v_mul_f32_e32 v4, 0xbfb8aa3b, v4
	v_mul_f32_e32 v5, 0xbfb8aa3b, v5
	v_exp_f32_e32 v15, v6
	v_exp_f32_e32 v8, v8
	v_exp_f32_e32 v9, v9
	v_exp_f32_e32 v2, v2
	v_exp_f32_e32 v3, v3
	v_exp_f32_e32 v4, v4
	v_exp_f32_e32 v5, v5
	v_fma_f32 v16, v178, v16, v138
	v_fmac_f32_e32 v139, v177, v17
	v_fmac_f32_e32 v135, v155, v12
	v_log_f32_e32 v16, v16
	v_log_f32_e32 v17, v139
	v_log_f32_e32 v20, v135
	v_add_f32_e32 v14, 1.0, v14
	v_add_f32_e32 v15, 1.0, v15
	v_add_f32_e32 v8, 1.0, v8
	v_add_f32_e32 v9, 1.0, v9
	v_add_f32_e32 v2, 1.0, v2
	v_add_f32_e32 v3, 1.0, v3
	v_add_f32_e32 v4, 1.0, v4
	v_add_f32_e32 v5, 1.0, v5
	s_mov_b64 s[14:15], 0xb0000
	v_rcp_f32_e32 v14, v14
	v_rcp_f32_e32 v15, v15
	v_rcp_f32_e32 v8, v8
	v_rcp_f32_e32 v9, v9
	v_rcp_f32_e32 v2, v2
	v_rcp_f32_e32 v3, v3
	v_rcp_f32_e32 v4, v4
	v_rcp_f32_e32 v5, v5
	v_lshl_add_u64 v[136:137], v[166:167], 0, s[14:15]
	s_mov_b32 s14, 0xb0000
	v_add_co_u32_e32 v6, vcc, s14, v166
	v_cvt_pk_f16_f32 v11, v16, v17
	v_cvt_pk_f16_f32 v12, v18, v13
	v_cvt_pk_f16_f32 v13, v19, v20
	v_addc_co_u32_e32 v7, vcc, 0, v167, vcc
	s_waitcnt lgkmcnt(6)
	v_subrev_u32_e32 v236, s82, v236
	global_store_dwordx4 v236, v[232:235], s[82:83] sc1
	ds_bpermute_b32 v244, v250, v10
	ds_bpermute_b32 v245, v250, v11
	ds_bpermute_b32 v246, v250, v12
	ds_bpermute_b32 v247, v250, v13
	ds_bpermute_b32 v248, v250, v6
	v_fma_f32 v6, v153, v14, v128
	v_fma_f32 v7, v168, v15, v129
	v_fma_f32 v8, v121, v8, v130
	v_fmac_f32_e32 v131, v122, v9
	v_fma_f32 v2, v123, v2, v124
	v_fma_f32 v3, v120, v3, v125
	v_fma_f32 v4, v118, v4, v126
	v_fmac_f32_e32 v127, v119, v5
	v_log_f32_e32 v6, v6
	v_log_f32_e32 v7, v7
	v_log_f32_e32 v8, v8
	v_log_f32_e32 v9, v131
	v_log_f32_e32 v2, v2
	v_log_f32_e32 v3, v3
	v_log_f32_e32 v4, v4
	v_log_f32_e32 v5, v127
	v_cvt_pk_f16_f32 v196, v181, v182
	v_cvt_pk_f16_f32 v132, v6, v7
	v_cvt_pk_f16_f32 v133, v8, v9
	v_cvt_pk_f16_f32 v134, v2, v3
	v_cvt_pk_f16_f32 v135, v4, v5
	s_waitcnt lgkmcnt(5)
	v_subrev_u32_e32 v242, s82, v242
	global_store_dwordx4 v242, v[238:241], s[82:83] offset:64 sc1
	ds_bpermute_b32 v232, v250, v194
	ds_bpermute_b32 v233, v250, v195
	ds_bpermute_b32 v234, v250, v196
	ds_bpermute_b32 v235, v250, v197
	ds_bpermute_b32 v236, v250, v166
	s_andn2_b64 vcc, exec, s[38:39]
	s_mov_b64 s[28:29], -1
	s_waitcnt lgkmcnt(5)
	v_subrev_u32_e32 v248, s82, v248
	global_store_dwordx4 v248, v[244:247], s[82:83] sc1
	ds_bpermute_b32 v238, v250, v132
	ds_bpermute_b32 v239, v250, v133
	ds_bpermute_b32 v240, v250, v134
	ds_bpermute_b32 v241, v250, v135
	ds_bpermute_b32 v242, v250, v136
	s_waitcnt lgkmcnt(5)
	v_subrev_u32_e32 v236, s82, v236
	global_store_dwordx4 v236, v[232:235], s[82:83] offset:64 sc1
	s_waitcnt lgkmcnt(0)
	v_subrev_u32_e32 v242, s82, v242
	global_store_dwordx4 v242, v[238:241], s[82:83] offset:64 sc1
	s_cbranch_vccnz .LBB0_495
